# gMLP units in the non-scan half of the scan phase: all global loads of a LayerNorm row set and of a group issued up front behind counted vmcnt waits instead of one round trip each; MFMA section with t
# speedup vs baseline: 1.0194x; 1.0194x over previous
; __device__ __forceinline__ void unpk8(const u32x4 w, f32x4& a, f32x4& b) { a = (f32x4){bflo(w.x), bfhi(w.x), bflo(w.y), bfhi(w.y)}; b = (f32x4){bflo(w.z), bfhi(w.z), bflo(w.w), bfhi(w.w)}; }
; __device__ __forceinline__ void gmlp_unit(Frame& F, const Args& a, int layer, int unit) {
;     ...
;     for (int r = 0; r < 16; ++r) { const int tok = wave * 16 + r; const bf16* rowp = GUV + (t0 + tok) * 2048 + 1024;
;         f32x4 x0, x1, x2, x3; unpk8(*(const v4u*)(rowp + lane * 8), x0, x1); unpk8(*(const v4u*)(rowp + 512 + lane * 8), x2, x3);
;         const f32x4 sv = (x0 + x1) + (x2 + x3), qv = (x0 * x0 + x1 * x1) + (x2 * x2 + x3 * x3);
;         const float s = wave_sum((sv.x + sv.y) + (sv.z + sv.w)), q = wave_sum((qv.x + qv.y) + (qv.z + qv.w));
;         const float mean = s * (1.f / 1024.f), var = fmaxf(q * (1.f / 1024.f) - mean * mean, 0.f);
;         if (lane == 0) { st[tok * 2] = mean; st[tok * 2 + 1] = 1.f / sqrtf(var + 1e-5f); } }
.LBB0_828:
	s_ashr_i32 s21, s20, 31
	s_lshl_b64 s[36:37], s[20:21], 19
	v_readlane_b32 s21, v254, 19
	v_mbcnt_lo_u32_b32 v6, -1, 0
	v_mbcnt_hi_u32_b32 v6, -1, v6
	s_add_u32 s21, s6, s21
	v_readlane_b32 s22, v254, 20
	s_addc_u32 s23, s7, s22
	v_lshlrev_b32_e32 v2, 3, v6
	s_add_u32 s22, s21, s36
	v_ashrrev_i32_e32 v3, 31, v2
	s_addc_u32 s23, s23, s37
	s_mov_b32 s3, 0
	v_cmp_eq_u32_e64 s[42:43], 0, v6
	v_lshl_add_u64 v[4:5], v[2:3], 1, s[22:23]
	global_load_dwordx4 v[32:35], v[4:5], off
	global_load_dwordx4 v[36:39], v[4:5], off offset:1024
	v_lshl_add_u64 v[4:5], v[4:5], 0, s[78:79]
	global_load_dwordx4 v[40:43], v[4:5], off
	global_load_dwordx4 v[44:47], v[4:5], off offset:1024
	v_lshl_add_u64 v[4:5], v[4:5], 0, s[78:79]
	global_load_dwordx4 v[48:51], v[4:5], off
	global_load_dwordx4 v[52:55], v[4:5], off offset:1024
	v_lshl_add_u64 v[4:5], v[4:5], 0, s[78:79]
	global_load_dwordx4 v[56:59], v[4:5], off
	global_load_dwordx4 v[60:63], v[4:5], off offset:1024
	v_lshl_add_u64 v[4:5], v[4:5], 0, s[78:79]
	global_load_dwordx4 v[64:67], v[4:5], off
	global_load_dwordx4 v[68:71], v[4:5], off offset:1024
	v_lshl_add_u64 v[4:5], v[4:5], 0, s[78:79]
	global_load_dwordx4 v[72:75], v[4:5], off
	global_load_dwordx4 v[76:79], v[4:5], off offset:1024
	v_lshl_add_u64 v[4:5], v[4:5], 0, s[78:79]
	global_load_dwordx4 v[80:83], v[4:5], off
	global_load_dwordx4 v[84:87], v[4:5], off offset:1024
	v_lshl_add_u64 v[4:5], v[4:5], 0, s[78:79]
	global_load_dwordx4 v[88:91], v[4:5], off
	global_load_dwordx4 v[92:95], v[4:5], off offset:1024
	v_lshl_add_u64 v[4:5], v[4:5], 0, s[78:79]
	global_load_dwordx4 v[100:103], v[4:5], off
	global_load_dwordx4 v[104:107], v[4:5], off offset:1024
	v_lshl_add_u64 v[4:5], v[4:5], 0, s[78:79]
	global_load_dwordx4 v[108:111], v[4:5], off
	global_load_dwordx4 v[112:115], v[4:5], off offset:1024
	v_lshl_add_u64 v[4:5], v[4:5], 0, s[78:79]
	global_load_dwordx4 v[116:119], v[4:5], off
	global_load_dwordx4 v[120:123], v[4:5], off offset:1024
	v_lshl_add_u64 v[4:5], v[4:5], 0, s[78:79]
	global_load_dwordx4 v[124:127], v[4:5], off
	global_load_dwordx4 v[128:131], v[4:5], off offset:1024
	v_lshl_add_u64 v[4:5], v[4:5], 0, s[78:79]
	global_load_dwordx4 v[132:135], v[4:5], off
	global_load_dwordx4 v[136:139], v[4:5], off offset:1024
	v_lshl_add_u64 v[4:5], v[4:5], 0, s[78:79]
	global_load_dwordx4 v[140:143], v[4:5], off
	global_load_dwordx4 v[144:147], v[4:5], off offset:1024
	v_lshl_add_u64 v[4:5], v[4:5], 0, s[78:79]
	global_load_dwordx4 v[148:151], v[4:5], off
	global_load_dwordx4 v[152:155], v[4:5], off offset:1024
	v_lshl_add_u64 v[4:5], v[4:5], 0, s[78:79]
	global_load_dwordx4 v[156:159], v[4:5], off
	global_load_dwordx4 v[160:163], v[4:5], off offset:1024
	v_lshl_add_u64 v[4:5], v[4:5], 0, s[78:79]
	s_waitcnt vmcnt(30)
	v_lshlrev_b32_e32 v16, 16, v32
	v_and_b32_e32 v17, 0xffff0000, v32
	v_lshlrev_b32_e32 v8, 16, v33
	v_and_b32_e32 v9, 0xffff0000, v33
	v_lshlrev_b32_e32 v18, 16, v34
	v_and_b32_e32 v19, 0xffff0000, v34
	v_lshlrev_b32_e32 v10, 16, v35
	v_and_b32_e32 v11, 0xffff0000, v35
	v_lshlrev_b32_e32 v20, 16, v36
	v_and_b32_e32 v21, 0xffff0000, v36
	v_lshlrev_b32_e32 v12, 16, v37
	v_and_b32_e32 v13, 0xffff0000, v37
	v_lshlrev_b32_e32 v22, 16, v38
	v_and_b32_e32 v23, 0xffff0000, v38
	v_lshlrev_b32_e32 v14, 16, v39
	v_and_b32_e32 v15, 0xffff0000, v39
	v_pk_add_f32 v[24:25], v[16:17], v[18:19]
	v_pk_add_f32 v[26:27], v[8:9], v[10:11]
	v_pk_add_f32 v[28:29], v[20:21], v[22:23]
	v_pk_add_f32 v[30:31], v[12:13], v[14:15]
	v_pk_mul_f32 v[10:11], v[10:11], v[10:11]
	v_pk_mul_f32 v[18:19], v[18:19], v[18:19]
	v_pk_mul_f32 v[14:15], v[14:15], v[14:15]
	v_pk_mul_f32 v[22:23], v[22:23], v[22:23]
	v_pk_add_f32 v[26:27], v[26:27], v[30:31]
	v_pk_add_f32 v[24:25], v[24:25], v[28:29]
	v_pk_fma_f32 v[16:17], v[16:17], v[16:17], v[18:19]
	v_pk_fma_f32 v[8:9], v[8:9], v[8:9], v[10:11]
	v_pk_fma_f32 v[10:11], v[20:21], v[20:21], v[22:23]
	v_pk_fma_f32 v[12:13], v[12:13], v[12:13], v[14:15]
	v_pk_add_f32 v[10:11], v[16:17], v[10:11]
	v_pk_add_f32 v[8:9], v[8:9], v[12:13]
	v_add_f32_e32 v1, v24, v25
	v_add_f32_e32 v3, v26, v27
	v_add_f32_e32 v1, v1, v3
	v_add_f32_e32 v3, v10, v11
	v_add_f32_e32 v7, v8, v9
	v_add_f32_e32 v3, v3, v7
	v_add_f32_dpp v1, v1, v1 quad_perm:[1,0,3,2] row_mask:0xf bank_mask:0xf bound_ctrl:1
	s_nop 0
	v_add_f32_dpp v3, v3, v3 quad_perm:[1,0,3,2] row_mask:0xf bank_mask:0xf bound_ctrl:1
	v_add_f32_dpp v1, v1, v1 quad_perm:[2,3,0,1] row_mask:0xf bank_mask:0xf bound_ctrl:1
	s_nop 0
	v_add_f32_dpp v3, v3, v3 quad_perm:[2,3,0,1] row_mask:0xf bank_mask:0xf bound_ctrl:1
	v_add_f32_dpp v1, v1, v1 row_half_mirror row_mask:0xf bank_mask:0xf bound_ctrl:1
	s_nop 0
	v_add_f32_dpp v3, v3, v3 row_half_mirror row_mask:0xf bank_mask:0xf bound_ctrl:1
	v_add_f32_dpp v1, v1, v1 row_mirror row_mask:0xf bank_mask:0xf bound_ctrl:1
	v_mov_b32_e32 v7, v1
	v_add_f32_dpp v8, v3, v3 row_mirror row_mask:0xf bank_mask:0xf bound_ctrl:1
	v_mov_b32_e32 v9, v8
	v_permlane16_swap_b32_e32 v1, v7
	s_nop 0
	v_permlane16_swap_b32_e32 v8, v9
	v_add_f32_e32 v1, v1, v7
	v_add_f32_e32 v7, v8, v9
	v_mov_b32_e32 v3, v1
	v_mov_b32_e32 v8, v7
	s_nop 0
	v_permlane32_swap_b32_e32 v1, v3
	v_permlane32_swap_b32_e32 v7, v8
	s_and_saveexec_b64 s[22:23], s[42:43]
	s_cbranch_execz .Lgm_u1_st0
	v_add_f32_e32 v1, v1, v3
	v_add_f32_e32 v7, v7, v8
	v_mul_f32_e32 v8, 0x3a800000, v1
	v_mul_f32_e32 v1, v8, v8
	v_fma_f32 v1, v7, s13, -v1
	v_max_f32_e32 v1, 0, v1
	v_add_f32_e32 v1, 0x3727c5ac, v1
	v_mul_f32_e32 v3, 0x4f800000, v1
	v_cmp_gt_f32_e32 vcc, s69, v1
	s_add_i32 s21, s11, s3
	s_nop 0
	v_cndmask_b32_e32 v1, v1, v3, vcc
	v_sqrt_f32_e32 v3, v1
	s_nop 0
	v_add_u32_e32 v7, -1, v3
	v_fma_f32 v9, -v7, v3, v1
	v_cmp_ge_f32_e64 s[44:45], 0, v9
	v_add_u32_e32 v9, 1, v3
	s_nop 0
	v_cndmask_b32_e64 v7, v3, v7, s[44:45]
	v_fma_f32 v3, -v9, v3, v1
	v_cmp_lt_f32_e64 s[44:45], 0, v3
	s_nop 1
	v_cndmask_b32_e64 v3, v7, v9, s[44:45]
	v_mul_f32_e32 v7, 0x37800000, v3
	v_cndmask_b32_e32 v3, v3, v7, vcc
	v_cmp_class_f32_e32 vcc, v1, v242
	s_nop 1
	v_cndmask_b32_e32 v1, v3, v1, vcc
	v_div_scale_f32 v3, s[38:39], v1, v1, 1.0
	v_rcp_f32_e32 v7, v3
	s_nop 0
	v_fma_f32 v9, -v3, v7, 1.0
	v_fmac_f32_e32 v7, v9, v7
	v_div_scale_f32 v9, vcc, 1.0, v1, 1.0
	v_mul_f32_e32 v10, v9, v7
	v_fma_f32 v11, -v3, v10, v9
	v_fmac_f32_e32 v10, v11, v7
	v_fma_f32 v3, -v3, v10, v9
	v_div_fmas_f32 v3, v3, v7, v10
	v_div_fixup_f32 v9, v3, v1, 1.0
	v_mov_b32_e32 v1, s21
	ds_write_b64 v1, v[8:9]
; __device__ __forceinline__ void unpk8(const u32x4 w, f32x4& a, f32x4& b) { a = (f32x4){bflo(w.x), bfhi(w.x), bflo(w.y), bfhi(w.y)}; b = (f32x4){bflo(w.z), bfhi(w.z), bflo(w.w), bfhi(w.w)}; }
; __device__ __forceinline__ void gmlp_unit(Frame& F, const Args& a, int layer, int unit) {
;     ...
;     for (int r = 0; r < 16; ++r) { const int tok = wave * 16 + r; const bf16* rowp = GUV + (t0 + tok) * 2048 + 1024;
;         f32x4 x0, x1, x2, x3; unpk8(*(const v4u*)(rowp + lane * 8), x0, x1); unpk8(*(const v4u*)(rowp + 512 + lane * 8), x2, x3);
;         const f32x4 sv = (x0 + x1) + (x2 + x3), qv = (x0 * x0 + x1 * x1) + (x2 * x2 + x3 * x3);
;         const float s = wave_sum((sv.x + sv.y) + (sv.z + sv.w)), q = wave_sum((qv.x + qv.y) + (qv.z + qv.w));
;         const float mean = s * (1.f / 1024.f), var = fmaxf(q * (1.f / 1024.f) - mean * mean, 0.f);
;         if (lane == 0) { st[tok * 2] = mean; st[tok * 2 + 1] = 1.f / sqrtf(var + 1e-5f); } }
.Lgm_u1_st0:
	s_or_b64 exec, exec, s[22:23]
	s_add_i32 s3, s3, 8
	s_waitcnt vmcnt(28)
	v_lshlrev_b32_e32 v16, 16, v40
	v_and_b32_e32 v17, 0xffff0000, v40
	v_lshlrev_b32_e32 v8, 16, v41
	v_and_b32_e32 v9, 0xffff0000, v41
	v_lshlrev_b32_e32 v18, 16, v42
	v_and_b32_e32 v19, 0xffff0000, v42
	v_lshlrev_b32_e32 v10, 16, v43
	v_and_b32_e32 v11, 0xffff0000, v43
	v_lshlrev_b32_e32 v20, 16, v44
	v_and_b32_e32 v21, 0xffff0000, v44
	v_lshlrev_b32_e32 v12, 16, v45
	v_and_b32_e32 v13, 0xffff0000, v45
	v_lshlrev_b32_e32 v22, 16, v46
	v_and_b32_e32 v23, 0xffff0000, v46
	v_lshlrev_b32_e32 v14, 16, v47
	v_and_b32_e32 v15, 0xffff0000, v47
	v_pk_add_f32 v[24:25], v[16:17], v[18:19]
	v_pk_add_f32 v[26:27], v[8:9], v[10:11]
	v_pk_add_f32 v[28:29], v[20:21], v[22:23]
	v_pk_add_f32 v[30:31], v[12:13], v[14:15]
	v_pk_mul_f32 v[10:11], v[10:11], v[10:11]
	v_pk_mul_f32 v[18:19], v[18:19], v[18:19]
	v_pk_mul_f32 v[14:15], v[14:15], v[14:15]
	v_pk_mul_f32 v[22:23], v[22:23], v[22:23]
	v_pk_add_f32 v[26:27], v[26:27], v[30:31]
	v_pk_add_f32 v[24:25], v[24:25], v[28:29]
	v_pk_fma_f32 v[16:17], v[16:17], v[16:17], v[18:19]
	v_pk_fma_f32 v[8:9], v[8:9], v[8:9], v[10:11]
	v_pk_fma_f32 v[10:11], v[20:21], v[20:21], v[22:23]
	v_pk_fma_f32 v[12:13], v[12:13], v[12:13], v[14:15]
	v_pk_add_f32 v[10:11], v[16:17], v[10:11]
	v_pk_add_f32 v[8:9], v[8:9], v[12:13]
	v_add_f32_e32 v1, v24, v25
	v_add_f32_e32 v3, v26, v27
	v_add_f32_e32 v1, v1, v3
	v_add_f32_e32 v3, v10, v11
	v_add_f32_e32 v7, v8, v9
	v_add_f32_e32 v3, v3, v7
	v_add_f32_dpp v1, v1, v1 quad_perm:[1,0,3,2] row_mask:0xf bank_mask:0xf bound_ctrl:1
	s_nop 0
	v_add_f32_dpp v3, v3, v3 quad_perm:[1,0,3,2] row_mask:0xf bank_mask:0xf bound_ctrl:1
	v_add_f32_dpp v1, v1, v1 quad_perm:[2,3,0,1] row_mask:0xf bank_mask:0xf bound_ctrl:1
	s_nop 0
	v_add_f32_dpp v3, v3, v3 quad_perm:[2,3,0,1] row_mask:0xf bank_mask:0xf bound_ctrl:1
	v_add_f32_dpp v1, v1, v1 row_half_mirror row_mask:0xf bank_mask:0xf bound_ctrl:1
	s_nop 0
	v_add_f32_dpp v3, v3, v3 row_half_mirror row_mask:0xf bank_mask:0xf bound_ctrl:1
	v_add_f32_dpp v1, v1, v1 row_mirror row_mask:0xf bank_mask:0xf bound_ctrl:1
	v_mov_b32_e32 v7, v1
	v_add_f32_dpp v8, v3, v3 row_mirror row_mask:0xf bank_mask:0xf bound_ctrl:1
	v_mov_b32_e32 v9, v8
	v_permlane16_swap_b32_e32 v1, v7
	s_nop 0
	v_permlane16_swap_b32_e32 v8, v9
	v_add_f32_e32 v1, v1, v7
	v_add_f32_e32 v7, v8, v9
	v_mov_b32_e32 v3, v1
	v_mov_b32_e32 v8, v7
	s_nop 0
	v_permlane32_swap_b32_e32 v1, v3
	v_permlane32_swap_b32_e32 v7, v8
	s_and_saveexec_b64 s[22:23], s[42:43]
	s_cbranch_execz .Lgm_u1_st1
	v_add_f32_e32 v1, v1, v3
	v_add_f32_e32 v7, v7, v8
	v_mul_f32_e32 v8, 0x3a800000, v1
	v_mul_f32_e32 v1, v8, v8
	v_fma_f32 v1, v7, s13, -v1
	v_max_f32_e32 v1, 0, v1
	v_add_f32_e32 v1, 0x3727c5ac, v1
	v_mul_f32_e32 v3, 0x4f800000, v1
	v_cmp_gt_f32_e32 vcc, s69, v1
	s_add_i32 s21, s11, s3
	s_nop 0
	v_cndmask_b32_e32 v1, v1, v3, vcc
	v_sqrt_f32_e32 v3, v1
	s_nop 0
	v_add_u32_e32 v7, -1, v3
	v_fma_f32 v9, -v7, v3, v1
	v_cmp_ge_f32_e64 s[44:45], 0, v9
	v_add_u32_e32 v9, 1, v3
	s_nop 0
	v_cndmask_b32_e64 v7, v3, v7, s[44:45]
	v_fma_f32 v3, -v9, v3, v1
	v_cmp_lt_f32_e64 s[44:45], 0, v3
	s_nop 1
	v_cndmask_b32_e64 v3, v7, v9, s[44:45]
	v_mul_f32_e32 v7, 0x37800000, v3
	v_cndmask_b32_e32 v3, v3, v7, vcc
	v_cmp_class_f32_e32 vcc, v1, v242
	s_nop 1
	v_cndmask_b32_e32 v1, v3, v1, vcc
	v_div_scale_f32 v3, s[38:39], v1, v1, 1.0
	v_rcp_f32_e32 v7, v3
	s_nop 0
	v_fma_f32 v9, -v3, v7, 1.0
	v_fmac_f32_e32 v7, v9, v7
	v_div_scale_f32 v9, vcc, 1.0, v1, 1.0
	v_mul_f32_e32 v10, v9, v7
	v_fma_f32 v11, -v3, v10, v9
	v_fmac_f32_e32 v10, v11, v7
	v_fma_f32 v3, -v3, v10, v9
	v_div_fmas_f32 v3, v3, v7, v10
	v_div_fixup_f32 v9, v3, v1, 1.0
	v_mov_b32_e32 v1, s21
	ds_write_b64 v1, v[8:9]
.Lgm_u1_st1:
	s_or_b64 exec, exec, s[22:23]
	s_add_i32 s3, s3, 8
	s_waitcnt vmcnt(26)
	v_lshlrev_b32_e32 v16, 16, v48
	v_and_b32_e32 v17, 0xffff0000, v48
	v_lshlrev_b32_e32 v8, 16, v49
	v_and_b32_e32 v9, 0xffff0000, v49
	v_lshlrev_b32_e32 v18, 16, v50
	v_and_b32_e32 v19, 0xffff0000, v50
	v_lshlrev_b32_e32 v10, 16, v51
	v_and_b32_e32 v11, 0xffff0000, v51
	v_lshlrev_b32_e32 v20, 16, v52
	v_and_b32_e32 v21, 0xffff0000, v52
	v_lshlrev_b32_e32 v12, 16, v53
	v_and_b32_e32 v13, 0xffff0000, v53
	v_lshlrev_b32_e32 v22, 16, v54
	v_and_b32_e32 v23, 0xffff0000, v54
	v_lshlrev_b32_e32 v14, 16, v55
	v_and_b32_e32 v15, 0xffff0000, v55
	v_pk_add_f32 v[24:25], v[16:17], v[18:19]
	v_pk_add_f32 v[26:27], v[8:9], v[10:11]
	v_pk_add_f32 v[28:29], v[20:21], v[22:23]
	v_pk_add_f32 v[30:31], v[12:13], v[14:15]
	v_pk_mul_f32 v[10:11], v[10:11], v[10:11]
	v_pk_mul_f32 v[18:19], v[18:19], v[18:19]
	v_pk_mul_f32 v[14:15], v[14:15], v[14:15]
	v_pk_mul_f32 v[22:23], v[22:23], v[22:23]
	v_pk_add_f32 v[26:27], v[26:27], v[30:31]
	v_pk_add_f32 v[24:25], v[24:25], v[28:29]
	v_pk_fma_f32 v[16:17], v[16:17], v[16:17], v[18:19]
	v_pk_fma_f32 v[8:9], v[8:9], v[8:9], v[10:11]
	v_pk_fma_f32 v[10:11], v[20:21], v[20:21], v[22:23]
	v_pk_fma_f32 v[12:13], v[12:13], v[12:13], v[14:15]
	v_pk_add_f32 v[10:11], v[16:17], v[10:11]
	v_pk_add_f32 v[8:9], v[8:9], v[12:13]
	v_add_f32_e32 v1, v24, v25
	v_add_f32_e32 v3, v26, v27
	v_add_f32_e32 v1, v1, v3
	v_add_f32_e32 v3, v10, v11
	v_add_f32_e32 v7, v8, v9
	v_add_f32_e32 v3, v3, v7
	v_add_f32_dpp v1, v1, v1 quad_perm:[1,0,3,2] row_mask:0xf bank_mask:0xf bound_ctrl:1
	s_nop 0
	v_add_f32_dpp v3, v3, v3 quad_perm:[1,0,3,2] row_mask:0xf bank_mask:0xf bound_ctrl:1
	v_add_f32_dpp v1, v1, v1 quad_perm:[2,3,0,1] row_mask:0xf bank_mask:0xf bound_ctrl:1
	s_nop 0
	v_add_f32_dpp v3, v3, v3 quad_perm:[2,3,0,1] row_mask:0xf bank_mask:0xf bound_ctrl:1
	v_add_f32_dpp v1, v1, v1 row_half_mirror row_mask:0xf bank_mask:0xf bound_ctrl:1
	s_nop 0
	v_add_f32_dpp v3, v3, v3 row_half_mirror row_mask:0xf bank_mask:0xf bound_ctrl:1
	v_add_f32_dpp v1, v1, v1 row_mirror row_mask:0xf bank_mask:0xf bound_ctrl:1
	v_mov_b32_e32 v7, v1
	v_add_f32_dpp v8, v3, v3 row_mirror row_mask:0xf bank_mask:0xf bound_ctrl:1
	v_mov_b32_e32 v9, v8
	v_permlane16_swap_b32_e32 v1, v7
	s_nop 0
	v_permlane16_swap_b32_e32 v8, v9
	v_add_f32_e32 v1, v1, v7
	v_add_f32_e32 v7, v8, v9
	v_mov_b32_e32 v3, v1
	v_mov_b32_e32 v8, v7
	s_nop 0
	v_permlane32_swap_b32_e32 v1, v3
	v_permlane32_swap_b32_e32 v7, v8
	s_and_saveexec_b64 s[22:23], s[42:43]
	s_cbranch_execz .Lgm_u1_st2
; __device__ __forceinline__ void unpk8(const u32x4 w, f32x4& a, f32x4& b) { a = (f32x4){bflo(w.x), bfhi(w.x), bflo(w.y), bfhi(w.y)}; b = (f32x4){bflo(w.z), bfhi(w.z), bflo(w.w), bfhi(w.w)}; }
; __device__ __forceinline__ void gmlp_unit(Frame& F, const Args& a, int layer, int unit) {
;     ...
;     for (int r = 0; r < 16; ++r) { const int tok = wave * 16 + r; const bf16* rowp = GUV + (t0 + tok) * 2048 + 1024;
;         f32x4 x0, x1, x2, x3; unpk8(*(const v4u*)(rowp + lane * 8), x0, x1); unpk8(*(const v4u*)(rowp + 512 + lane * 8), x2, x3);
;         const f32x4 sv = (x0 + x1) + (x2 + x3), qv = (x0 * x0 + x1 * x1) + (x2 * x2 + x3 * x3);
;         const float s = wave_sum((sv.x + sv.y) + (sv.z + sv.w)), q = wave_sum((qv.x + qv.y) + (qv.z + qv.w));
;         const float mean = s * (1.f / 1024.f), var = fmaxf(q * (1.f / 1024.f) - mean * mean, 0.f);
;         if (lane == 0) { st[tok * 2] = mean; st[tok * 2 + 1] = 1.f / sqrtf(var + 1e-5f); } }
	v_add_f32_e32 v1, v1, v3
	v_add_f32_e32 v7, v7, v8
	v_mul_f32_e32 v8, 0x3a800000, v1
	v_mul_f32_e32 v1, v8, v8
	v_fma_f32 v1, v7, s13, -v1
	v_max_f32_e32 v1, 0, v1
	v_add_f32_e32 v1, 0x3727c5ac, v1
	v_mul_f32_e32 v3, 0x4f800000, v1
	v_cmp_gt_f32_e32 vcc, s69, v1
	s_add_i32 s21, s11, s3
	s_nop 0
	v_cndmask_b32_e32 v1, v1, v3, vcc
	v_sqrt_f32_e32 v3, v1
	s_nop 0
	v_add_u32_e32 v7, -1, v3
	v_fma_f32 v9, -v7, v3, v1
	v_cmp_ge_f32_e64 s[44:45], 0, v9
	v_add_u32_e32 v9, 1, v3
	s_nop 0
	v_cndmask_b32_e64 v7, v3, v7, s[44:45]
	v_fma_f32 v3, -v9, v3, v1
	v_cmp_lt_f32_e64 s[44:45], 0, v3
	s_nop 1
	v_cndmask_b32_e64 v3, v7, v9, s[44:45]
	v_mul_f32_e32 v7, 0x37800000, v3
	v_cndmask_b32_e32 v3, v3, v7, vcc
	v_cmp_class_f32_e32 vcc, v1, v242
	s_nop 1
	v_cndmask_b32_e32 v1, v3, v1, vcc
	v_div_scale_f32 v3, s[38:39], v1, v1, 1.0
	v_rcp_f32_e32 v7, v3
	s_nop 0
	v_fma_f32 v9, -v3, v7, 1.0
	v_fmac_f32_e32 v7, v9, v7
	v_div_scale_f32 v9, vcc, 1.0, v1, 1.0
	v_mul_f32_e32 v10, v9, v7
	v_fma_f32 v11, -v3, v10, v9
	v_fmac_f32_e32 v10, v11, v7
	v_fma_f32 v3, -v3, v10, v9
	v_div_fmas_f32 v3, v3, v7, v10
	v_div_fixup_f32 v9, v3, v1, 1.0
	v_mov_b32_e32 v1, s21
	ds_write_b64 v1, v[8:9]
.Lgm_u1_st2:
	s_or_b64 exec, exec, s[22:23]
	s_add_i32 s3, s3, 8
	s_waitcnt vmcnt(24)
	v_lshlrev_b32_e32 v16, 16, v56
	v_and_b32_e32 v17, 0xffff0000, v56
	v_lshlrev_b32_e32 v8, 16, v57
	v_and_b32_e32 v9, 0xffff0000, v57
	v_lshlrev_b32_e32 v18, 16, v58
	v_and_b32_e32 v19, 0xffff0000, v58
	v_lshlrev_b32_e32 v10, 16, v59
	v_and_b32_e32 v11, 0xffff0000, v59
	v_lshlrev_b32_e32 v20, 16, v60
	v_and_b32_e32 v21, 0xffff0000, v60
	v_lshlrev_b32_e32 v12, 16, v61
	v_and_b32_e32 v13, 0xffff0000, v61
	v_lshlrev_b32_e32 v22, 16, v62
	v_and_b32_e32 v23, 0xffff0000, v62
	v_lshlrev_b32_e32 v14, 16, v63
	v_and_b32_e32 v15, 0xffff0000, v63
	v_pk_add_f32 v[24:25], v[16:17], v[18:19]
	v_pk_add_f32 v[26:27], v[8:9], v[10:11]
	v_pk_add_f32 v[28:29], v[20:21], v[22:23]
	v_pk_add_f32 v[30:31], v[12:13], v[14:15]
	v_pk_mul_f32 v[10:11], v[10:11], v[10:11]
	v_pk_mul_f32 v[18:19], v[18:19], v[18:19]
	v_pk_mul_f32 v[14:15], v[14:15], v[14:15]
	v_pk_mul_f32 v[22:23], v[22:23], v[22:23]
	v_pk_add_f32 v[26:27], v[26:27], v[30:31]
	v_pk_add_f32 v[24:25], v[24:25], v[28:29]
	v_pk_fma_f32 v[16:17], v[16:17], v[16:17], v[18:19]
	v_pk_fma_f32 v[8:9], v[8:9], v[8:9], v[10:11]
	v_pk_fma_f32 v[10:11], v[20:21], v[20:21], v[22:23]
	v_pk_fma_f32 v[12:13], v[12:13], v[12:13], v[14:15]
	v_pk_add_f32 v[10:11], v[16:17], v[10:11]
	v_pk_add_f32 v[8:9], v[8:9], v[12:13]
	v_add_f32_e32 v1, v24, v25
	v_add_f32_e32 v3, v26, v27
	v_add_f32_e32 v1, v1, v3
	v_add_f32_e32 v3, v10, v11
	v_add_f32_e32 v7, v8, v9
	v_add_f32_e32 v3, v3, v7
	v_add_f32_dpp v1, v1, v1 quad_perm:[1,0,3,2] row_mask:0xf bank_mask:0xf bound_ctrl:1
	s_nop 0
	v_add_f32_dpp v3, v3, v3 quad_perm:[1,0,3,2] row_mask:0xf bank_mask:0xf bound_ctrl:1
	v_add_f32_dpp v1, v1, v1 quad_perm:[2,3,0,1] row_mask:0xf bank_mask:0xf bound_ctrl:1
	s_nop 0
	v_add_f32_dpp v3, v3, v3 quad_perm:[2,3,0,1] row_mask:0xf bank_mask:0xf bound_ctrl:1
	v_add_f32_dpp v1, v1, v1 row_half_mirror row_mask:0xf bank_mask:0xf bound_ctrl:1
	s_nop 0
	v_add_f32_dpp v3, v3, v3 row_half_mirror row_mask:0xf bank_mask:0xf bound_ctrl:1
	v_add_f32_dpp v1, v1, v1 row_mirror row_mask:0xf bank_mask:0xf bound_ctrl:1
	v_mov_b32_e32 v7, v1
	v_add_f32_dpp v8, v3, v3 row_mirror row_mask:0xf bank_mask:0xf bound_ctrl:1
	v_mov_b32_e32 v9, v8
	v_permlane16_swap_b32_e32 v1, v7
	s_nop 0
	v_permlane16_swap_b32_e32 v8, v9
	v_add_f32_e32 v1, v1, v7
	v_add_f32_e32 v7, v8, v9
	v_mov_b32_e32 v3, v1
	v_mov_b32_e32 v8, v7
	s_nop 0
	v_permlane32_swap_b32_e32 v1, v3
	v_permlane32_swap_b32_e32 v7, v8
	s_and_saveexec_b64 s[22:23], s[42:43]
	s_cbranch_execz .Lgm_u1_st3
	v_add_f32_e32 v1, v1, v3
	v_add_f32_e32 v7, v7, v8
	v_mul_f32_e32 v8, 0x3a800000, v1
	v_mul_f32_e32 v1, v8, v8
	v_fma_f32 v1, v7, s13, -v1
	v_max_f32_e32 v1, 0, v1
	v_add_f32_e32 v1, 0x3727c5ac, v1
	v_mul_f32_e32 v3, 0x4f800000, v1
	v_cmp_gt_f32_e32 vcc, s69, v1
	s_add_i32 s21, s11, s3
	s_nop 0
	v_cndmask_b32_e32 v1, v1, v3, vcc
	v_sqrt_f32_e32 v3, v1
	s_nop 0
	v_add_u32_e32 v7, -1, v3
	v_fma_f32 v9, -v7, v3, v1
	v_cmp_ge_f32_e64 s[44:45], 0, v9
	v_add_u32_e32 v9, 1, v3
	s_nop 0
	v_cndmask_b32_e64 v7, v3, v7, s[44:45]
	v_fma_f32 v3, -v9, v3, v1
	v_cmp_lt_f32_e64 s[44:45], 0, v3
	s_nop 1
	v_cndmask_b32_e64 v3, v7, v9, s[44:45]
	v_mul_f32_e32 v7, 0x37800000, v3
	v_cndmask_b32_e32 v3, v3, v7, vcc
	v_cmp_class_f32_e32 vcc, v1, v242
	s_nop 1
	v_cndmask_b32_e32 v1, v3, v1, vcc
	v_div_scale_f32 v3, s[38:39], v1, v1, 1.0
	v_rcp_f32_e32 v7, v3
	s_nop 0
	v_fma_f32 v9, -v3, v7, 1.0
	v_fmac_f32_e32 v7, v9, v7
	v_div_scale_f32 v9, vcc, 1.0, v1, 1.0
	v_mul_f32_e32 v10, v9, v7
	v_fma_f32 v11, -v3, v10, v9
	v_fmac_f32_e32 v10, v11, v7
	v_fma_f32 v3, -v3, v10, v9
	v_div_fmas_f32 v3, v3, v7, v10
	v_div_fixup_f32 v9, v3, v1, 1.0
	v_mov_b32_e32 v1, s21
	ds_write_b64 v1, v[8:9]
; __device__ __forceinline__ void unpk8(const u32x4 w, f32x4& a, f32x4& b) { a = (f32x4){bflo(w.x), bfhi(w.x), bflo(w.y), bfhi(w.y)}; b = (f32x4){bflo(w.z), bfhi(w.z), bflo(w.w), bfhi(w.w)}; }
; __device__ __forceinline__ void gmlp_unit(Frame& F, const Args& a, int layer, int unit) {
;     ...
;     for (int r = 0; r < 16; ++r) { const int tok = wave * 16 + r; const bf16* rowp = GUV + (t0 + tok) * 2048 + 1024;
;         f32x4 x0, x1, x2, x3; unpk8(*(const v4u*)(rowp + lane * 8), x0, x1); unpk8(*(const v4u*)(rowp + 512 + lane * 8), x2, x3);
;         const f32x4 sv = (x0 + x1) + (x2 + x3), qv = (x0 * x0 + x1 * x1) + (x2 * x2 + x3 * x3);
;         const float s = wave_sum((sv.x + sv.y) + (sv.z + sv.w)), q = wave_sum((qv.x + qv.y) + (qv.z + qv.w));
;         const float mean = s * (1.f / 1024.f), var = fmaxf(q * (1.f / 1024.f) - mean * mean, 0.f);
;         if (lane == 0) { st[tok * 2] = mean; st[tok * 2 + 1] = 1.f / sqrtf(var + 1e-5f); } }
.Lgm_u1_st3:
	s_or_b64 exec, exec, s[22:23]
	s_add_i32 s3, s3, 8
	s_waitcnt vmcnt(22)
	v_lshlrev_b32_e32 v16, 16, v64
	v_and_b32_e32 v17, 0xffff0000, v64
	v_lshlrev_b32_e32 v8, 16, v65
	v_and_b32_e32 v9, 0xffff0000, v65
	v_lshlrev_b32_e32 v18, 16, v66
	v_and_b32_e32 v19, 0xffff0000, v66
	v_lshlrev_b32_e32 v10, 16, v67
	v_and_b32_e32 v11, 0xffff0000, v67
	v_lshlrev_b32_e32 v20, 16, v68
	v_and_b32_e32 v21, 0xffff0000, v68
	v_lshlrev_b32_e32 v12, 16, v69
	v_and_b32_e32 v13, 0xffff0000, v69
	v_lshlrev_b32_e32 v22, 16, v70
	v_and_b32_e32 v23, 0xffff0000, v70
	v_lshlrev_b32_e32 v14, 16, v71
	v_and_b32_e32 v15, 0xffff0000, v71
	v_pk_add_f32 v[24:25], v[16:17], v[18:19]
	v_pk_add_f32 v[26:27], v[8:9], v[10:11]
	v_pk_add_f32 v[28:29], v[20:21], v[22:23]
	v_pk_add_f32 v[30:31], v[12:13], v[14:15]
	v_pk_mul_f32 v[10:11], v[10:11], v[10:11]
	v_pk_mul_f32 v[18:19], v[18:19], v[18:19]
	v_pk_mul_f32 v[14:15], v[14:15], v[14:15]
	v_pk_mul_f32 v[22:23], v[22:23], v[22:23]
	v_pk_add_f32 v[26:27], v[26:27], v[30:31]
	v_pk_add_f32 v[24:25], v[24:25], v[28:29]
	v_pk_fma_f32 v[16:17], v[16:17], v[16:17], v[18:19]
	v_pk_fma_f32 v[8:9], v[8:9], v[8:9], v[10:11]
	v_pk_fma_f32 v[10:11], v[20:21], v[20:21], v[22:23]
	v_pk_fma_f32 v[12:13], v[12:13], v[12:13], v[14:15]
	v_pk_add_f32 v[10:11], v[16:17], v[10:11]
	v_pk_add_f32 v[8:9], v[8:9], v[12:13]
	v_add_f32_e32 v1, v24, v25
	v_add_f32_e32 v3, v26, v27
	v_add_f32_e32 v1, v1, v3
	v_add_f32_e32 v3, v10, v11
	v_add_f32_e32 v7, v8, v9
	v_add_f32_e32 v3, v3, v7
	v_add_f32_dpp v1, v1, v1 quad_perm:[1,0,3,2] row_mask:0xf bank_mask:0xf bound_ctrl:1
	s_nop 0
	v_add_f32_dpp v3, v3, v3 quad_perm:[1,0,3,2] row_mask:0xf bank_mask:0xf bound_ctrl:1
	v_add_f32_dpp v1, v1, v1 quad_perm:[2,3,0,1] row_mask:0xf bank_mask:0xf bound_ctrl:1
	s_nop 0
	v_add_f32_dpp v3, v3, v3 quad_perm:[2,3,0,1] row_mask:0xf bank_mask:0xf bound_ctrl:1
	v_add_f32_dpp v1, v1, v1 row_half_mirror row_mask:0xf bank_mask:0xf bound_ctrl:1
	s_nop 0
	v_add_f32_dpp v3, v3, v3 row_half_mirror row_mask:0xf bank_mask:0xf bound_ctrl:1
	v_add_f32_dpp v1, v1, v1 row_mirror row_mask:0xf bank_mask:0xf bound_ctrl:1
	v_mov_b32_e32 v7, v1
	v_add_f32_dpp v8, v3, v3 row_mirror row_mask:0xf bank_mask:0xf bound_ctrl:1
	v_mov_b32_e32 v9, v8
	v_permlane16_swap_b32_e32 v1, v7
	s_nop 0
	v_permlane16_swap_b32_e32 v8, v9
	v_add_f32_e32 v1, v1, v7
	v_add_f32_e32 v7, v8, v9
	v_mov_b32_e32 v3, v1
	v_mov_b32_e32 v8, v7
	s_nop 0
	v_permlane32_swap_b32_e32 v1, v3
	v_permlane32_swap_b32_e32 v7, v8
	s_and_saveexec_b64 s[22:23], s[42:43]
	s_cbranch_execz .Lgm_u1_st4
	v_add_f32_e32 v1, v1, v3
	v_add_f32_e32 v7, v7, v8
	v_mul_f32_e32 v8, 0x3a800000, v1
	v_mul_f32_e32 v1, v8, v8
	v_fma_f32 v1, v7, s13, -v1
	v_max_f32_e32 v1, 0, v1
	v_add_f32_e32 v1, 0x3727c5ac, v1
	v_mul_f32_e32 v3, 0x4f800000, v1
	v_cmp_gt_f32_e32 vcc, s69, v1
	s_add_i32 s21, s11, s3
	s_nop 0
	v_cndmask_b32_e32 v1, v1, v3, vcc
	v_sqrt_f32_e32 v3, v1
	s_nop 0
	v_add_u32_e32 v7, -1, v3
	v_fma_f32 v9, -v7, v3, v1
	v_cmp_ge_f32_e64 s[44:45], 0, v9
	v_add_u32_e32 v9, 1, v3
	s_nop 0
	v_cndmask_b32_e64 v7, v3, v7, s[44:45]
	v_fma_f32 v3, -v9, v3, v1
	v_cmp_lt_f32_e64 s[44:45], 0, v3
	s_nop 1
	v_cndmask_b32_e64 v3, v7, v9, s[44:45]
	v_mul_f32_e32 v7, 0x37800000, v3
	v_cndmask_b32_e32 v3, v3, v7, vcc
	v_cmp_class_f32_e32 vcc, v1, v242
	s_nop 1
	v_cndmask_b32_e32 v1, v3, v1, vcc
	v_div_scale_f32 v3, s[38:39], v1, v1, 1.0
	v_rcp_f32_e32 v7, v3
	s_nop 0
	v_fma_f32 v9, -v3, v7, 1.0
	v_fmac_f32_e32 v7, v9, v7
	v_div_scale_f32 v9, vcc, 1.0, v1, 1.0
	v_mul_f32_e32 v10, v9, v7
	v_fma_f32 v11, -v3, v10, v9
	v_fmac_f32_e32 v10, v11, v7
	v_fma_f32 v3, -v3, v10, v9
	v_div_fmas_f32 v3, v3, v7, v10
	v_div_fixup_f32 v9, v3, v1, 1.0
	v_mov_b32_e32 v1, s21
	ds_write_b64 v1, v[8:9]
.Lgm_u1_st4:
	s_or_b64 exec, exec, s[22:23]
	s_add_i32 s3, s3, 8
	s_waitcnt vmcnt(20)
	v_lshlrev_b32_e32 v16, 16, v72
	v_and_b32_e32 v17, 0xffff0000, v72
	v_lshlrev_b32_e32 v8, 16, v73
	v_and_b32_e32 v9, 0xffff0000, v73
	v_lshlrev_b32_e32 v18, 16, v74
	v_and_b32_e32 v19, 0xffff0000, v74
	v_lshlrev_b32_e32 v10, 16, v75
	v_and_b32_e32 v11, 0xffff0000, v75
	v_lshlrev_b32_e32 v20, 16, v76
	v_and_b32_e32 v21, 0xffff0000, v76
	v_lshlrev_b32_e32 v12, 16, v77
	v_and_b32_e32 v13, 0xffff0000, v77
	v_lshlrev_b32_e32 v22, 16, v78
	v_and_b32_e32 v23, 0xffff0000, v78
	v_lshlrev_b32_e32 v14, 16, v79
	v_and_b32_e32 v15, 0xffff0000, v79
	v_pk_add_f32 v[24:25], v[16:17], v[18:19]
	v_pk_add_f32 v[26:27], v[8:9], v[10:11]
	v_pk_add_f32 v[28:29], v[20:21], v[22:23]
	v_pk_add_f32 v[30:31], v[12:13], v[14:15]
	v_pk_mul_f32 v[10:11], v[10:11], v[10:11]
	v_pk_mul_f32 v[18:19], v[18:19], v[18:19]
	v_pk_mul_f32 v[14:15], v[14:15], v[14:15]
	v_pk_mul_f32 v[22:23], v[22:23], v[22:23]
	v_pk_add_f32 v[26:27], v[26:27], v[30:31]
	v_pk_add_f32 v[24:25], v[24:25], v[28:29]
	v_pk_fma_f32 v[16:17], v[16:17], v[16:17], v[18:19]
	v_pk_fma_f32 v[8:9], v[8:9], v[8:9], v[10:11]
	v_pk_fma_f32 v[10:11], v[20:21], v[20:21], v[22:23]
	v_pk_fma_f32 v[12:13], v[12:13], v[12:13], v[14:15]
	v_pk_add_f32 v[10:11], v[16:17], v[10:11]
	v_pk_add_f32 v[8:9], v[8:9], v[12:13]
	v_add_f32_e32 v1, v24, v25
	v_add_f32_e32 v3, v26, v27
	v_add_f32_e32 v1, v1, v3
	v_add_f32_e32 v3, v10, v11
	v_add_f32_e32 v7, v8, v9
	v_add_f32_e32 v3, v3, v7
	v_add_f32_dpp v1, v1, v1 quad_perm:[1,0,3,2] row_mask:0xf bank_mask:0xf bound_ctrl:1
	s_nop 0
	v_add_f32_dpp v3, v3, v3 quad_perm:[1,0,3,2] row_mask:0xf bank_mask:0xf bound_ctrl:1
	v_add_f32_dpp v1, v1, v1 quad_perm:[2,3,0,1] row_mask:0xf bank_mask:0xf bound_ctrl:1
	s_nop 0
	v_add_f32_dpp v3, v3, v3 quad_perm:[2,3,0,1] row_mask:0xf bank_mask:0xf bound_ctrl:1
	v_add_f32_dpp v1, v1, v1 row_half_mirror row_mask:0xf bank_mask:0xf bound_ctrl:1
	s_nop 0
	v_add_f32_dpp v3, v3, v3 row_half_mirror row_mask:0xf bank_mask:0xf bound_ctrl:1
	v_add_f32_dpp v1, v1, v1 row_mirror row_mask:0xf bank_mask:0xf bound_ctrl:1
	v_mov_b32_e32 v7, v1
	v_add_f32_dpp v8, v3, v3 row_mirror row_mask:0xf bank_mask:0xf bound_ctrl:1
	v_mov_b32_e32 v9, v8
	v_permlane16_swap_b32_e32 v1, v7
	s_nop 0
	v_permlane16_swap_b32_e32 v8, v9
	v_add_f32_e32 v1, v1, v7
	v_add_f32_e32 v7, v8, v9
	v_mov_b32_e32 v3, v1
	v_mov_b32_e32 v8, v7
	s_nop 0
	v_permlane32_swap_b32_e32 v1, v3
	v_permlane32_swap_b32_e32 v7, v8
	s_and_saveexec_b64 s[22:23], s[42:43]
	s_cbranch_execz .Lgm_u1_st5
; __device__ __forceinline__ void unpk8(const u32x4 w, f32x4& a, f32x4& b) { a = (f32x4){bflo(w.x), bfhi(w.x), bflo(w.y), bfhi(w.y)}; b = (f32x4){bflo(w.z), bfhi(w.z), bflo(w.w), bfhi(w.w)}; }
; __device__ __forceinline__ void gmlp_unit(Frame& F, const Args& a, int layer, int unit) {
;     ...
;     for (int r = 0; r < 16; ++r) { const int tok = wave * 16 + r; const bf16* rowp = GUV + (t0 + tok) * 2048 + 1024;
;         f32x4 x0, x1, x2, x3; unpk8(*(const v4u*)(rowp + lane * 8), x0, x1); unpk8(*(const v4u*)(rowp + 512 + lane * 8), x2, x3);
;         const f32x4 sv = (x0 + x1) + (x2 + x3), qv = (x0 * x0 + x1 * x1) + (x2 * x2 + x3 * x3);
;         const float s = wave_sum((sv.x + sv.y) + (sv.z + sv.w)), q = wave_sum((qv.x + qv.y) + (qv.z + qv.w));
;         const float mean = s * (1.f / 1024.f), var = fmaxf(q * (1.f / 1024.f) - mean * mean, 0.f);
;         if (lane == 0) { st[tok * 2] = mean; st[tok * 2 + 1] = 1.f / sqrtf(var + 1e-5f); } }
	v_add_f32_e32 v1, v1, v3
	v_add_f32_e32 v7, v7, v8
	v_mul_f32_e32 v8, 0x3a800000, v1
	v_mul_f32_e32 v1, v8, v8
	v_fma_f32 v1, v7, s13, -v1
	v_max_f32_e32 v1, 0, v1
	v_add_f32_e32 v1, 0x3727c5ac, v1
	v_mul_f32_e32 v3, 0x4f800000, v1
	v_cmp_gt_f32_e32 vcc, s69, v1
	s_add_i32 s21, s11, s3
	s_nop 0
	v_cndmask_b32_e32 v1, v1, v3, vcc
	v_sqrt_f32_e32 v3, v1
	s_nop 0
	v_add_u32_e32 v7, -1, v3
	v_fma_f32 v9, -v7, v3, v1
	v_cmp_ge_f32_e64 s[44:45], 0, v9
	v_add_u32_e32 v9, 1, v3
	s_nop 0
	v_cndmask_b32_e64 v7, v3, v7, s[44:45]
	v_fma_f32 v3, -v9, v3, v1
	v_cmp_lt_f32_e64 s[44:45], 0, v3
	s_nop 1
	v_cndmask_b32_e64 v3, v7, v9, s[44:45]
	v_mul_f32_e32 v7, 0x37800000, v3
	v_cndmask_b32_e32 v3, v3, v7, vcc
	v_cmp_class_f32_e32 vcc, v1, v242
	s_nop 1
	v_cndmask_b32_e32 v1, v3, v1, vcc
	v_div_scale_f32 v3, s[38:39], v1, v1, 1.0
	v_rcp_f32_e32 v7, v3
	s_nop 0
	v_fma_f32 v9, -v3, v7, 1.0
	v_fmac_f32_e32 v7, v9, v7
	v_div_scale_f32 v9, vcc, 1.0, v1, 1.0
	v_mul_f32_e32 v10, v9, v7
	v_fma_f32 v11, -v3, v10, v9
	v_fmac_f32_e32 v10, v11, v7
	v_fma_f32 v3, -v3, v10, v9
	v_div_fmas_f32 v3, v3, v7, v10
	v_div_fixup_f32 v9, v3, v1, 1.0
	v_mov_b32_e32 v1, s21
	ds_write_b64 v1, v[8:9]
.Lgm_u1_st5:
	s_or_b64 exec, exec, s[22:23]
	s_add_i32 s3, s3, 8
	s_waitcnt vmcnt(18)
	v_lshlrev_b32_e32 v16, 16, v80
	v_and_b32_e32 v17, 0xffff0000, v80
	v_lshlrev_b32_e32 v8, 16, v81
	v_and_b32_e32 v9, 0xffff0000, v81
	v_lshlrev_b32_e32 v18, 16, v82
	v_and_b32_e32 v19, 0xffff0000, v82
	v_lshlrev_b32_e32 v10, 16, v83
	v_and_b32_e32 v11, 0xffff0000, v83
	v_lshlrev_b32_e32 v20, 16, v84
	v_and_b32_e32 v21, 0xffff0000, v84
	v_lshlrev_b32_e32 v12, 16, v85
	v_and_b32_e32 v13, 0xffff0000, v85
	v_lshlrev_b32_e32 v22, 16, v86
	v_and_b32_e32 v23, 0xffff0000, v86
	v_lshlrev_b32_e32 v14, 16, v87
	v_and_b32_e32 v15, 0xffff0000, v87
	v_pk_add_f32 v[24:25], v[16:17], v[18:19]
	v_pk_add_f32 v[26:27], v[8:9], v[10:11]
	v_pk_add_f32 v[28:29], v[20:21], v[22:23]
	v_pk_add_f32 v[30:31], v[12:13], v[14:15]
	v_pk_mul_f32 v[10:11], v[10:11], v[10:11]
	v_pk_mul_f32 v[18:19], v[18:19], v[18:19]
	v_pk_mul_f32 v[14:15], v[14:15], v[14:15]
	v_pk_mul_f32 v[22:23], v[22:23], v[22:23]
	v_pk_add_f32 v[26:27], v[26:27], v[30:31]
	v_pk_add_f32 v[24:25], v[24:25], v[28:29]
	v_pk_fma_f32 v[16:17], v[16:17], v[16:17], v[18:19]
	v_pk_fma_f32 v[8:9], v[8:9], v[8:9], v[10:11]
	v_pk_fma_f32 v[10:11], v[20:21], v[20:21], v[22:23]
	v_pk_fma_f32 v[12:13], v[12:13], v[12:13], v[14:15]
	v_pk_add_f32 v[10:11], v[16:17], v[10:11]
	v_pk_add_f32 v[8:9], v[8:9], v[12:13]
	v_add_f32_e32 v1, v24, v25
	v_add_f32_e32 v3, v26, v27
	v_add_f32_e32 v1, v1, v3
	v_add_f32_e32 v3, v10, v11
	v_add_f32_e32 v7, v8, v9
	v_add_f32_e32 v3, v3, v7
	v_add_f32_dpp v1, v1, v1 quad_perm:[1,0,3,2] row_mask:0xf bank_mask:0xf bound_ctrl:1
	s_nop 0
	v_add_f32_dpp v3, v3, v3 quad_perm:[1,0,3,2] row_mask:0xf bank_mask:0xf bound_ctrl:1
	v_add_f32_dpp v1, v1, v1 quad_perm:[2,3,0,1] row_mask:0xf bank_mask:0xf bound_ctrl:1
	s_nop 0
	v_add_f32_dpp v3, v3, v3 quad_perm:[2,3,0,1] row_mask:0xf bank_mask:0xf bound_ctrl:1
	v_add_f32_dpp v1, v1, v1 row_half_mirror row_mask:0xf bank_mask:0xf bound_ctrl:1
	s_nop 0
	v_add_f32_dpp v3, v3, v3 row_half_mirror row_mask:0xf bank_mask:0xf bound_ctrl:1
	v_add_f32_dpp v1, v1, v1 row_mirror row_mask:0xf bank_mask:0xf bound_ctrl:1
	v_mov_b32_e32 v7, v1
	v_add_f32_dpp v8, v3, v3 row_mirror row_mask:0xf bank_mask:0xf bound_ctrl:1
	v_mov_b32_e32 v9, v8
	v_permlane16_swap_b32_e32 v1, v7
	s_nop 0
	v_permlane16_swap_b32_e32 v8, v9
	v_add_f32_e32 v1, v1, v7
	v_add_f32_e32 v7, v8, v9
	v_mov_b32_e32 v3, v1
	v_mov_b32_e32 v8, v7
	s_nop 0
	v_permlane32_swap_b32_e32 v1, v3
	v_permlane32_swap_b32_e32 v7, v8
	s_and_saveexec_b64 s[22:23], s[42:43]
	s_cbranch_execz .Lgm_u1_st6
	v_add_f32_e32 v1, v1, v3
	v_add_f32_e32 v7, v7, v8
	v_mul_f32_e32 v8, 0x3a800000, v1
	v_mul_f32_e32 v1, v8, v8
	v_fma_f32 v1, v7, s13, -v1
	v_max_f32_e32 v1, 0, v1
	v_add_f32_e32 v1, 0x3727c5ac, v1
	v_mul_f32_e32 v3, 0x4f800000, v1
	v_cmp_gt_f32_e32 vcc, s69, v1
	s_add_i32 s21, s11, s3
	s_nop 0
	v_cndmask_b32_e32 v1, v1, v3, vcc
	v_sqrt_f32_e32 v3, v1
	s_nop 0
	v_add_u32_e32 v7, -1, v3
	v_fma_f32 v9, -v7, v3, v1
	v_cmp_ge_f32_e64 s[44:45], 0, v9
	v_add_u32_e32 v9, 1, v3
	s_nop 0
	v_cndmask_b32_e64 v7, v3, v7, s[44:45]
	v_fma_f32 v3, -v9, v3, v1
	v_cmp_lt_f32_e64 s[44:45], 0, v3
	s_nop 1
	v_cndmask_b32_e64 v3, v7, v9, s[44:45]
	v_mul_f32_e32 v7, 0x37800000, v3
	v_cndmask_b32_e32 v3, v3, v7, vcc
	v_cmp_class_f32_e32 vcc, v1, v242
	s_nop 1
	v_cndmask_b32_e32 v1, v3, v1, vcc
	v_div_scale_f32 v3, s[38:39], v1, v1, 1.0
	v_rcp_f32_e32 v7, v3
	s_nop 0
	v_fma_f32 v9, -v3, v7, 1.0
	v_fmac_f32_e32 v7, v9, v7
	v_div_scale_f32 v9, vcc, 1.0, v1, 1.0
	v_mul_f32_e32 v10, v9, v7
	v_fma_f32 v11, -v3, v10, v9
	v_fmac_f32_e32 v10, v11, v7
	v_fma_f32 v3, -v3, v10, v9
	v_div_fmas_f32 v3, v3, v7, v10
	v_div_fixup_f32 v9, v3, v1, 1.0
	v_mov_b32_e32 v1, s21
	ds_write_b64 v1, v[8:9]
; __device__ __forceinline__ void unpk8(const u32x4 w, f32x4& a, f32x4& b) { a = (f32x4){bflo(w.x), bfhi(w.x), bflo(w.y), bfhi(w.y)}; b = (f32x4){bflo(w.z), bfhi(w.z), bflo(w.w), bfhi(w.w)}; }
; __device__ __forceinline__ void gmlp_unit(Frame& F, const Args& a, int layer, int unit) {
;     ...
;     for (int r = 0; r < 16; ++r) { const int tok = wave * 16 + r; const bf16* rowp = GUV + (t0 + tok) * 2048 + 1024;
;         f32x4 x0, x1, x2, x3; unpk8(*(const v4u*)(rowp + lane * 8), x0, x1); unpk8(*(const v4u*)(rowp + 512 + lane * 8), x2, x3);
;         const f32x4 sv = (x0 + x1) + (x2 + x3), qv = (x0 * x0 + x1 * x1) + (x2 * x2 + x3 * x3);
;         const float s = wave_sum((sv.x + sv.y) + (sv.z + sv.w)), q = wave_sum((qv.x + qv.y) + (qv.z + qv.w));
;         const float mean = s * (1.f / 1024.f), var = fmaxf(q * (1.f / 1024.f) - mean * mean, 0.f);
;         if (lane == 0) { st[tok * 2] = mean; st[tok * 2 + 1] = 1.f / sqrtf(var + 1e-5f); } }
.Lgm_u1_st6:
	s_or_b64 exec, exec, s[22:23]
	s_add_i32 s3, s3, 8
	s_waitcnt vmcnt(16)
	v_lshlrev_b32_e32 v16, 16, v88
	v_and_b32_e32 v17, 0xffff0000, v88
	v_lshlrev_b32_e32 v8, 16, v89
	v_and_b32_e32 v9, 0xffff0000, v89
	v_lshlrev_b32_e32 v18, 16, v90
	v_and_b32_e32 v19, 0xffff0000, v90
	v_lshlrev_b32_e32 v10, 16, v91
	v_and_b32_e32 v11, 0xffff0000, v91
	v_lshlrev_b32_e32 v20, 16, v92
	v_and_b32_e32 v21, 0xffff0000, v92
	v_lshlrev_b32_e32 v12, 16, v93
	v_and_b32_e32 v13, 0xffff0000, v93
	v_lshlrev_b32_e32 v22, 16, v94
	v_and_b32_e32 v23, 0xffff0000, v94
	v_lshlrev_b32_e32 v14, 16, v95
	v_and_b32_e32 v15, 0xffff0000, v95
	v_pk_add_f32 v[24:25], v[16:17], v[18:19]
	v_pk_add_f32 v[26:27], v[8:9], v[10:11]
	v_pk_add_f32 v[28:29], v[20:21], v[22:23]
	v_pk_add_f32 v[30:31], v[12:13], v[14:15]
	v_pk_mul_f32 v[10:11], v[10:11], v[10:11]
	v_pk_mul_f32 v[18:19], v[18:19], v[18:19]
	v_pk_mul_f32 v[14:15], v[14:15], v[14:15]
	v_pk_mul_f32 v[22:23], v[22:23], v[22:23]
	v_pk_add_f32 v[26:27], v[26:27], v[30:31]
	v_pk_add_f32 v[24:25], v[24:25], v[28:29]
	v_pk_fma_f32 v[16:17], v[16:17], v[16:17], v[18:19]
	v_pk_fma_f32 v[8:9], v[8:9], v[8:9], v[10:11]
	v_pk_fma_f32 v[10:11], v[20:21], v[20:21], v[22:23]
	v_pk_fma_f32 v[12:13], v[12:13], v[12:13], v[14:15]
	v_pk_add_f32 v[10:11], v[16:17], v[10:11]
	v_pk_add_f32 v[8:9], v[8:9], v[12:13]
	v_add_f32_e32 v1, v24, v25
	v_add_f32_e32 v3, v26, v27
	v_add_f32_e32 v1, v1, v3
	v_add_f32_e32 v3, v10, v11
	v_add_f32_e32 v7, v8, v9
	v_add_f32_e32 v3, v3, v7
	v_add_f32_dpp v1, v1, v1 quad_perm:[1,0,3,2] row_mask:0xf bank_mask:0xf bound_ctrl:1
	s_nop 0
	v_add_f32_dpp v3, v3, v3 quad_perm:[1,0,3,2] row_mask:0xf bank_mask:0xf bound_ctrl:1
	v_add_f32_dpp v1, v1, v1 quad_perm:[2,3,0,1] row_mask:0xf bank_mask:0xf bound_ctrl:1
	s_nop 0
	v_add_f32_dpp v3, v3, v3 quad_perm:[2,3,0,1] row_mask:0xf bank_mask:0xf bound_ctrl:1
	v_add_f32_dpp v1, v1, v1 row_half_mirror row_mask:0xf bank_mask:0xf bound_ctrl:1
	s_nop 0
	v_add_f32_dpp v3, v3, v3 row_half_mirror row_mask:0xf bank_mask:0xf bound_ctrl:1
	v_add_f32_dpp v1, v1, v1 row_mirror row_mask:0xf bank_mask:0xf bound_ctrl:1
	v_mov_b32_e32 v7, v1
	v_add_f32_dpp v8, v3, v3 row_mirror row_mask:0xf bank_mask:0xf bound_ctrl:1
	v_mov_b32_e32 v9, v8
	v_permlane16_swap_b32_e32 v1, v7
	s_nop 0
	v_permlane16_swap_b32_e32 v8, v9
	v_add_f32_e32 v1, v1, v7
	v_add_f32_e32 v7, v8, v9
	v_mov_b32_e32 v3, v1
	v_mov_b32_e32 v8, v7
	s_nop 0
	v_permlane32_swap_b32_e32 v1, v3
	v_permlane32_swap_b32_e32 v7, v8
	s_and_saveexec_b64 s[22:23], s[42:43]
	s_cbranch_execz .Lgm_u1_st7
	v_add_f32_e32 v1, v1, v3
	v_add_f32_e32 v7, v7, v8
	v_mul_f32_e32 v8, 0x3a800000, v1
	v_mul_f32_e32 v1, v8, v8
	v_fma_f32 v1, v7, s13, -v1
	v_max_f32_e32 v1, 0, v1
	v_add_f32_e32 v1, 0x3727c5ac, v1
	v_mul_f32_e32 v3, 0x4f800000, v1
	v_cmp_gt_f32_e32 vcc, s69, v1
	s_add_i32 s21, s11, s3
	s_nop 0
	v_cndmask_b32_e32 v1, v1, v3, vcc
	v_sqrt_f32_e32 v3, v1
	s_nop 0
	v_add_u32_e32 v7, -1, v3
	v_fma_f32 v9, -v7, v3, v1
	v_cmp_ge_f32_e64 s[44:45], 0, v9
	v_add_u32_e32 v9, 1, v3
	s_nop 0
	v_cndmask_b32_e64 v7, v3, v7, s[44:45]
	v_fma_f32 v3, -v9, v3, v1
	v_cmp_lt_f32_e64 s[44:45], 0, v3
	s_nop 1
	v_cndmask_b32_e64 v3, v7, v9, s[44:45]
	v_mul_f32_e32 v7, 0x37800000, v3
	v_cndmask_b32_e32 v3, v3, v7, vcc
	v_cmp_class_f32_e32 vcc, v1, v242
	s_nop 1
	v_cndmask_b32_e32 v1, v3, v1, vcc
	v_div_scale_f32 v3, s[38:39], v1, v1, 1.0
	v_rcp_f32_e32 v7, v3
	s_nop 0
	v_fma_f32 v9, -v3, v7, 1.0
	v_fmac_f32_e32 v7, v9, v7
	v_div_scale_f32 v9, vcc, 1.0, v1, 1.0
	v_mul_f32_e32 v10, v9, v7
	v_fma_f32 v11, -v3, v10, v9
	v_fmac_f32_e32 v10, v11, v7
	v_fma_f32 v3, -v3, v10, v9
	v_div_fmas_f32 v3, v3, v7, v10
	v_div_fixup_f32 v9, v3, v1, 1.0
	v_mov_b32_e32 v1, s21
	ds_write_b64 v1, v[8:9]
.Lgm_u1_st7:
	s_or_b64 exec, exec, s[22:23]
	s_add_i32 s3, s3, 8
	s_waitcnt vmcnt(14)
	v_lshlrev_b32_e32 v16, 16, v100
	v_and_b32_e32 v17, 0xffff0000, v100
	v_lshlrev_b32_e32 v8, 16, v101
	v_and_b32_e32 v9, 0xffff0000, v101
	v_lshlrev_b32_e32 v18, 16, v102
	v_and_b32_e32 v19, 0xffff0000, v102
	v_lshlrev_b32_e32 v10, 16, v103
	v_and_b32_e32 v11, 0xffff0000, v103
	v_lshlrev_b32_e32 v20, 16, v104
	v_and_b32_e32 v21, 0xffff0000, v104
	v_lshlrev_b32_e32 v12, 16, v105
	v_and_b32_e32 v13, 0xffff0000, v105
	v_lshlrev_b32_e32 v22, 16, v106
	v_and_b32_e32 v23, 0xffff0000, v106
	v_lshlrev_b32_e32 v14, 16, v107
	v_and_b32_e32 v15, 0xffff0000, v107
	v_pk_add_f32 v[24:25], v[16:17], v[18:19]
	v_pk_add_f32 v[26:27], v[8:9], v[10:11]
	v_pk_add_f32 v[28:29], v[20:21], v[22:23]
	v_pk_add_f32 v[30:31], v[12:13], v[14:15]
	v_pk_mul_f32 v[10:11], v[10:11], v[10:11]
	v_pk_mul_f32 v[18:19], v[18:19], v[18:19]
	v_pk_mul_f32 v[14:15], v[14:15], v[14:15]
	v_pk_mul_f32 v[22:23], v[22:23], v[22:23]
	v_pk_add_f32 v[26:27], v[26:27], v[30:31]
	v_pk_add_f32 v[24:25], v[24:25], v[28:29]
	v_pk_fma_f32 v[16:17], v[16:17], v[16:17], v[18:19]
	v_pk_fma_f32 v[8:9], v[8:9], v[8:9], v[10:11]
	v_pk_fma_f32 v[10:11], v[20:21], v[20:21], v[22:23]
	v_pk_fma_f32 v[12:13], v[12:13], v[12:13], v[14:15]
	v_pk_add_f32 v[10:11], v[16:17], v[10:11]
	v_pk_add_f32 v[8:9], v[8:9], v[12:13]
	v_add_f32_e32 v1, v24, v25
	v_add_f32_e32 v3, v26, v27
	v_add_f32_e32 v1, v1, v3
	v_add_f32_e32 v3, v10, v11
	v_add_f32_e32 v7, v8, v9
	v_add_f32_e32 v3, v3, v7
	v_add_f32_dpp v1, v1, v1 quad_perm:[1,0,3,2] row_mask:0xf bank_mask:0xf bound_ctrl:1
	s_nop 0
	v_add_f32_dpp v3, v3, v3 quad_perm:[1,0,3,2] row_mask:0xf bank_mask:0xf bound_ctrl:1
	v_add_f32_dpp v1, v1, v1 quad_perm:[2,3,0,1] row_mask:0xf bank_mask:0xf bound_ctrl:1
	s_nop 0
	v_add_f32_dpp v3, v3, v3 quad_perm:[2,3,0,1] row_mask:0xf bank_mask:0xf bound_ctrl:1
	v_add_f32_dpp v1, v1, v1 row_half_mirror row_mask:0xf bank_mask:0xf bound_ctrl:1
	s_nop 0
	v_add_f32_dpp v3, v3, v3 row_half_mirror row_mask:0xf bank_mask:0xf bound_ctrl:1
	v_add_f32_dpp v1, v1, v1 row_mirror row_mask:0xf bank_mask:0xf bound_ctrl:1
	v_mov_b32_e32 v7, v1
	v_add_f32_dpp v8, v3, v3 row_mirror row_mask:0xf bank_mask:0xf bound_ctrl:1
	v_mov_b32_e32 v9, v8
	v_permlane16_swap_b32_e32 v1, v7
	s_nop 0
	v_permlane16_swap_b32_e32 v8, v9
	v_add_f32_e32 v1, v1, v7
	v_add_f32_e32 v7, v8, v9
	v_mov_b32_e32 v3, v1
	v_mov_b32_e32 v8, v7
	s_nop 0
	v_permlane32_swap_b32_e32 v1, v3
	v_permlane32_swap_b32_e32 v7, v8
	s_and_saveexec_b64 s[22:23], s[42:43]
	s_cbranch_execz .Lgm_u1_st8
; __device__ __forceinline__ void unpk8(const u32x4 w, f32x4& a, f32x4& b) { a = (f32x4){bflo(w.x), bfhi(w.x), bflo(w.y), bfhi(w.y)}; b = (f32x4){bflo(w.z), bfhi(w.z), bflo(w.w), bfhi(w.w)}; }
; __device__ __forceinline__ void gmlp_unit(Frame& F, const Args& a, int layer, int unit) {
;     ...
;     for (int r = 0; r < 16; ++r) { const int tok = wave * 16 + r; const bf16* rowp = GUV + (t0 + tok) * 2048 + 1024;
;         f32x4 x0, x1, x2, x3; unpk8(*(const v4u*)(rowp + lane * 8), x0, x1); unpk8(*(const v4u*)(rowp + 512 + lane * 8), x2, x3);
;         const f32x4 sv = (x0 + x1) + (x2 + x3), qv = (x0 * x0 + x1 * x1) + (x2 * x2 + x3 * x3);
;         const float s = wave_sum((sv.x + sv.y) + (sv.z + sv.w)), q = wave_sum((qv.x + qv.y) + (qv.z + qv.w));
;         const float mean = s * (1.f / 1024.f), var = fmaxf(q * (1.f / 1024.f) - mean * mean, 0.f);
;         if (lane == 0) { st[tok * 2] = mean; st[tok * 2 + 1] = 1.f / sqrtf(var + 1e-5f); } }
	v_add_f32_e32 v1, v1, v3
	v_add_f32_e32 v7, v7, v8
	v_mul_f32_e32 v8, 0x3a800000, v1
	v_mul_f32_e32 v1, v8, v8
	v_fma_f32 v1, v7, s13, -v1
	v_max_f32_e32 v1, 0, v1
	v_add_f32_e32 v1, 0x3727c5ac, v1
	v_mul_f32_e32 v3, 0x4f800000, v1
	v_cmp_gt_f32_e32 vcc, s69, v1
	s_add_i32 s21, s11, s3
	s_nop 0
	v_cndmask_b32_e32 v1, v1, v3, vcc
	v_sqrt_f32_e32 v3, v1
	s_nop 0
	v_add_u32_e32 v7, -1, v3
	v_fma_f32 v9, -v7, v3, v1
	v_cmp_ge_f32_e64 s[44:45], 0, v9
	v_add_u32_e32 v9, 1, v3
	s_nop 0
	v_cndmask_b32_e64 v7, v3, v7, s[44:45]
	v_fma_f32 v3, -v9, v3, v1
	v_cmp_lt_f32_e64 s[44:45], 0, v3
	s_nop 1
	v_cndmask_b32_e64 v3, v7, v9, s[44:45]
	v_mul_f32_e32 v7, 0x37800000, v3
	v_cndmask_b32_e32 v3, v3, v7, vcc
	v_cmp_class_f32_e32 vcc, v1, v242
	s_nop 1
	v_cndmask_b32_e32 v1, v3, v1, vcc
	v_div_scale_f32 v3, s[38:39], v1, v1, 1.0
	v_rcp_f32_e32 v7, v3
	s_nop 0
	v_fma_f32 v9, -v3, v7, 1.0
	v_fmac_f32_e32 v7, v9, v7
	v_div_scale_f32 v9, vcc, 1.0, v1, 1.0
	v_mul_f32_e32 v10, v9, v7
	v_fma_f32 v11, -v3, v10, v9
	v_fmac_f32_e32 v10, v11, v7
	v_fma_f32 v3, -v3, v10, v9
	v_div_fmas_f32 v3, v3, v7, v10
	v_div_fixup_f32 v9, v3, v1, 1.0
	v_mov_b32_e32 v1, s21
	ds_write_b64 v1, v[8:9]
.Lgm_u1_st8:
	s_or_b64 exec, exec, s[22:23]
	s_add_i32 s3, s3, 8
	s_waitcnt vmcnt(12)
	v_lshlrev_b32_e32 v16, 16, v108
	v_and_b32_e32 v17, 0xffff0000, v108
	v_lshlrev_b32_e32 v8, 16, v109
	v_and_b32_e32 v9, 0xffff0000, v109
	v_lshlrev_b32_e32 v18, 16, v110
	v_and_b32_e32 v19, 0xffff0000, v110
	v_lshlrev_b32_e32 v10, 16, v111
	v_and_b32_e32 v11, 0xffff0000, v111
	v_lshlrev_b32_e32 v20, 16, v112
	v_and_b32_e32 v21, 0xffff0000, v112
	v_lshlrev_b32_e32 v12, 16, v113
	v_and_b32_e32 v13, 0xffff0000, v113
	v_lshlrev_b32_e32 v22, 16, v114
	v_and_b32_e32 v23, 0xffff0000, v114
	v_lshlrev_b32_e32 v14, 16, v115
	v_and_b32_e32 v15, 0xffff0000, v115
	v_pk_add_f32 v[24:25], v[16:17], v[18:19]
	v_pk_add_f32 v[26:27], v[8:9], v[10:11]
	v_pk_add_f32 v[28:29], v[20:21], v[22:23]
	v_pk_add_f32 v[30:31], v[12:13], v[14:15]
	v_pk_mul_f32 v[10:11], v[10:11], v[10:11]
	v_pk_mul_f32 v[18:19], v[18:19], v[18:19]
	v_pk_mul_f32 v[14:15], v[14:15], v[14:15]
	v_pk_mul_f32 v[22:23], v[22:23], v[22:23]
	v_pk_add_f32 v[26:27], v[26:27], v[30:31]
	v_pk_add_f32 v[24:25], v[24:25], v[28:29]
	v_pk_fma_f32 v[16:17], v[16:17], v[16:17], v[18:19]
	v_pk_fma_f32 v[8:9], v[8:9], v[8:9], v[10:11]
	v_pk_fma_f32 v[10:11], v[20:21], v[20:21], v[22:23]
	v_pk_fma_f32 v[12:13], v[12:13], v[12:13], v[14:15]
	v_pk_add_f32 v[10:11], v[16:17], v[10:11]
	v_pk_add_f32 v[8:9], v[8:9], v[12:13]
	v_add_f32_e32 v1, v24, v25
	v_add_f32_e32 v3, v26, v27
	v_add_f32_e32 v1, v1, v3
	v_add_f32_e32 v3, v10, v11
	v_add_f32_e32 v7, v8, v9
	v_add_f32_e32 v3, v3, v7
	v_add_f32_dpp v1, v1, v1 quad_perm:[1,0,3,2] row_mask:0xf bank_mask:0xf bound_ctrl:1
	s_nop 0
	v_add_f32_dpp v3, v3, v3 quad_perm:[1,0,3,2] row_mask:0xf bank_mask:0xf bound_ctrl:1
	v_add_f32_dpp v1, v1, v1 quad_perm:[2,3,0,1] row_mask:0xf bank_mask:0xf bound_ctrl:1
	s_nop 0
	v_add_f32_dpp v3, v3, v3 quad_perm:[2,3,0,1] row_mask:0xf bank_mask:0xf bound_ctrl:1
	v_add_f32_dpp v1, v1, v1 row_half_mirror row_mask:0xf bank_mask:0xf bound_ctrl:1
	s_nop 0
	v_add_f32_dpp v3, v3, v3 row_half_mirror row_mask:0xf bank_mask:0xf bound_ctrl:1
	v_add_f32_dpp v1, v1, v1 row_mirror row_mask:0xf bank_mask:0xf bound_ctrl:1
	v_mov_b32_e32 v7, v1
	v_add_f32_dpp v8, v3, v3 row_mirror row_mask:0xf bank_mask:0xf bound_ctrl:1
	v_mov_b32_e32 v9, v8
	v_permlane16_swap_b32_e32 v1, v7
	s_nop 0
	v_permlane16_swap_b32_e32 v8, v9
	v_add_f32_e32 v1, v1, v7
	v_add_f32_e32 v7, v8, v9
	v_mov_b32_e32 v3, v1
	v_mov_b32_e32 v8, v7
	s_nop 0
	v_permlane32_swap_b32_e32 v1, v3
	v_permlane32_swap_b32_e32 v7, v8
	s_and_saveexec_b64 s[22:23], s[42:43]
	s_cbranch_execz .Lgm_u1_st9
	v_add_f32_e32 v1, v1, v3
	v_add_f32_e32 v7, v7, v8
	v_mul_f32_e32 v8, 0x3a800000, v1
	v_mul_f32_e32 v1, v8, v8
	v_fma_f32 v1, v7, s13, -v1
	v_max_f32_e32 v1, 0, v1
	v_add_f32_e32 v1, 0x3727c5ac, v1
	v_mul_f32_e32 v3, 0x4f800000, v1
	v_cmp_gt_f32_e32 vcc, s69, v1
	s_add_i32 s21, s11, s3
	s_nop 0
	v_cndmask_b32_e32 v1, v1, v3, vcc
	v_sqrt_f32_e32 v3, v1
	s_nop 0
	v_add_u32_e32 v7, -1, v3
	v_fma_f32 v9, -v7, v3, v1
	v_cmp_ge_f32_e64 s[44:45], 0, v9
	v_add_u32_e32 v9, 1, v3
	s_nop 0
	v_cndmask_b32_e64 v7, v3, v7, s[44:45]
	v_fma_f32 v3, -v9, v3, v1
	v_cmp_lt_f32_e64 s[44:45], 0, v3
	s_nop 1
	v_cndmask_b32_e64 v3, v7, v9, s[44:45]
	v_mul_f32_e32 v7, 0x37800000, v3
	v_cndmask_b32_e32 v3, v3, v7, vcc
	v_cmp_class_f32_e32 vcc, v1, v242
	s_nop 1
	v_cndmask_b32_e32 v1, v3, v1, vcc
	v_div_scale_f32 v3, s[38:39], v1, v1, 1.0
	v_rcp_f32_e32 v7, v3
	s_nop 0
	v_fma_f32 v9, -v3, v7, 1.0
	v_fmac_f32_e32 v7, v9, v7
	v_div_scale_f32 v9, vcc, 1.0, v1, 1.0
	v_mul_f32_e32 v10, v9, v7
	v_fma_f32 v11, -v3, v10, v9
	v_fmac_f32_e32 v10, v11, v7
	v_fma_f32 v3, -v3, v10, v9
	v_div_fmas_f32 v3, v3, v7, v10
	v_div_fixup_f32 v9, v3, v1, 1.0
	v_mov_b32_e32 v1, s21
	ds_write_b64 v1, v[8:9]
; __device__ __forceinline__ void unpk8(const u32x4 w, f32x4& a, f32x4& b) { a = (f32x4){bflo(w.x), bfhi(w.x), bflo(w.y), bfhi(w.y)}; b = (f32x4){bflo(w.z), bfhi(w.z), bflo(w.w), bfhi(w.w)}; }
; __device__ __forceinline__ void gmlp_unit(Frame& F, const Args& a, int layer, int unit) {
;     ...
;     for (int r = 0; r < 16; ++r) { const int tok = wave * 16 + r; const bf16* rowp = GUV + (t0 + tok) * 2048 + 1024;
;         f32x4 x0, x1, x2, x3; unpk8(*(const v4u*)(rowp + lane * 8), x0, x1); unpk8(*(const v4u*)(rowp + 512 + lane * 8), x2, x3);
;         const f32x4 sv = (x0 + x1) + (x2 + x3), qv = (x0 * x0 + x1 * x1) + (x2 * x2 + x3 * x3);
;         const float s = wave_sum((sv.x + sv.y) + (sv.z + sv.w)), q = wave_sum((qv.x + qv.y) + (qv.z + qv.w));
;         const float mean = s * (1.f / 1024.f), var = fmaxf(q * (1.f / 1024.f) - mean * mean, 0.f);
;         if (lane == 0) { st[tok * 2] = mean; st[tok * 2 + 1] = 1.f / sqrtf(var + 1e-5f); } }
.Lgm_u1_st9:
	s_or_b64 exec, exec, s[22:23]
	s_add_i32 s3, s3, 8
	s_waitcnt vmcnt(10)
	v_lshlrev_b32_e32 v16, 16, v116
	v_and_b32_e32 v17, 0xffff0000, v116
	v_lshlrev_b32_e32 v8, 16, v117
	v_and_b32_e32 v9, 0xffff0000, v117
	v_lshlrev_b32_e32 v18, 16, v118
	v_and_b32_e32 v19, 0xffff0000, v118
	v_lshlrev_b32_e32 v10, 16, v119
	v_and_b32_e32 v11, 0xffff0000, v119
	v_lshlrev_b32_e32 v20, 16, v120
	v_and_b32_e32 v21, 0xffff0000, v120
	v_lshlrev_b32_e32 v12, 16, v121
	v_and_b32_e32 v13, 0xffff0000, v121
	v_lshlrev_b32_e32 v22, 16, v122
	v_and_b32_e32 v23, 0xffff0000, v122
	v_lshlrev_b32_e32 v14, 16, v123
	v_and_b32_e32 v15, 0xffff0000, v123
	v_pk_add_f32 v[24:25], v[16:17], v[18:19]
	v_pk_add_f32 v[26:27], v[8:9], v[10:11]
	v_pk_add_f32 v[28:29], v[20:21], v[22:23]
	v_pk_add_f32 v[30:31], v[12:13], v[14:15]
	v_pk_mul_f32 v[10:11], v[10:11], v[10:11]
	v_pk_mul_f32 v[18:19], v[18:19], v[18:19]
	v_pk_mul_f32 v[14:15], v[14:15], v[14:15]
	v_pk_mul_f32 v[22:23], v[22:23], v[22:23]
	v_pk_add_f32 v[26:27], v[26:27], v[30:31]
	v_pk_add_f32 v[24:25], v[24:25], v[28:29]
	v_pk_fma_f32 v[16:17], v[16:17], v[16:17], v[18:19]
	v_pk_fma_f32 v[8:9], v[8:9], v[8:9], v[10:11]
	v_pk_fma_f32 v[10:11], v[20:21], v[20:21], v[22:23]
	v_pk_fma_f32 v[12:13], v[12:13], v[12:13], v[14:15]
	v_pk_add_f32 v[10:11], v[16:17], v[10:11]
	v_pk_add_f32 v[8:9], v[8:9], v[12:13]
	v_add_f32_e32 v1, v24, v25
	v_add_f32_e32 v3, v26, v27
	v_add_f32_e32 v1, v1, v3
	v_add_f32_e32 v3, v10, v11
	v_add_f32_e32 v7, v8, v9
	v_add_f32_e32 v3, v3, v7
	v_add_f32_dpp v1, v1, v1 quad_perm:[1,0,3,2] row_mask:0xf bank_mask:0xf bound_ctrl:1
	s_nop 0
	v_add_f32_dpp v3, v3, v3 quad_perm:[1,0,3,2] row_mask:0xf bank_mask:0xf bound_ctrl:1
	v_add_f32_dpp v1, v1, v1 quad_perm:[2,3,0,1] row_mask:0xf bank_mask:0xf bound_ctrl:1
	s_nop 0
	v_add_f32_dpp v3, v3, v3 quad_perm:[2,3,0,1] row_mask:0xf bank_mask:0xf bound_ctrl:1
	v_add_f32_dpp v1, v1, v1 row_half_mirror row_mask:0xf bank_mask:0xf bound_ctrl:1
	s_nop 0
	v_add_f32_dpp v3, v3, v3 row_half_mirror row_mask:0xf bank_mask:0xf bound_ctrl:1
	v_add_f32_dpp v1, v1, v1 row_mirror row_mask:0xf bank_mask:0xf bound_ctrl:1
	v_mov_b32_e32 v7, v1
	v_add_f32_dpp v8, v3, v3 row_mirror row_mask:0xf bank_mask:0xf bound_ctrl:1
	v_mov_b32_e32 v9, v8
	v_permlane16_swap_b32_e32 v1, v7
	s_nop 0
	v_permlane16_swap_b32_e32 v8, v9
	v_add_f32_e32 v1, v1, v7
	v_add_f32_e32 v7, v8, v9
	v_mov_b32_e32 v3, v1
	v_mov_b32_e32 v8, v7
	s_nop 0
	v_permlane32_swap_b32_e32 v1, v3
	v_permlane32_swap_b32_e32 v7, v8
	s_and_saveexec_b64 s[22:23], s[42:43]
	s_cbranch_execz .Lgm_u1_st10
	v_add_f32_e32 v1, v1, v3
	v_add_f32_e32 v7, v7, v8
	v_mul_f32_e32 v8, 0x3a800000, v1
	v_mul_f32_e32 v1, v8, v8
	v_fma_f32 v1, v7, s13, -v1
	v_max_f32_e32 v1, 0, v1
	v_add_f32_e32 v1, 0x3727c5ac, v1
	v_mul_f32_e32 v3, 0x4f800000, v1
	v_cmp_gt_f32_e32 vcc, s69, v1
	s_add_i32 s21, s11, s3
	s_nop 0
	v_cndmask_b32_e32 v1, v1, v3, vcc
	v_sqrt_f32_e32 v3, v1
	s_nop 0
	v_add_u32_e32 v7, -1, v3
	v_fma_f32 v9, -v7, v3, v1
	v_cmp_ge_f32_e64 s[44:45], 0, v9
	v_add_u32_e32 v9, 1, v3
	s_nop 0
	v_cndmask_b32_e64 v7, v3, v7, s[44:45]
	v_fma_f32 v3, -v9, v3, v1
	v_cmp_lt_f32_e64 s[44:45], 0, v3
	s_nop 1
	v_cndmask_b32_e64 v3, v7, v9, s[44:45]
	v_mul_f32_e32 v7, 0x37800000, v3
	v_cndmask_b32_e32 v3, v3, v7, vcc
	v_cmp_class_f32_e32 vcc, v1, v242
	s_nop 1
	v_cndmask_b32_e32 v1, v3, v1, vcc
	v_div_scale_f32 v3, s[38:39], v1, v1, 1.0
	v_rcp_f32_e32 v7, v3
	s_nop 0
	v_fma_f32 v9, -v3, v7, 1.0
	v_fmac_f32_e32 v7, v9, v7
	v_div_scale_f32 v9, vcc, 1.0, v1, 1.0
	v_mul_f32_e32 v10, v9, v7
	v_fma_f32 v11, -v3, v10, v9
	v_fmac_f32_e32 v10, v11, v7
	v_fma_f32 v3, -v3, v10, v9
	v_div_fmas_f32 v3, v3, v7, v10
	v_div_fixup_f32 v9, v3, v1, 1.0
	v_mov_b32_e32 v1, s21
	ds_write_b64 v1, v[8:9]
.Lgm_u1_st10:
	s_or_b64 exec, exec, s[22:23]
	s_add_i32 s3, s3, 8
	s_waitcnt vmcnt(8)
	v_lshlrev_b32_e32 v16, 16, v124
	v_and_b32_e32 v17, 0xffff0000, v124
	v_lshlrev_b32_e32 v8, 16, v125
	v_and_b32_e32 v9, 0xffff0000, v125
	v_lshlrev_b32_e32 v18, 16, v126
	v_and_b32_e32 v19, 0xffff0000, v126
	v_lshlrev_b32_e32 v10, 16, v127
	v_and_b32_e32 v11, 0xffff0000, v127
	v_lshlrev_b32_e32 v20, 16, v128
	v_and_b32_e32 v21, 0xffff0000, v128
	v_lshlrev_b32_e32 v12, 16, v129
	v_and_b32_e32 v13, 0xffff0000, v129
	v_lshlrev_b32_e32 v22, 16, v130
	v_and_b32_e32 v23, 0xffff0000, v130
	v_lshlrev_b32_e32 v14, 16, v131
	v_and_b32_e32 v15, 0xffff0000, v131
	v_pk_add_f32 v[24:25], v[16:17], v[18:19]
	v_pk_add_f32 v[26:27], v[8:9], v[10:11]
	v_pk_add_f32 v[28:29], v[20:21], v[22:23]
	v_pk_add_f32 v[30:31], v[12:13], v[14:15]
	v_pk_mul_f32 v[10:11], v[10:11], v[10:11]
	v_pk_mul_f32 v[18:19], v[18:19], v[18:19]
	v_pk_mul_f32 v[14:15], v[14:15], v[14:15]
	v_pk_mul_f32 v[22:23], v[22:23], v[22:23]
	v_pk_add_f32 v[26:27], v[26:27], v[30:31]
	v_pk_add_f32 v[24:25], v[24:25], v[28:29]
	v_pk_fma_f32 v[16:17], v[16:17], v[16:17], v[18:19]
	v_pk_fma_f32 v[8:9], v[8:9], v[8:9], v[10:11]
	v_pk_fma_f32 v[10:11], v[20:21], v[20:21], v[22:23]
	v_pk_fma_f32 v[12:13], v[12:13], v[12:13], v[14:15]
	v_pk_add_f32 v[10:11], v[16:17], v[10:11]
	v_pk_add_f32 v[8:9], v[8:9], v[12:13]
	v_add_f32_e32 v1, v24, v25
	v_add_f32_e32 v3, v26, v27
	v_add_f32_e32 v1, v1, v3
	v_add_f32_e32 v3, v10, v11
	v_add_f32_e32 v7, v8, v9
	v_add_f32_e32 v3, v3, v7
	v_add_f32_dpp v1, v1, v1 quad_perm:[1,0,3,2] row_mask:0xf bank_mask:0xf bound_ctrl:1
	s_nop 0
	v_add_f32_dpp v3, v3, v3 quad_perm:[1,0,3,2] row_mask:0xf bank_mask:0xf bound_ctrl:1
	v_add_f32_dpp v1, v1, v1 quad_perm:[2,3,0,1] row_mask:0xf bank_mask:0xf bound_ctrl:1
	s_nop 0
	v_add_f32_dpp v3, v3, v3 quad_perm:[2,3,0,1] row_mask:0xf bank_mask:0xf bound_ctrl:1
	v_add_f32_dpp v1, v1, v1 row_half_mirror row_mask:0xf bank_mask:0xf bound_ctrl:1
	s_nop 0
	v_add_f32_dpp v3, v3, v3 row_half_mirror row_mask:0xf bank_mask:0xf bound_ctrl:1
	v_add_f32_dpp v1, v1, v1 row_mirror row_mask:0xf bank_mask:0xf bound_ctrl:1
	v_mov_b32_e32 v7, v1
	v_add_f32_dpp v8, v3, v3 row_mirror row_mask:0xf bank_mask:0xf bound_ctrl:1
	v_mov_b32_e32 v9, v8
	v_permlane16_swap_b32_e32 v1, v7
	s_nop 0
	v_permlane16_swap_b32_e32 v8, v9
	v_add_f32_e32 v1, v1, v7
	v_add_f32_e32 v7, v8, v9
	v_mov_b32_e32 v3, v1
	v_mov_b32_e32 v8, v7
	s_nop 0
	v_permlane32_swap_b32_e32 v1, v3
	v_permlane32_swap_b32_e32 v7, v8
	s_and_saveexec_b64 s[22:23], s[42:43]
	s_cbranch_execz .Lgm_u1_st11
; __device__ __forceinline__ void unpk8(const u32x4 w, f32x4& a, f32x4& b) { a = (f32x4){bflo(w.x), bfhi(w.x), bflo(w.y), bfhi(w.y)}; b = (f32x4){bflo(w.z), bfhi(w.z), bflo(w.w), bfhi(w.w)}; }
; __device__ __forceinline__ void gmlp_unit(Frame& F, const Args& a, int layer, int unit) {
;     ...
;     for (int r = 0; r < 16; ++r) { const int tok = wave * 16 + r; const bf16* rowp = GUV + (t0 + tok) * 2048 + 1024;
;         f32x4 x0, x1, x2, x3; unpk8(*(const v4u*)(rowp + lane * 8), x0, x1); unpk8(*(const v4u*)(rowp + 512 + lane * 8), x2, x3);
;         const f32x4 sv = (x0 + x1) + (x2 + x3), qv = (x0 * x0 + x1 * x1) + (x2 * x2 + x3 * x3);
;         const float s = wave_sum((sv.x + sv.y) + (sv.z + sv.w)), q = wave_sum((qv.x + qv.y) + (qv.z + qv.w));
;         const float mean = s * (1.f / 1024.f), var = fmaxf(q * (1.f / 1024.f) - mean * mean, 0.f);
;         if (lane == 0) { st[tok * 2] = mean; st[tok * 2 + 1] = 1.f / sqrtf(var + 1e-5f); } }
	v_add_f32_e32 v1, v1, v3
	v_add_f32_e32 v7, v7, v8
	v_mul_f32_e32 v8, 0x3a800000, v1
	v_mul_f32_e32 v1, v8, v8
	v_fma_f32 v1, v7, s13, -v1
	v_max_f32_e32 v1, 0, v1
	v_add_f32_e32 v1, 0x3727c5ac, v1
	v_mul_f32_e32 v3, 0x4f800000, v1
	v_cmp_gt_f32_e32 vcc, s69, v1
	s_add_i32 s21, s11, s3
	s_nop 0
	v_cndmask_b32_e32 v1, v1, v3, vcc
	v_sqrt_f32_e32 v3, v1
	s_nop 0
	v_add_u32_e32 v7, -1, v3
	v_fma_f32 v9, -v7, v3, v1
	v_cmp_ge_f32_e64 s[44:45], 0, v9
	v_add_u32_e32 v9, 1, v3
	s_nop 0
	v_cndmask_b32_e64 v7, v3, v7, s[44:45]
	v_fma_f32 v3, -v9, v3, v1
	v_cmp_lt_f32_e64 s[44:45], 0, v3
	s_nop 1
	v_cndmask_b32_e64 v3, v7, v9, s[44:45]
	v_mul_f32_e32 v7, 0x37800000, v3
	v_cndmask_b32_e32 v3, v3, v7, vcc
	v_cmp_class_f32_e32 vcc, v1, v242
	s_nop 1
	v_cndmask_b32_e32 v1, v3, v1, vcc
	v_div_scale_f32 v3, s[38:39], v1, v1, 1.0
	v_rcp_f32_e32 v7, v3
	s_nop 0
	v_fma_f32 v9, -v3, v7, 1.0
	v_fmac_f32_e32 v7, v9, v7
	v_div_scale_f32 v9, vcc, 1.0, v1, 1.0
	v_mul_f32_e32 v10, v9, v7
	v_fma_f32 v11, -v3, v10, v9
	v_fmac_f32_e32 v10, v11, v7
	v_fma_f32 v3, -v3, v10, v9
	v_div_fmas_f32 v3, v3, v7, v10
	v_div_fixup_f32 v9, v3, v1, 1.0
	v_mov_b32_e32 v1, s21
	ds_write_b64 v1, v[8:9]
.Lgm_u1_st11:
	s_or_b64 exec, exec, s[22:23]
	s_add_i32 s3, s3, 8
	s_waitcnt vmcnt(6)
	v_lshlrev_b32_e32 v16, 16, v132
	v_and_b32_e32 v17, 0xffff0000, v132
	v_lshlrev_b32_e32 v8, 16, v133
	v_and_b32_e32 v9, 0xffff0000, v133
	v_lshlrev_b32_e32 v18, 16, v134
	v_and_b32_e32 v19, 0xffff0000, v134
	v_lshlrev_b32_e32 v10, 16, v135
	v_and_b32_e32 v11, 0xffff0000, v135
	v_lshlrev_b32_e32 v20, 16, v136
	v_and_b32_e32 v21, 0xffff0000, v136
	v_lshlrev_b32_e32 v12, 16, v137
	v_and_b32_e32 v13, 0xffff0000, v137
	v_lshlrev_b32_e32 v22, 16, v138
	v_and_b32_e32 v23, 0xffff0000, v138
	v_lshlrev_b32_e32 v14, 16, v139
	v_and_b32_e32 v15, 0xffff0000, v139
	v_pk_add_f32 v[24:25], v[16:17], v[18:19]
	v_pk_add_f32 v[26:27], v[8:9], v[10:11]
	v_pk_add_f32 v[28:29], v[20:21], v[22:23]
	v_pk_add_f32 v[30:31], v[12:13], v[14:15]
	v_pk_mul_f32 v[10:11], v[10:11], v[10:11]
	v_pk_mul_f32 v[18:19], v[18:19], v[18:19]
	v_pk_mul_f32 v[14:15], v[14:15], v[14:15]
	v_pk_mul_f32 v[22:23], v[22:23], v[22:23]
	v_pk_add_f32 v[26:27], v[26:27], v[30:31]
	v_pk_add_f32 v[24:25], v[24:25], v[28:29]
	v_pk_fma_f32 v[16:17], v[16:17], v[16:17], v[18:19]
	v_pk_fma_f32 v[8:9], v[8:9], v[8:9], v[10:11]
	v_pk_fma_f32 v[10:11], v[20:21], v[20:21], v[22:23]
	v_pk_fma_f32 v[12:13], v[12:13], v[12:13], v[14:15]
	v_pk_add_f32 v[10:11], v[16:17], v[10:11]
	v_pk_add_f32 v[8:9], v[8:9], v[12:13]
	v_add_f32_e32 v1, v24, v25
	v_add_f32_e32 v3, v26, v27
	v_add_f32_e32 v1, v1, v3
	v_add_f32_e32 v3, v10, v11
	v_add_f32_e32 v7, v8, v9
	v_add_f32_e32 v3, v3, v7
	v_add_f32_dpp v1, v1, v1 quad_perm:[1,0,3,2] row_mask:0xf bank_mask:0xf bound_ctrl:1
	s_nop 0
	v_add_f32_dpp v3, v3, v3 quad_perm:[1,0,3,2] row_mask:0xf bank_mask:0xf bound_ctrl:1
	v_add_f32_dpp v1, v1, v1 quad_perm:[2,3,0,1] row_mask:0xf bank_mask:0xf bound_ctrl:1
	s_nop 0
	v_add_f32_dpp v3, v3, v3 quad_perm:[2,3,0,1] row_mask:0xf bank_mask:0xf bound_ctrl:1
	v_add_f32_dpp v1, v1, v1 row_half_mirror row_mask:0xf bank_mask:0xf bound_ctrl:1
	s_nop 0
	v_add_f32_dpp v3, v3, v3 row_half_mirror row_mask:0xf bank_mask:0xf bound_ctrl:1
	v_add_f32_dpp v1, v1, v1 row_mirror row_mask:0xf bank_mask:0xf bound_ctrl:1
	v_mov_b32_e32 v7, v1
	v_add_f32_dpp v8, v3, v3 row_mirror row_mask:0xf bank_mask:0xf bound_ctrl:1
	v_mov_b32_e32 v9, v8
	v_permlane16_swap_b32_e32 v1, v7
	s_nop 0
	v_permlane16_swap_b32_e32 v8, v9
	v_add_f32_e32 v1, v1, v7
	v_add_f32_e32 v7, v8, v9
	v_mov_b32_e32 v3, v1
	v_mov_b32_e32 v8, v7
	s_nop 0
	v_permlane32_swap_b32_e32 v1, v3
	v_permlane32_swap_b32_e32 v7, v8
	s_and_saveexec_b64 s[22:23], s[42:43]
	s_cbranch_execz .Lgm_u1_st12
	v_add_f32_e32 v1, v1, v3
	v_add_f32_e32 v7, v7, v8
	v_mul_f32_e32 v8, 0x3a800000, v1
	v_mul_f32_e32 v1, v8, v8
	v_fma_f32 v1, v7, s13, -v1
	v_max_f32_e32 v1, 0, v1
	v_add_f32_e32 v1, 0x3727c5ac, v1
	v_mul_f32_e32 v3, 0x4f800000, v1
	v_cmp_gt_f32_e32 vcc, s69, v1
	s_add_i32 s21, s11, s3
	s_nop 0
	v_cndmask_b32_e32 v1, v1, v3, vcc
	v_sqrt_f32_e32 v3, v1
	s_nop 0
	v_add_u32_e32 v7, -1, v3
	v_fma_f32 v9, -v7, v3, v1
	v_cmp_ge_f32_e64 s[44:45], 0, v9
	v_add_u32_e32 v9, 1, v3
	s_nop 0
	v_cndmask_b32_e64 v7, v3, v7, s[44:45]
	v_fma_f32 v3, -v9, v3, v1
	v_cmp_lt_f32_e64 s[44:45], 0, v3
	s_nop 1
	v_cndmask_b32_e64 v3, v7, v9, s[44:45]
	v_mul_f32_e32 v7, 0x37800000, v3
	v_cndmask_b32_e32 v3, v3, v7, vcc
	v_cmp_class_f32_e32 vcc, v1, v242
	s_nop 1
	v_cndmask_b32_e32 v1, v3, v1, vcc
	v_div_scale_f32 v3, s[38:39], v1, v1, 1.0
	v_rcp_f32_e32 v7, v3
	s_nop 0
	v_fma_f32 v9, -v3, v7, 1.0
	v_fmac_f32_e32 v7, v9, v7
	v_div_scale_f32 v9, vcc, 1.0, v1, 1.0
	v_mul_f32_e32 v10, v9, v7
	v_fma_f32 v11, -v3, v10, v9
	v_fmac_f32_e32 v10, v11, v7
	v_fma_f32 v3, -v3, v10, v9
	v_div_fmas_f32 v3, v3, v7, v10
	v_div_fixup_f32 v9, v3, v1, 1.0
	v_mov_b32_e32 v1, s21
	ds_write_b64 v1, v[8:9]
; __device__ __forceinline__ void unpk8(const u32x4 w, f32x4& a, f32x4& b) { a = (f32x4){bflo(w.x), bfhi(w.x), bflo(w.y), bfhi(w.y)}; b = (f32x4){bflo(w.z), bfhi(w.z), bflo(w.w), bfhi(w.w)}; }
; __device__ __forceinline__ void gmlp_unit(Frame& F, const Args& a, int layer, int unit) {
;     ...
;     for (int r = 0; r < 16; ++r) { const int tok = wave * 16 + r; const bf16* rowp = GUV + (t0 + tok) * 2048 + 1024;
;         f32x4 x0, x1, x2, x3; unpk8(*(const v4u*)(rowp + lane * 8), x0, x1); unpk8(*(const v4u*)(rowp + 512 + lane * 8), x2, x3);
;         const f32x4 sv = (x0 + x1) + (x2 + x3), qv = (x0 * x0 + x1 * x1) + (x2 * x2 + x3 * x3);
;         const float s = wave_sum((sv.x + sv.y) + (sv.z + sv.w)), q = wave_sum((qv.x + qv.y) + (qv.z + qv.w));
;         const float mean = s * (1.f / 1024.f), var = fmaxf(q * (1.f / 1024.f) - mean * mean, 0.f);
;         if (lane == 0) { st[tok * 2] = mean; st[tok * 2 + 1] = 1.f / sqrtf(var + 1e-5f); } }
.Lgm_u1_st12:
	s_or_b64 exec, exec, s[22:23]
	s_add_i32 s3, s3, 8
	s_waitcnt vmcnt(4)
	v_lshlrev_b32_e32 v16, 16, v140
	v_and_b32_e32 v17, 0xffff0000, v140
	v_lshlrev_b32_e32 v8, 16, v141
	v_and_b32_e32 v9, 0xffff0000, v141
	v_lshlrev_b32_e32 v18, 16, v142
	v_and_b32_e32 v19, 0xffff0000, v142
	v_lshlrev_b32_e32 v10, 16, v143
	v_and_b32_e32 v11, 0xffff0000, v143
	v_lshlrev_b32_e32 v20, 16, v144
	v_and_b32_e32 v21, 0xffff0000, v144
	v_lshlrev_b32_e32 v12, 16, v145
	v_and_b32_e32 v13, 0xffff0000, v145
	v_lshlrev_b32_e32 v22, 16, v146
	v_and_b32_e32 v23, 0xffff0000, v146
	v_lshlrev_b32_e32 v14, 16, v147
	v_and_b32_e32 v15, 0xffff0000, v147
	v_pk_add_f32 v[24:25], v[16:17], v[18:19]
	v_pk_add_f32 v[26:27], v[8:9], v[10:11]
	v_pk_add_f32 v[28:29], v[20:21], v[22:23]
	v_pk_add_f32 v[30:31], v[12:13], v[14:15]
	v_pk_mul_f32 v[10:11], v[10:11], v[10:11]
	v_pk_mul_f32 v[18:19], v[18:19], v[18:19]
	v_pk_mul_f32 v[14:15], v[14:15], v[14:15]
	v_pk_mul_f32 v[22:23], v[22:23], v[22:23]
	v_pk_add_f32 v[26:27], v[26:27], v[30:31]
	v_pk_add_f32 v[24:25], v[24:25], v[28:29]
	v_pk_fma_f32 v[16:17], v[16:17], v[16:17], v[18:19]
	v_pk_fma_f32 v[8:9], v[8:9], v[8:9], v[10:11]
	v_pk_fma_f32 v[10:11], v[20:21], v[20:21], v[22:23]
	v_pk_fma_f32 v[12:13], v[12:13], v[12:13], v[14:15]
	v_pk_add_f32 v[10:11], v[16:17], v[10:11]
	v_pk_add_f32 v[8:9], v[8:9], v[12:13]
	v_add_f32_e32 v1, v24, v25
	v_add_f32_e32 v3, v26, v27
	v_add_f32_e32 v1, v1, v3
	v_add_f32_e32 v3, v10, v11
	v_add_f32_e32 v7, v8, v9
	v_add_f32_e32 v3, v3, v7
	v_add_f32_dpp v1, v1, v1 quad_perm:[1,0,3,2] row_mask:0xf bank_mask:0xf bound_ctrl:1
	s_nop 0
	v_add_f32_dpp v3, v3, v3 quad_perm:[1,0,3,2] row_mask:0xf bank_mask:0xf bound_ctrl:1
	v_add_f32_dpp v1, v1, v1 quad_perm:[2,3,0,1] row_mask:0xf bank_mask:0xf bound_ctrl:1
	s_nop 0
	v_add_f32_dpp v3, v3, v3 quad_perm:[2,3,0,1] row_mask:0xf bank_mask:0xf bound_ctrl:1
	v_add_f32_dpp v1, v1, v1 row_half_mirror row_mask:0xf bank_mask:0xf bound_ctrl:1
	s_nop 0
	v_add_f32_dpp v3, v3, v3 row_half_mirror row_mask:0xf bank_mask:0xf bound_ctrl:1
	v_add_f32_dpp v1, v1, v1 row_mirror row_mask:0xf bank_mask:0xf bound_ctrl:1
	v_mov_b32_e32 v7, v1
	v_add_f32_dpp v8, v3, v3 row_mirror row_mask:0xf bank_mask:0xf bound_ctrl:1
	v_mov_b32_e32 v9, v8
	v_permlane16_swap_b32_e32 v1, v7
	s_nop 0
	v_permlane16_swap_b32_e32 v8, v9
	v_add_f32_e32 v1, v1, v7
	v_add_f32_e32 v7, v8, v9
	v_mov_b32_e32 v3, v1
	v_mov_b32_e32 v8, v7
	s_nop 0
	v_permlane32_swap_b32_e32 v1, v3
	v_permlane32_swap_b32_e32 v7, v8
	s_and_saveexec_b64 s[22:23], s[42:43]
	s_cbranch_execz .Lgm_u1_st13
	v_add_f32_e32 v1, v1, v3
	v_add_f32_e32 v7, v7, v8
	v_mul_f32_e32 v8, 0x3a800000, v1
	v_mul_f32_e32 v1, v8, v8
	v_fma_f32 v1, v7, s13, -v1
	v_max_f32_e32 v1, 0, v1
	v_add_f32_e32 v1, 0x3727c5ac, v1
	v_mul_f32_e32 v3, 0x4f800000, v1
	v_cmp_gt_f32_e32 vcc, s69, v1
	s_add_i32 s21, s11, s3
	s_nop 0
	v_cndmask_b32_e32 v1, v1, v3, vcc
	v_sqrt_f32_e32 v3, v1
	s_nop 0
	v_add_u32_e32 v7, -1, v3
	v_fma_f32 v9, -v7, v3, v1
	v_cmp_ge_f32_e64 s[44:45], 0, v9
	v_add_u32_e32 v9, 1, v3
	s_nop 0
	v_cndmask_b32_e64 v7, v3, v7, s[44:45]
	v_fma_f32 v3, -v9, v3, v1
	v_cmp_lt_f32_e64 s[44:45], 0, v3
	s_nop 1
	v_cndmask_b32_e64 v3, v7, v9, s[44:45]
	v_mul_f32_e32 v7, 0x37800000, v3
	v_cndmask_b32_e32 v3, v3, v7, vcc
	v_cmp_class_f32_e32 vcc, v1, v242
	s_nop 1
	v_cndmask_b32_e32 v1, v3, v1, vcc
	v_div_scale_f32 v3, s[38:39], v1, v1, 1.0
	v_rcp_f32_e32 v7, v3
	s_nop 0
	v_fma_f32 v9, -v3, v7, 1.0
	v_fmac_f32_e32 v7, v9, v7
	v_div_scale_f32 v9, vcc, 1.0, v1, 1.0
	v_mul_f32_e32 v10, v9, v7
	v_fma_f32 v11, -v3, v10, v9
	v_fmac_f32_e32 v10, v11, v7
	v_fma_f32 v3, -v3, v10, v9
	v_div_fmas_f32 v3, v3, v7, v10
	v_div_fixup_f32 v9, v3, v1, 1.0
	v_mov_b32_e32 v1, s21
	ds_write_b64 v1, v[8:9]
.Lgm_u1_st13:
	s_or_b64 exec, exec, s[22:23]
	s_add_i32 s3, s3, 8
	s_waitcnt vmcnt(2)
	v_lshlrev_b32_e32 v16, 16, v148
	v_and_b32_e32 v17, 0xffff0000, v148
	v_lshlrev_b32_e32 v8, 16, v149
	v_and_b32_e32 v9, 0xffff0000, v149
	v_lshlrev_b32_e32 v18, 16, v150
	v_and_b32_e32 v19, 0xffff0000, v150
	v_lshlrev_b32_e32 v10, 16, v151
	v_and_b32_e32 v11, 0xffff0000, v151
	v_lshlrev_b32_e32 v20, 16, v152
	v_and_b32_e32 v21, 0xffff0000, v152
	v_lshlrev_b32_e32 v12, 16, v153
	v_and_b32_e32 v13, 0xffff0000, v153
	v_lshlrev_b32_e32 v22, 16, v154
	v_and_b32_e32 v23, 0xffff0000, v154
	v_lshlrev_b32_e32 v14, 16, v155
	v_and_b32_e32 v15, 0xffff0000, v155
	v_pk_add_f32 v[24:25], v[16:17], v[18:19]
	v_pk_add_f32 v[26:27], v[8:9], v[10:11]
	v_pk_add_f32 v[28:29], v[20:21], v[22:23]
	v_pk_add_f32 v[30:31], v[12:13], v[14:15]
	v_pk_mul_f32 v[10:11], v[10:11], v[10:11]
	v_pk_mul_f32 v[18:19], v[18:19], v[18:19]
	v_pk_mul_f32 v[14:15], v[14:15], v[14:15]
	v_pk_mul_f32 v[22:23], v[22:23], v[22:23]
	v_pk_add_f32 v[26:27], v[26:27], v[30:31]
	v_pk_add_f32 v[24:25], v[24:25], v[28:29]
	v_pk_fma_f32 v[16:17], v[16:17], v[16:17], v[18:19]
	v_pk_fma_f32 v[8:9], v[8:9], v[8:9], v[10:11]
	v_pk_fma_f32 v[10:11], v[20:21], v[20:21], v[22:23]
	v_pk_fma_f32 v[12:13], v[12:13], v[12:13], v[14:15]
	v_pk_add_f32 v[10:11], v[16:17], v[10:11]
	v_pk_add_f32 v[8:9], v[8:9], v[12:13]
	v_add_f32_e32 v1, v24, v25
	v_add_f32_e32 v3, v26, v27
	v_add_f32_e32 v1, v1, v3
	v_add_f32_e32 v3, v10, v11
	v_add_f32_e32 v7, v8, v9
	v_add_f32_e32 v3, v3, v7
	v_add_f32_dpp v1, v1, v1 quad_perm:[1,0,3,2] row_mask:0xf bank_mask:0xf bound_ctrl:1
	s_nop 0
	v_add_f32_dpp v3, v3, v3 quad_perm:[1,0,3,2] row_mask:0xf bank_mask:0xf bound_ctrl:1
	v_add_f32_dpp v1, v1, v1 quad_perm:[2,3,0,1] row_mask:0xf bank_mask:0xf bound_ctrl:1
	s_nop 0
	v_add_f32_dpp v3, v3, v3 quad_perm:[2,3,0,1] row_mask:0xf bank_mask:0xf bound_ctrl:1
	v_add_f32_dpp v1, v1, v1 row_half_mirror row_mask:0xf bank_mask:0xf bound_ctrl:1
	s_nop 0
	v_add_f32_dpp v3, v3, v3 row_half_mirror row_mask:0xf bank_mask:0xf bound_ctrl:1
	v_add_f32_dpp v1, v1, v1 row_mirror row_mask:0xf bank_mask:0xf bound_ctrl:1
	v_mov_b32_e32 v7, v1
	v_add_f32_dpp v8, v3, v3 row_mirror row_mask:0xf bank_mask:0xf bound_ctrl:1
	v_mov_b32_e32 v9, v8
	v_permlane16_swap_b32_e32 v1, v7
	s_nop 0
	v_permlane16_swap_b32_e32 v8, v9
	v_add_f32_e32 v1, v1, v7
	v_add_f32_e32 v7, v8, v9
	v_mov_b32_e32 v3, v1
	v_mov_b32_e32 v8, v7
	s_nop 0
	v_permlane32_swap_b32_e32 v1, v3
	v_permlane32_swap_b32_e32 v7, v8
	s_and_saveexec_b64 s[22:23], s[42:43]
	s_cbranch_execz .Lgm_u1_st14
; __device__ __forceinline__ void unpk8(const u32x4 w, f32x4& a, f32x4& b) { a = (f32x4){bflo(w.x), bfhi(w.x), bflo(w.y), bfhi(w.y)}; b = (f32x4){bflo(w.z), bfhi(w.z), bflo(w.w), bfhi(w.w)}; }
; __device__ __forceinline__ void gmlp_unit(Frame& F, const Args& a, int layer, int unit) {
;     ...
;     for (int r = 0; r < 16; ++r) { const int tok = wave * 16 + r; const bf16* rowp = GUV + (t0 + tok) * 2048 + 1024;
;         f32x4 x0, x1, x2, x3; unpk8(*(const v4u*)(rowp + lane * 8), x0, x1); unpk8(*(const v4u*)(rowp + 512 + lane * 8), x2, x3);
;         const f32x4 sv = (x0 + x1) + (x2 + x3), qv = (x0 * x0 + x1 * x1) + (x2 * x2 + x3 * x3);
;         const float s = wave_sum((sv.x + sv.y) + (sv.z + sv.w)), q = wave_sum((qv.x + qv.y) + (qv.z + qv.w));
;         const float mean = s * (1.f / 1024.f), var = fmaxf(q * (1.f / 1024.f) - mean * mean, 0.f);
;         if (lane == 0) { st[tok * 2] = mean; st[tok * 2 + 1] = 1.f / sqrtf(var + 1e-5f); } }
	v_add_f32_e32 v1, v1, v3
	v_add_f32_e32 v7, v7, v8
	v_mul_f32_e32 v8, 0x3a800000, v1
	v_mul_f32_e32 v1, v8, v8
	v_fma_f32 v1, v7, s13, -v1
	v_max_f32_e32 v1, 0, v1
	v_add_f32_e32 v1, 0x3727c5ac, v1
	v_mul_f32_e32 v3, 0x4f800000, v1
	v_cmp_gt_f32_e32 vcc, s69, v1
	s_add_i32 s21, s11, s3
	s_nop 0
	v_cndmask_b32_e32 v1, v1, v3, vcc
	v_sqrt_f32_e32 v3, v1
	s_nop 0
	v_add_u32_e32 v7, -1, v3
	v_fma_f32 v9, -v7, v3, v1
	v_cmp_ge_f32_e64 s[44:45], 0, v9
	v_add_u32_e32 v9, 1, v3
	s_nop 0
	v_cndmask_b32_e64 v7, v3, v7, s[44:45]
	v_fma_f32 v3, -v9, v3, v1
	v_cmp_lt_f32_e64 s[44:45], 0, v3
	s_nop 1
	v_cndmask_b32_e64 v3, v7, v9, s[44:45]
	v_mul_f32_e32 v7, 0x37800000, v3
	v_cndmask_b32_e32 v3, v3, v7, vcc
	v_cmp_class_f32_e32 vcc, v1, v242
	s_nop 1
	v_cndmask_b32_e32 v1, v3, v1, vcc
	v_div_scale_f32 v3, s[38:39], v1, v1, 1.0
	v_rcp_f32_e32 v7, v3
	s_nop 0
	v_fma_f32 v9, -v3, v7, 1.0
	v_fmac_f32_e32 v7, v9, v7
	v_div_scale_f32 v9, vcc, 1.0, v1, 1.0
	v_mul_f32_e32 v10, v9, v7
	v_fma_f32 v11, -v3, v10, v9
	v_fmac_f32_e32 v10, v11, v7
	v_fma_f32 v3, -v3, v10, v9
	v_div_fmas_f32 v3, v3, v7, v10
	v_div_fixup_f32 v9, v3, v1, 1.0
	v_mov_b32_e32 v1, s21
	ds_write_b64 v1, v[8:9]
.Lgm_u1_st14:
	s_or_b64 exec, exec, s[22:23]
	s_add_i32 s3, s3, 8
	s_waitcnt vmcnt(0)
	v_lshlrev_b32_e32 v16, 16, v156
	v_and_b32_e32 v17, 0xffff0000, v156
	v_lshlrev_b32_e32 v8, 16, v157
	v_and_b32_e32 v9, 0xffff0000, v157
	v_lshlrev_b32_e32 v18, 16, v158
	v_and_b32_e32 v19, 0xffff0000, v158
	v_lshlrev_b32_e32 v10, 16, v159
	v_and_b32_e32 v11, 0xffff0000, v159
	v_lshlrev_b32_e32 v20, 16, v160
	v_and_b32_e32 v21, 0xffff0000, v160
	v_lshlrev_b32_e32 v12, 16, v161
	v_and_b32_e32 v13, 0xffff0000, v161
	v_lshlrev_b32_e32 v22, 16, v162
	v_and_b32_e32 v23, 0xffff0000, v162
	v_lshlrev_b32_e32 v14, 16, v163
	v_and_b32_e32 v15, 0xffff0000, v163
	v_pk_add_f32 v[24:25], v[16:17], v[18:19]
	v_pk_add_f32 v[26:27], v[8:9], v[10:11]
	v_pk_add_f32 v[28:29], v[20:21], v[22:23]
	v_pk_add_f32 v[30:31], v[12:13], v[14:15]
	v_pk_mul_f32 v[10:11], v[10:11], v[10:11]
	v_pk_mul_f32 v[18:19], v[18:19], v[18:19]
	v_pk_mul_f32 v[14:15], v[14:15], v[14:15]
	v_pk_mul_f32 v[22:23], v[22:23], v[22:23]
	v_pk_add_f32 v[26:27], v[26:27], v[30:31]
	v_pk_add_f32 v[24:25], v[24:25], v[28:29]
	v_pk_fma_f32 v[16:17], v[16:17], v[16:17], v[18:19]
	v_pk_fma_f32 v[8:9], v[8:9], v[8:9], v[10:11]
	v_pk_fma_f32 v[10:11], v[20:21], v[20:21], v[22:23]
	v_pk_fma_f32 v[12:13], v[12:13], v[12:13], v[14:15]
	v_pk_add_f32 v[10:11], v[16:17], v[10:11]
	v_pk_add_f32 v[8:9], v[8:9], v[12:13]
	v_add_f32_e32 v1, v24, v25
	v_add_f32_e32 v3, v26, v27
	v_add_f32_e32 v1, v1, v3
	v_add_f32_e32 v3, v10, v11
	v_add_f32_e32 v7, v8, v9
	v_add_f32_e32 v3, v3, v7
	v_add_f32_dpp v1, v1, v1 quad_perm:[1,0,3,2] row_mask:0xf bank_mask:0xf bound_ctrl:1
	s_nop 0
	v_add_f32_dpp v3, v3, v3 quad_perm:[1,0,3,2] row_mask:0xf bank_mask:0xf bound_ctrl:1
	v_add_f32_dpp v1, v1, v1 quad_perm:[2,3,0,1] row_mask:0xf bank_mask:0xf bound_ctrl:1
	s_nop 0
	v_add_f32_dpp v3, v3, v3 quad_perm:[2,3,0,1] row_mask:0xf bank_mask:0xf bound_ctrl:1
	v_add_f32_dpp v1, v1, v1 row_half_mirror row_mask:0xf bank_mask:0xf bound_ctrl:1
	s_nop 0
	v_add_f32_dpp v3, v3, v3 row_half_mirror row_mask:0xf bank_mask:0xf bound_ctrl:1
	v_add_f32_dpp v1, v1, v1 row_mirror row_mask:0xf bank_mask:0xf bound_ctrl:1
	v_mov_b32_e32 v7, v1
	v_add_f32_dpp v8, v3, v3 row_mirror row_mask:0xf bank_mask:0xf bound_ctrl:1
	v_mov_b32_e32 v9, v8
	v_permlane16_swap_b32_e32 v1, v7
	s_nop 0
	v_permlane16_swap_b32_e32 v8, v9
	v_add_f32_e32 v1, v1, v7
	v_add_f32_e32 v7, v8, v9
	v_mov_b32_e32 v3, v1
	v_mov_b32_e32 v8, v7
	s_nop 0
	v_permlane32_swap_b32_e32 v1, v3
	v_permlane32_swap_b32_e32 v7, v8
	s_and_saveexec_b64 s[22:23], s[42:43]
	s_cbranch_execz .Lgm_u1_st15
	v_add_f32_e32 v1, v1, v3
	v_add_f32_e32 v7, v7, v8
	v_mul_f32_e32 v8, 0x3a800000, v1
	v_mul_f32_e32 v1, v8, v8
	v_fma_f32 v1, v7, s13, -v1
	v_max_f32_e32 v1, 0, v1
	v_add_f32_e32 v1, 0x3727c5ac, v1
	v_mul_f32_e32 v3, 0x4f800000, v1
	v_cmp_gt_f32_e32 vcc, s69, v1
	s_add_i32 s21, s11, s3
	s_nop 0
	v_cndmask_b32_e32 v1, v1, v3, vcc
	v_sqrt_f32_e32 v3, v1
	s_nop 0
	v_add_u32_e32 v7, -1, v3
	v_fma_f32 v9, -v7, v3, v1
	v_cmp_ge_f32_e64 s[44:45], 0, v9
	v_add_u32_e32 v9, 1, v3
	s_nop 0
	v_cndmask_b32_e64 v7, v3, v7, s[44:45]
	v_fma_f32 v3, -v9, v3, v1
	v_cmp_lt_f32_e64 s[44:45], 0, v3
	s_nop 1
	v_cndmask_b32_e64 v3, v7, v9, s[44:45]
	v_mul_f32_e32 v7, 0x37800000, v3
	v_cndmask_b32_e32 v3, v3, v7, vcc
	v_cmp_class_f32_e32 vcc, v1, v242
	s_nop 1
	v_cndmask_b32_e32 v1, v3, v1, vcc
	v_div_scale_f32 v3, s[38:39], v1, v1, 1.0
	v_rcp_f32_e32 v7, v3
	s_nop 0
	v_fma_f32 v9, -v3, v7, 1.0
	v_fmac_f32_e32 v7, v9, v7
	v_div_scale_f32 v9, vcc, 1.0, v1, 1.0
	v_mul_f32_e32 v10, v9, v7
	v_fma_f32 v11, -v3, v10, v9
	v_fmac_f32_e32 v10, v11, v7
	v_fma_f32 v3, -v3, v10, v9
	v_div_fmas_f32 v3, v3, v7, v10
	v_div_fixup_f32 v9, v3, v1, 1.0
	v_mov_b32_e32 v1, s21
	ds_write_b64 v1, v[8:9]
.Lgm_u1_st15:
	s_or_b64 exec, exec, s[22:23]
	s_add_i32 s3, s3, 8
; __device__ __forceinline__ void gmlp_unit(Frame& F, const Args& a, int layer, int unit) {
;     ...
;     const size_t t0 = (size_t)unit * 128; const int tid = F.tid, lane = F.lane, wave = F.wave;
;     LAS float* st = (LAS float*)F.lds; LAS bf16* sA = (LAS bf16*)(F.lds + 1024); LAS bf16* sB = (LAS bf16*)(F.lds + 1024 + 128 * TP * 2);
;     bf16* GUV = (bf16*)(F.ws + WS_GUV); const bf16* GMW = (const bf16*)(F.ws + WS_DB + (size_t)(layer & 1) * DB_SET + DB_GMW);
;     const float* lng = a.in[19] + (size_t)layer * 1024; const float* lnb = a.in[20] + (size_t)layer * 1024; const float* bsp = a.in[22] + (size_t)layer * 1024;
;     for (int r = 0; r < 16; ++r) { const int tok = wave * 16 + r; const bf16* rowp = GUV + (t0 + tok) * 2048 + 1024;
;         f32x4 x0, x1, x2, x3; unpk8(*(const v4u*)(rowp + lane * 8), x0, x1); unpk8(*(const v4u*)(rowp + 512 + lane * 8), x2, x3);
;         const f32x4 sv = (x0 + x1) + (x2 + x3), qv = (x0 * x0 + x1 * x1) + (x2 * x2 + x3 * x3);
;         const float s = wave_sum((sv.x + sv.y) + (sv.z + sv.w)), q = wave_sum((qv.x + qv.y) + (qv.z + qv.w));
;         const float mean = s * (1.f / 1024.f), var = fmaxf(q * (1.f / 1024.f) - mean * mean, 0.f);
;         if (lane == 0) { st[tok * 2] = mean; st[tok * 2 + 1] = 1.f / sqrtf(var + 1e-5f); } }
;     __syncthreads();
;     for (int g = 0; g < 8; ++g) {
; #pragma unroll
;         for (int i = 0; i < 4; ++i) { const int pc = tid + 512 * i, rr = pc >> 4, c16 = pc & 15;
;             *(LAS v4u*)(sA + rr * TP + c16 * 8) = *(const v4u*)(GMW + (size_t)g * 16384 + rr * 128 + c16 * 8); }
;         { const int p = tid & 127, oc0 = tid >> 7; const float mean = st[p * 2], rstd = st[p * 2 + 1];
; #pragma unroll
;           for (int i = 0; i < 4; ++i) { const int oc = oc0 + 4 * i, c0 = g * 128 + oc * 8;
;               f32x4 x0, x1; unpk8(*(const v4u*)(GUV + (t0 + p) * 2048 + 1024 + c0), x0, x1);
;               const f32x4 g0 = *(const f32x4*)(lng + c0), g1 = *(const f32x4*)(lng + c0 + 4), b0 = *(const f32x4*)(lnb + c0), b1 = *(const f32x4*)(lnb + c0 + 4);
;     ...
;           for (int mt = 0; mt < 4; ++mt) { const int tt = 64 * wm + 16 * mt + fr; const float bsv = bsp[g * 128 + tt];
; #pragma unroll
;               for (int nt = 0; nt < 2; ++nt) { const int c = g * 128 + 32 * wn + 16 * nt + 4 * fq;
;                   const v2u uw = *(const v2u*)(GUV + (t0 + tt) * 2048 + c);
.LBB0_832:
	s_lshl_b32 s22, s5, 1
	v_and_b32_e32 v19, 15, v6
	v_and_b32_e32 v4, -16, v6
	s_ashr_i32 s23, s22, 31
	v_add_u32_e32 v3, s27, v6
	v_add_u32_e32 v20, 0, v4
	v_or_b32_e32 v7, s75, v19
	v_or_b32_e32 v4, s77, v19
	v_ashrrev_i32_e32 v6, 2, v6
	s_lshl_b64 s[38:39], s[22:23], 7
	v_mul_u32_u24_e32 v22, 0x110, v7
	v_and_b32_e32 v23, -4, v6
	v_or_b32_e32 v6, 48, v4
	v_mov_b32_e32 v7, v0
	s_add_u32 s42, s6, 0x28400000
	v_lshl_add_u64 v[6:7], s[38:39], 0, v[6:7]
	s_addc_u32 s43, s7, 0
	v_ashrrev_i32_e32 v5, 4, v3
	s_movk_i32 s3, 0x110
	v_lshlrev_b64 v[6:7], 12, v[6:7]
	v_and_b32_e32 v1, 0x78, v2
	v_and_b32_e32 v2, -8, v5
	v_lshl_add_u64 v[26:27], s[42:43], 0, v[6:7]
	v_lshlrev_b32_e32 v6, 7, v5
	v_mul_lo_u32 v24, v5, s3
	v_add_u32_e32 v5, 0x200, v3
	v_ashrrev_i32_e32 v5, 4, v5
	v_lshlrev_b32_e32 v8, 7, v5
	v_mul_lo_u32 v25, v5, s3
	v_add_u32_e32 v5, 0x400, v3
	v_ashrrev_i32_e32 v5, 4, v5
	v_lshlrev_b32_e32 v10, 7, v5
	v_mul_lo_u32 v41, v5, s3
	v_mov_b32_e32 v5, v0
	v_lshl_add_u64 v[14:15], s[38:39], 0, v[4:5]
	v_lshlrev_b64 v[14:15], 12, v[14:15]
	v_mul_lo_u32 v21, v4, s3
	v_lshl_add_u64 v[28:29], s[42:43], 0, v[14:15]
	v_or_b32_e32 v14, 16, v4
	v_or_b32_e32 v4, 32, v4
	v_mov_b32_e32 v15, v0
	v_lshl_add_u64 v[4:5], s[38:39], 0, v[4:5]
	v_lshl_add_u64 v[14:15], s[38:39], 0, v[14:15]
	v_lshlrev_b64 v[4:5], 12, v[4:5]
	v_lshlrev_b64 v[14:15], 12, v[14:15]
	v_lshl_add_u64 v[32:33], s[42:43], 0, v[4:5]
	v_lshlrev_b32_e32 v4, 4, v19
	v_mov_b32_e32 v5, v0
	v_ashrrev_i32_e32 v7, 31, v6
	v_lshl_add_u64 v[30:31], s[42:43], 0, v[14:15]
	v_lshl_add_u64 v[4:5], s[0:1], 0, v[4:5]
	v_readlane_b32 s40, v251, 34
	v_and_b32_e32 v17, 0x7f, v3
	v_add_u32_e32 v3, 0x600, v3
	v_lshl_add_u64 v[34:35], v[6:7], 1, v[4:5]
	v_add_u32_e32 v6, s77, v19
	v_mov_b32_e32 v7, v0
	v_readlane_b32 s52, v251, 46
	v_readlane_b32 s53, v251, 47
	s_add_u32 s36, s36, 0x28400880
	v_ashrrev_i32_e32 v3, 4, v3
	v_lshl_add_u64 v[38:39], v[6:7], 2, s[52:53]
	s_addc_u32 s37, s37, 0
	v_lshlrev_b32_e32 v6, 12, v17
	v_lshl_add_u32 v16, v1, 1, 0
	v_lshl_add_u32 v1, v17, 3, 0
	v_lshlrev_b32_e32 v12, 7, v3
	v_mul_lo_u32 v52, v3, s3
	v_lshl_add_u64 v[6:7], s[36:37], 0, v[6:7]
	v_ashrrev_i32_e32 v3, 31, v2
	v_mad_i32_i24 v18, v17, -6, v1
	v_ashrrev_i32_e32 v9, 31, v8
	v_ashrrev_i32_e32 v11, 31, v10
	v_ashrrev_i32_e32 v13, 31, v12
	v_mul_lo_u32 v53, v2, s3
	v_readlane_b32 s46, v251, 40
	v_readlane_b32 s47, v251, 41
	v_readlane_b32 s48, v251, 42
	v_readlane_b32 s49, v251, 43
	v_lshl_add_u64 v[44:45], v[2:3], 1, v[6:7]
	v_lshlrev_b64 v[2:3], 2, v[2:3]
	v_lshl_add_u64 v[36:37], v[8:9], 1, v[4:5]
	v_add_u32_e32 v40, s75, v23
	v_lshl_add_u64 v[42:43], v[10:11], 1, v[4:5]
	v_lshl_add_u64 v[46:47], v[12:13], 1, v[4:5]
	v_lshl_add_u64 v[48:49], s[48:49], 0, v[2:3]
	v_lshl_add_u64 v[50:51], s[46:47], 0, v[2:3]
	s_mov_b64 s[36:37], 0
	v_add_u32_e32 v56, v16, v24
	v_add_u32_e32 v57, v16, v25
	v_add_u32_e32 v58, v16, v41
	v_add_u32_e32 v59, v16, v52
	v_add_u32_e32 v60, v18, v53
	v_add_u32_e32 v61, v20, v21
	v_add_u32_e32 v62, v20, v22
	s_waitcnt lgkmcnt(0)
	s_barrier
	v_readlane_b32 s41, v251, 35
	v_readlane_b32 s42, v251, 36
	v_readlane_b32 s43, v251, 37
	v_readlane_b32 s44, v251, 38
	v_readlane_b32 s45, v251, 39
	v_readlane_b32 s50, v251, 44
	v_readlane_b32 s51, v251, 45
	v_readlane_b32 s54, v251, 48
	v_readlane_b32 s55, v251, 49
.LBB0_833:
	v_lshl_add_u64 v[2:3], s[6:7], 0, v[34:35]
	global_load_dwordx4 v[100:103], v[2:3], off
	v_lshl_add_u64 v[34:35], v[34:35], 0, s[34:35]
	v_lshl_add_u64 v[2:3], s[6:7], 0, v[36:37]
	global_load_dwordx4 v[104:107], v[2:3], off
	v_lshl_add_u64 v[36:37], v[36:37], 0, s[34:35]
	v_lshl_add_u64 v[2:3], s[6:7], 0, v[42:43]
	global_load_dwordx4 v[108:111], v[2:3], off
	v_lshl_add_u64 v[42:43], v[42:43], 0, s[34:35]
	v_lshl_add_u64 v[2:3], s[6:7], 0, v[46:47]
	global_load_dwordx4 v[112:115], v[2:3], off
	v_lshl_add_u64 v[46:47], v[46:47], 0, s[34:35]
	v_lshl_add_u64 v[4:5], s[6:7], 0, v[44:45]
	v_lshl_add_u64 v[8:9], v[50:51], 0, s[36:37]
	v_lshl_add_u64 v[6:7], v[48:49], 0, s[36:37]
	ds_read_b64 v[2:3], v1
	v_lshl_add_u64 v[44:45], v[44:45], 0, s[66:67]
	global_load_dwordx4 v[116:119], v[4:5], off offset:-128
	global_load_dwordx4 v[132:135], v[8:9], off
	global_load_dwordx4 v[136:139], v[8:9], off offset:16
	global_load_dwordx4 v[164:167], v[6:7], off
	global_load_dwordx4 v[168:171], v[6:7], off offset:16
	global_load_dwordx4 v[120:123], v[4:5], off offset:-64
	global_load_dwordx4 v[140:143], v[8:9], off offset:128
	global_load_dwordx4 v[144:147], v[8:9], off offset:144
	global_load_dwordx4 v[172:175], v[6:7], off offset:128
	global_load_dwordx4 v[176:179], v[6:7], off offset:144
	global_load_dwordx4 v[124:127], v[4:5], off
	global_load_dwordx4 v[148:151], v[8:9], off offset:256
	global_load_dwordx4 v[152:155], v[8:9], off offset:272
	global_load_dwordx4 v[180:183], v[6:7], off offset:256
	global_load_dwordx4 v[184:187], v[6:7], off offset:272
	global_load_dwordx4 v[128:131], v[4:5], off offset:64
	global_load_dwordx4 v[156:159], v[8:9], off offset:384
	global_load_dwordx4 v[160:163], v[8:9], off offset:400
	global_load_dwordx4 v[188:191], v[6:7], off offset:384
	global_load_dwordx4 v[192:195], v[6:7], off offset:400
	v_ashrrev_i32_e32 v41, 31, v40
	v_lshl_add_u64 v[54:55], v[38:39], 0, s[36:37]
	v_lshlrev_b64 v[52:53], 1, v[40:41]
	v_add_u32_e32 v40, 0x80, v40
	v_lshl_add_u64 v[232:233], v[28:29], 0, v[52:53]
	v_lshl_add_u64 v[234:235], v[30:31], 0, v[52:53]
	v_lshl_add_u64 v[236:237], v[32:33], 0, v[52:53]
	v_lshl_add_u64 v[238:239], v[26:27], 0, v[52:53]
	global_load_dword v196, v[54:55], off
	global_load_dwordx2 v[204:205], v[232:233], off
	global_load_dwordx2 v[206:207], v[232:233], off offset:32
	global_load_dword v198, v[54:55], off offset:64
	global_load_dwordx2 v[224:225], v[234:235], off
	global_load_dwordx2 v[226:227], v[234:235], off offset:32
	global_load_dword v200, v[54:55], off offset:128
	global_load_dwordx2 v[228:229], v[236:237], off
	global_load_dwordx2 v[230:231], v[236:237], off offset:32
	global_load_dword v202, v[54:55], off offset:192
	global_load_dwordx2 v[246:247], v[238:239], off
	global_load_dwordx2 v[248:249], v[238:239], off offset:32
	s_waitcnt vmcnt(35)
; __device__ __forceinline__ void unpk8(const u32x4 w, f32x4& a, f32x4& b) { a = (f32x4){bflo(w.x), bfhi(w.x), bflo(w.y), bfhi(w.y)}; b = (f32x4){bflo(w.z), bfhi(w.z), bflo(w.w), bfhi(w.w)}; }
; __device__ __forceinline__ u32x4 pk8(const f32x4 a, const f32x4 b) { u32x4 w; w.x = cvt_pk_bf16(a[0], a[1]); w.y = cvt_pk_bf16(a[2], a[3]); w.z = cvt_pk_bf16(b[0], b[1]); w.w = cvt_pk_bf16(b[2], b[3]); return w; }
; #define LAS __attribute__((address_space(3)))
; __device__ __forceinline__ void gmlp_unit(Frame& F, const Args& a, int layer, int unit) {
;     ...
;         for (int i = 0; i < 4; ++i) { const int pc = tid + 512 * i, rr = pc >> 4, c16 = pc & 15;
;             *(LAS v4u*)(sA + rr * TP + c16 * 8) = *(const v4u*)(GMW + (size_t)g * 16384 + rr * 128 + c16 * 8); }
;         { const int p = tid & 127, oc0 = tid >> 7; const float mean = st[p * 2], rstd = st[p * 2 + 1];
; #pragma unroll
;           for (int i = 0; i < 4; ++i) { const int oc = oc0 + 4 * i, c0 = g * 128 + oc * 8;
;               f32x4 x0, x1; unpk8(*(const v4u*)(GUV + (t0 + p) * 2048 + 1024 + c0), x0, x1);
;               const f32x4 g0 = *(const f32x4*)(lng + c0), g1 = *(const f32x4*)(lng + c0 + 4), b0 = *(const f32x4*)(lnb + c0), b1 = *(const f32x4*)(lnb + c0 + 4);
;               x0 = (x0 - mean) * rstd * g0 + b0; x1 = (x1 - mean) * rstd * g1 + b1;
;               const v4u w = pk8(x0, x1);
;               LAS bf16* d = sB + (oc * 8) * TP + p;
;               d[0 * TP] = (bf16)(w.x & 0xffffu); d[1 * TP] = (bf16)(w.x >> 16); d[2 * TP] = (bf16)(w.y & 0xffffu); d[3 * TP] = (bf16)(w.y >> 16);
;               d[4 * TP] = (bf16)(w.z & 0xffffu); d[5 * TP] = (bf16)(w.z >> 16); d[6 * TP] = (bf16)(w.w & 0xffffu); d[7 * TP] = (bf16)(w.w >> 16); } }
;         __syncthreads();
	ds_write_b128 v56, v[100:103] offset:1024
	s_waitcnt vmcnt(34)
	ds_write_b128 v57, v[104:107] offset:1024
	s_waitcnt vmcnt(33)
	ds_write_b128 v58, v[108:111] offset:1024
	s_waitcnt vmcnt(32)
	ds_write_b128 v59, v[112:115] offset:1024
	s_waitcnt lgkmcnt(4)
	s_waitcnt vmcnt(27)
	v_lshlrev_b32_e32 v41, 16, v116
	v_and_b32_e32 v54, 0xffff0000, v116
	v_lshlrev_b32_e32 v52, 16, v117
	v_and_b32_e32 v53, 0xffff0000, v117
	v_lshlrev_b32_e32 v63, 16, v118
	v_and_b32_e32 v64, 0xffff0000, v118
	v_lshlrev_b32_e32 v65, 16, v119
	v_and_b32_e32 v66, 0xffff0000, v119
	v_sub_f32_e32 v53, v53, v2
	v_sub_f32_e32 v52, v52, v2
	v_sub_f32_e32 v55, v54, v2
	v_sub_f32_e32 v54, v41, v2
	v_pk_mul_f32 v[52:53], v[2:3], v[52:53] op_sel:[1,0]
	v_pk_mul_f32 v[54:55], v[2:3], v[54:55] op_sel:[1,0]
	v_pk_fma_f32 v[134:135], v[134:135], v[52:53], v[166:167]
	v_sub_f32_e32 v167, v64, v2
	v_sub_f32_e32 v166, v63, v2
	v_pk_fma_f32 v[132:133], v[132:133], v[54:55], v[164:165]
	v_sub_f32_e32 v165, v66, v2
	v_sub_f32_e32 v164, v65, v2
	v_pk_mul_f32 v[166:167], v[2:3], v[166:167] op_sel:[1,0]
	v_pk_mul_f32 v[164:165], v[2:3], v[164:165] op_sel:[1,0]
	v_pk_fma_f32 v[136:137], v[136:137], v[166:167], v[168:169]
	v_cvt_pk_bf16_f32 v132, v132, v133
	v_pk_fma_f32 v[138:139], v[138:139], v[164:165], v[170:171]
	v_cvt_pk_bf16_f32 v133, v134, v135
	v_cvt_pk_bf16_f32 v136, v136, v137
	s_nop 0
	v_cvt_pk_bf16_f32 v137, v138, v139
	ds_write_b16 v60, v132 offset:35840
	ds_write_b16_d16_hi v60, v132 offset:36112
	ds_write_b16 v60, v133 offset:36384
	ds_write_b16_d16_hi v60, v133 offset:36656
	ds_write_b16 v60, v136 offset:36928
	ds_write_b16_d16_hi v60, v136 offset:37200
	ds_write_b16 v60, v137 offset:37472
	ds_write_b16_d16_hi v60, v137 offset:37744
	s_waitcnt vmcnt(22)
	v_lshlrev_b32_e32 v41, 16, v120
	v_and_b32_e32 v54, 0xffff0000, v120
	v_lshlrev_b32_e32 v52, 16, v121
	v_and_b32_e32 v53, 0xffff0000, v121
	v_lshlrev_b32_e32 v63, 16, v122
	v_and_b32_e32 v64, 0xffff0000, v122
	v_lshlrev_b32_e32 v65, 16, v123
	v_and_b32_e32 v66, 0xffff0000, v123
	v_sub_f32_e32 v53, v53, v2
	v_sub_f32_e32 v52, v52, v2
	v_sub_f32_e32 v55, v54, v2
	v_sub_f32_e32 v54, v41, v2
	v_pk_mul_f32 v[52:53], v[2:3], v[52:53] op_sel:[1,0]
	v_pk_mul_f32 v[54:55], v[2:3], v[54:55] op_sel:[1,0]
	v_pk_fma_f32 v[142:143], v[142:143], v[52:53], v[174:175]
	v_sub_f32_e32 v175, v64, v2
	v_sub_f32_e32 v174, v63, v2
	v_pk_fma_f32 v[140:141], v[140:141], v[54:55], v[172:173]
	v_sub_f32_e32 v173, v66, v2
	v_sub_f32_e32 v172, v65, v2
	v_pk_mul_f32 v[174:175], v[2:3], v[174:175] op_sel:[1,0]
	v_pk_mul_f32 v[172:173], v[2:3], v[172:173] op_sel:[1,0]
	v_pk_fma_f32 v[144:145], v[144:145], v[174:175], v[176:177]
	v_cvt_pk_bf16_f32 v140, v140, v141
	v_pk_fma_f32 v[146:147], v[146:147], v[172:173], v[178:179]
	v_cvt_pk_bf16_f32 v141, v142, v143
	v_cvt_pk_bf16_f32 v144, v144, v145
	s_nop 0
	v_cvt_pk_bf16_f32 v145, v146, v147
	ds_write_b16 v60, v140 offset:44544
	ds_write_b16_d16_hi v60, v140 offset:44816
	ds_write_b16 v60, v141 offset:45088
	ds_write_b16_d16_hi v60, v141 offset:45360
	ds_write_b16 v60, v144 offset:45632
	ds_write_b16_d16_hi v60, v144 offset:45904
	ds_write_b16 v60, v145 offset:46176
	ds_write_b16_d16_hi v60, v145 offset:46448
	s_waitcnt vmcnt(17)
	v_lshlrev_b32_e32 v41, 16, v124
	v_and_b32_e32 v54, 0xffff0000, v124
	v_lshlrev_b32_e32 v52, 16, v125
	v_and_b32_e32 v53, 0xffff0000, v125
	v_lshlrev_b32_e32 v63, 16, v126
	v_and_b32_e32 v64, 0xffff0000, v126
	v_lshlrev_b32_e32 v65, 16, v127
	v_and_b32_e32 v66, 0xffff0000, v127
	v_sub_f32_e32 v53, v53, v2
	v_sub_f32_e32 v52, v52, v2
	v_sub_f32_e32 v55, v54, v2
	v_sub_f32_e32 v54, v41, v2
	v_pk_mul_f32 v[52:53], v[2:3], v[52:53] op_sel:[1,0]
	v_pk_mul_f32 v[54:55], v[2:3], v[54:55] op_sel:[1,0]
	v_pk_fma_f32 v[150:151], v[150:151], v[52:53], v[182:183]
	v_sub_f32_e32 v183, v64, v2
	v_sub_f32_e32 v182, v63, v2
	v_pk_fma_f32 v[148:149], v[148:149], v[54:55], v[180:181]
	v_sub_f32_e32 v181, v66, v2
	v_sub_f32_e32 v180, v65, v2
	v_pk_mul_f32 v[182:183], v[2:3], v[182:183] op_sel:[1,0]
	v_pk_mul_f32 v[180:181], v[2:3], v[180:181] op_sel:[1,0]
	v_pk_fma_f32 v[152:153], v[152:153], v[182:183], v[184:185]
	v_cvt_pk_bf16_f32 v148, v148, v149
	v_pk_fma_f32 v[154:155], v[154:155], v[180:181], v[186:187]
	v_cvt_pk_bf16_f32 v149, v150, v151
	v_cvt_pk_bf16_f32 v152, v152, v153
	s_nop 0
	v_cvt_pk_bf16_f32 v153, v154, v155
	ds_write_b16 v60, v148 offset:53248
	ds_write_b16_d16_hi v60, v148 offset:53520
	ds_write_b16 v60, v149 offset:53792
	ds_write_b16_d16_hi v60, v149 offset:54064
	ds_write_b16 v60, v152 offset:54336
	ds_write_b16_d16_hi v60, v152 offset:54608
	ds_write_b16 v60, v153 offset:54880
	ds_write_b16_d16_hi v60, v153 offset:55152
	s_waitcnt vmcnt(12)
	v_lshlrev_b32_e32 v41, 16, v128
	v_and_b32_e32 v54, 0xffff0000, v128
	v_lshlrev_b32_e32 v52, 16, v129
	v_and_b32_e32 v53, 0xffff0000, v129
	v_lshlrev_b32_e32 v63, 16, v130
	v_and_b32_e32 v64, 0xffff0000, v130
	v_lshlrev_b32_e32 v65, 16, v131
	v_and_b32_e32 v66, 0xffff0000, v131
	v_sub_f32_e32 v53, v53, v2
	v_sub_f32_e32 v52, v52, v2
	v_sub_f32_e32 v55, v54, v2
	v_sub_f32_e32 v54, v41, v2
	v_pk_mul_f32 v[52:53], v[2:3], v[52:53] op_sel:[1,0]
	v_pk_mul_f32 v[54:55], v[2:3], v[54:55] op_sel:[1,0]
	v_pk_fma_f32 v[158:159], v[158:159], v[52:53], v[190:191]
	v_sub_f32_e32 v191, v64, v2
	v_sub_f32_e32 v190, v63, v2
	v_pk_fma_f32 v[156:157], v[156:157], v[54:55], v[188:189]
	v_sub_f32_e32 v189, v66, v2
	v_sub_f32_e32 v188, v65, v2
	v_pk_mul_f32 v[190:191], v[2:3], v[190:191] op_sel:[1,0]
	v_pk_mul_f32 v[188:189], v[2:3], v[188:189] op_sel:[1,0]
	v_pk_fma_f32 v[160:161], v[160:161], v[190:191], v[192:193]
	v_cvt_pk_bf16_f32 v156, v156, v157
	v_pk_fma_f32 v[162:163], v[162:163], v[188:189], v[194:195]
	v_cvt_pk_bf16_f32 v157, v158, v159
	v_cvt_pk_bf16_f32 v160, v160, v161
	s_nop 0
	v_cvt_pk_bf16_f32 v161, v162, v163
	ds_write_b16 v60, v156 offset:61952
	ds_write_b16_d16_hi v60, v156 offset:62224
	ds_write_b16 v60, v157 offset:62496
	ds_write_b16_d16_hi v60, v157 offset:62768
	ds_write_b16 v60, v160 offset:63040
	ds_write_b16_d16_hi v60, v160 offset:63312
	ds_write_b16 v60, v161 offset:63584
	ds_write_b16_d16_hi v60, v161 offset:63856
	s_waitcnt lgkmcnt(0)
	s_barrier
; __device__ __forceinline__ unsigned cvt_pk_bf16(float lo, float hi) { unsigned r; asm volatile("v_cvt_pk_bf16_f32 %0, %1, %2" : "=v"(r) : "v"(lo), "v"(hi)); return r; }
; #define LAS __attribute__((address_space(3)))
; __device__ __forceinline__ void mma_128(const LAS bf16* sA, const LAS bf16* sBt, int wave, int lane, f32x4 (&acc)[4][2]) {
;     ...
; #pragma unroll
;     for (int kk = 0; kk < 4; ++kk) {
;         bf16x8 af[4], bf_[2];
; #pragma unroll
;         for (int mt = 0; mt < 4; ++mt) af[mt] = *(const LAS bf16x8*)(sA + (64 * wm + 16 * mt + fr) * TP + 32 * kk + 8 * fq);
; #pragma unroll
;         for (int nt = 0; nt < 2; ++nt) bf_[nt] = *(const LAS bf16x8*)(sBt + (32 * wn + 16 * nt + fr) * TP + 32 * kk + 8 * fq);
; #pragma unroll
;         for (int mt = 0; mt < 4; ++mt)
; #pragma unroll
;             for (int nt = 0; nt < 2; ++nt) acc[mt][nt] = __builtin_amdgcn_mfma_f32_16x16x32_bf16(bf_[nt], af[mt], acc[mt][nt], 0, 0, 0);
;     }
; __device__ __forceinline__ void gmlp_unit(Frame& F, const Args& a, int layer, int unit) {
;     ...
;           for (int mt = 0; mt < 4; ++mt) { const int tt = 64 * wm + 16 * mt + fr; const float bsv = bsp[g * 128 + tt];
; #pragma unroll
;               for (int nt = 0; nt < 2; ++nt) { const int c = g * 128 + 32 * wn + 16 * nt + 4 * fq;
;                   const v2u uw = *(const v2u*)(GUV + (t0 + tt) * 2048 + c);
;                   const f32x4 u4 = (f32x4){bflo(uw.x), bfhi(uw.x), bflo(uw.y), bfhi(uw.y)};
;                   const f32x4 yb = u4 * (acc[mt][nt] + bsv);
;                   v2u ow; ow.x = cvt_pk_bf16(yb.x, yb.y); ow.y = cvt_pk_bf16(yb.z, yb.w);
;                   *(v2u*)(GUV + (t0 + tt) * 2048 + c) = ow; } } }
	ds_read_b128 v[2:5], v61 offset:1024
	ds_read_b128 v[6:9], v61 offset:5376
	ds_read_b128 v[10:13], v61 offset:9728
	ds_read_b128 v[14:17], v61 offset:14080
	ds_read_b128 v[18:21], v62 offset:35840
	ds_read_b128 v[22:25], v62 offset:40192
	ds_read_b128 v[84:87], v61 offset:1088
	ds_read_b128 v[88:91], v61 offset:5440
	ds_read_b128 v[92:95], v61 offset:9792
	ds_read_b128 v[96:99], v61 offset:14144
	ds_read_b128 v[76:79], v62 offset:35904
	ds_read_b128 v[80:83], v62 offset:40256
	s_waitcnt lgkmcnt(6)
	v_mfma_f32_16x16x32_bf16 v[100:103], v[18:21], v[2:5], 0
	v_mfma_f32_16x16x32_bf16 v[104:107], v[22:25], v[2:5], 0
	v_mfma_f32_16x16x32_bf16 v[108:111], v[18:21], v[6:9], 0
	v_mfma_f32_16x16x32_bf16 v[112:115], v[22:25], v[6:9], 0
	v_mfma_f32_16x16x32_bf16 v[116:119], v[18:21], v[10:13], 0
	v_mfma_f32_16x16x32_bf16 v[120:123], v[22:25], v[10:13], 0
	v_mfma_f32_16x16x32_bf16 v[124:127], v[18:21], v[14:17], 0
	v_mfma_f32_16x16x32_bf16 v[128:131], v[22:25], v[14:17], 0
	ds_read_b128 v[2:5], v61 offset:1152
	ds_read_b128 v[6:9], v61 offset:5504
	ds_read_b128 v[10:13], v61 offset:9856
	ds_read_b128 v[14:17], v61 offset:14208
	ds_read_b128 v[18:21], v62 offset:35968
	ds_read_b128 v[22:25], v62 offset:40320
	s_waitcnt lgkmcnt(6)
	v_mfma_f32_16x16x32_bf16 v[100:103], v[76:79], v[84:87], v[100:103]
	v_mfma_f32_16x16x32_bf16 v[104:107], v[80:83], v[84:87], v[104:107]
	v_mfma_f32_16x16x32_bf16 v[108:111], v[76:79], v[88:91], v[108:111]
	v_mfma_f32_16x16x32_bf16 v[112:115], v[80:83], v[88:91], v[112:115]
	v_mfma_f32_16x16x32_bf16 v[116:119], v[76:79], v[92:95], v[116:119]
	v_mfma_f32_16x16x32_bf16 v[120:123], v[80:83], v[92:95], v[120:123]
	v_mfma_f32_16x16x32_bf16 v[124:127], v[76:79], v[96:99], v[124:127]
	v_mfma_f32_16x16x32_bf16 v[128:131], v[80:83], v[96:99], v[128:131]
	ds_read_b128 v[84:87], v61 offset:1216
	ds_read_b128 v[88:91], v61 offset:5568
	ds_read_b128 v[92:95], v61 offset:9920
	ds_read_b128 v[96:99], v61 offset:14272
	ds_read_b128 v[76:79], v62 offset:36032
	ds_read_b128 v[80:83], v62 offset:40384
	s_waitcnt lgkmcnt(6)
	v_mfma_f32_16x16x32_bf16 v[100:103], v[18:21], v[2:5], v[100:103]
	v_mfma_f32_16x16x32_bf16 v[104:107], v[22:25], v[2:5], v[104:107]
	v_mfma_f32_16x16x32_bf16 v[108:111], v[18:21], v[6:9], v[108:111]
	v_mfma_f32_16x16x32_bf16 v[112:115], v[22:25], v[6:9], v[112:115]
	v_mfma_f32_16x16x32_bf16 v[116:119], v[18:21], v[10:13], v[116:119]
	v_mfma_f32_16x16x32_bf16 v[120:123], v[22:25], v[10:13], v[120:123]
	v_mfma_f32_16x16x32_bf16 v[124:127], v[18:21], v[14:17], v[124:127]
	v_mfma_f32_16x16x32_bf16 v[128:131], v[22:25], v[14:17], v[128:131]
	s_waitcnt lgkmcnt(0)
	v_mfma_f32_16x16x32_bf16 v[100:103], v[76:79], v[84:87], v[100:103]
	v_mfma_f32_16x16x32_bf16 v[104:107], v[80:83], v[84:87], v[104:107]
	v_mfma_f32_16x16x32_bf16 v[108:111], v[76:79], v[88:91], v[108:111]
	v_mfma_f32_16x16x32_bf16 v[112:115], v[80:83], v[88:91], v[112:115]
	v_mfma_f32_16x16x32_bf16 v[116:119], v[76:79], v[92:95], v[116:119]
	v_mfma_f32_16x16x32_bf16 v[120:123], v[80:83], v[92:95], v[120:123]
	v_mfma_f32_16x16x32_bf16 v[124:127], v[76:79], v[96:99], v[124:127]
	v_mfma_f32_16x16x32_bf16 v[128:131], v[80:83], v[96:99], v[128:131]
	s_nop 7
	s_nop 1
	s_waitcnt vmcnt(9)
	v_lshlrev_b32_e32 v70, 16, v204
	v_and_b32_e32 v71, 0xffff0000, v204
	v_lshlrev_b32_e32 v68, 16, v205
	v_and_b32_e32 v69, 0xffff0000, v205
	v_pk_add_f32 v[72:73], v[102:103], v[196:197] op_sel_hi:[1,0]
	v_pk_add_f32 v[74:75], v[100:101], v[196:197] op_sel_hi:[1,0]
	v_pk_mul_f32 v[68:69], v[72:73], v[68:69]
	v_pk_mul_f32 v[70:71], v[74:75], v[70:71]
	v_cvt_pk_bf16_f32 v70, v70, v71
	v_cvt_pk_bf16_f32 v71, v68, v69
	global_store_dwordx2 v[232:233], v[70:71], off
	v_lshlrev_b32_e32 v16, 16, v206
	v_and_b32_e32 v17, 0xffff0000, v206
	v_lshlrev_b32_e32 v18, 16, v207
	v_and_b32_e32 v19, 0xffff0000, v207
	v_pk_add_f32 v[20:21], v[104:105], v[196:197] op_sel_hi:[1,0]
	v_pk_add_f32 v[22:23], v[106:107], v[196:197] op_sel_hi:[1,0]
	v_pk_mul_f32 v[20:21], v[20:21], v[16:17]
	v_pk_mul_f32 v[22:23], v[22:23], v[18:19]
	v_cvt_pk_bf16_f32 v20, v20, v21
	s_nop 0
	v_cvt_pk_bf16_f32 v21, v22, v23
	global_store_dwordx2 v[232:233], v[20:21], off offset:32
	s_waitcnt vmcnt(8)
	v_lshlrev_b32_e32 v70, 16, v224
	v_and_b32_e32 v71, 0xffff0000, v224
	v_lshlrev_b32_e32 v68, 16, v225
	v_and_b32_e32 v69, 0xffff0000, v225
	v_pk_add_f32 v[72:73], v[110:111], v[198:199] op_sel_hi:[1,0]
	v_pk_add_f32 v[74:75], v[108:109], v[198:199] op_sel_hi:[1,0]
	v_pk_mul_f32 v[68:69], v[72:73], v[68:69]
	v_pk_mul_f32 v[70:71], v[74:75], v[70:71]
	v_cvt_pk_bf16_f32 v70, v70, v71
	v_cvt_pk_bf16_f32 v71, v68, v69
	global_store_dwordx2 v[234:235], v[70:71], off
	v_lshlrev_b32_e32 v16, 16, v226
	v_and_b32_e32 v17, 0xffff0000, v226
	v_lshlrev_b32_e32 v18, 16, v227
	v_and_b32_e32 v19, 0xffff0000, v227
	v_pk_add_f32 v[20:21], v[112:113], v[198:199] op_sel_hi:[1,0]
	v_pk_add_f32 v[22:23], v[114:115], v[198:199] op_sel_hi:[1,0]
	v_pk_mul_f32 v[20:21], v[20:21], v[16:17]
	v_pk_mul_f32 v[22:23], v[22:23], v[18:19]
	v_cvt_pk_bf16_f32 v20, v20, v21
	s_nop 0
	v_cvt_pk_bf16_f32 v21, v22, v23
	global_store_dwordx2 v[234:235], v[20:21], off offset:32
	s_waitcnt vmcnt(7)
	v_lshlrev_b32_e32 v70, 16, v228
	v_and_b32_e32 v71, 0xffff0000, v228
	v_lshlrev_b32_e32 v68, 16, v229
	v_and_b32_e32 v69, 0xffff0000, v229
	v_pk_add_f32 v[72:73], v[118:119], v[200:201] op_sel_hi:[1,0]
	v_pk_add_f32 v[74:75], v[116:117], v[200:201] op_sel_hi:[1,0]
	v_pk_mul_f32 v[68:69], v[72:73], v[68:69]
	v_pk_mul_f32 v[70:71], v[74:75], v[70:71]
	v_cvt_pk_bf16_f32 v70, v70, v71
	v_cvt_pk_bf16_f32 v71, v68, v69
	global_store_dwordx2 v[236:237], v[70:71], off
	v_lshlrev_b32_e32 v16, 16, v230
	v_and_b32_e32 v17, 0xffff0000, v230
	v_lshlrev_b32_e32 v18, 16, v231
	v_and_b32_e32 v19, 0xffff0000, v231
	v_pk_add_f32 v[20:21], v[120:121], v[200:201] op_sel_hi:[1,0]
	v_pk_add_f32 v[22:23], v[122:123], v[200:201] op_sel_hi:[1,0]
	v_pk_mul_f32 v[20:21], v[20:21], v[16:17]
	v_pk_mul_f32 v[22:23], v[22:23], v[18:19]
	v_cvt_pk_bf16_f32 v20, v20, v21
	s_nop 0
	v_cvt_pk_bf16_f32 v21, v22, v23
	global_store_dwordx2 v[236:237], v[20:21], off offset:32
	s_waitcnt vmcnt(6)
; __device__ __forceinline__ unsigned cvt_pk_bf16(float lo, float hi) { unsigned r; asm volatile("v_cvt_pk_bf16_f32 %0, %1, %2" : "=v"(r) : "v"(lo), "v"(hi)); return r; }
; __device__ __forceinline__ void unpk8(const u32x4 w, f32x4& a, f32x4& b) { a = (f32x4){bflo(w.x), bfhi(w.x), bflo(w.y), bfhi(w.y)}; b = (f32x4){bflo(w.z), bfhi(w.z), bflo(w.w), bfhi(w.w)}; }
; __device__ __forceinline__ void gmlp_unit(Frame& F, const Args& a, int layer, int unit) {
;     ...
;     for (int r = 0; r < 16; ++r) { const int tok = wave * 16 + r; const bf16* rowp = GUV + (t0 + tok) * 2048 + 1024;
;         f32x4 x0, x1, x2, x3; unpk8(*(const v4u*)(rowp + lane * 8), x0, x1); unpk8(*(const v4u*)(rowp + 512 + lane * 8), x2, x3);
;         const f32x4 sv = (x0 + x1) + (x2 + x3), qv = (x0 * x0 + x1 * x1) + (x2 * x2 + x3 * x3);
;         const float s = wave_sum((sv.x + sv.y) + (sv.z + sv.w)), q = wave_sum((qv.x + qv.y) + (qv.z + qv.w));
;         const float mean = s * (1.f / 1024.f), var = fmaxf(q * (1.f / 1024.f) - mean * mean, 0.f);
;         if (lane == 0) { st[tok * 2] = mean; st[tok * 2 + 1] = 1.f / sqrtf(var + 1e-5f); } }
;     ...
;           for (int mt = 0; mt < 4; ++mt) { const int tt = 64 * wm + 16 * mt + fr; const float bsv = bsp[g * 128 + tt];
; #pragma unroll
;               for (int nt = 0; nt < 2; ++nt) { const int c = g * 128 + 32 * wn + 16 * nt + 4 * fq;
;                   const v2u uw = *(const v2u*)(GUV + (t0 + tt) * 2048 + c);
;                   const f32x4 u4 = (f32x4){bflo(uw.x), bfhi(uw.x), bflo(uw.y), bfhi(uw.y)};
;                   const f32x4 yb = u4 * (acc[mt][nt] + bsv);
;                   v2u ow; ow.x = cvt_pk_bf16(yb.x, yb.y); ow.y = cvt_pk_bf16(yb.z, yb.w);
;                   *(v2u*)(GUV + (t0 + tt) * 2048 + c) = ow; } } }
;         __syncthreads();
;     }
	v_lshlrev_b32_e32 v70, 16, v246
	v_and_b32_e32 v71, 0xffff0000, v246
	v_lshlrev_b32_e32 v68, 16, v247
	v_and_b32_e32 v69, 0xffff0000, v247
	v_pk_add_f32 v[72:73], v[126:127], v[202:203] op_sel_hi:[1,0]
	v_pk_add_f32 v[74:75], v[124:125], v[202:203] op_sel_hi:[1,0]
	v_pk_mul_f32 v[68:69], v[72:73], v[68:69]
	v_pk_mul_f32 v[70:71], v[74:75], v[70:71]
	v_cvt_pk_bf16_f32 v70, v70, v71
	v_cvt_pk_bf16_f32 v71, v68, v69
	global_store_dwordx2 v[238:239], v[70:71], off
	v_lshlrev_b32_e32 v16, 16, v248
	v_and_b32_e32 v17, 0xffff0000, v248
	v_lshlrev_b32_e32 v18, 16, v249
	v_and_b32_e32 v19, 0xffff0000, v249
	v_pk_add_f32 v[20:21], v[128:129], v[202:203] op_sel_hi:[1,0]
	v_pk_add_f32 v[22:23], v[130:131], v[202:203] op_sel_hi:[1,0]
	v_pk_mul_f32 v[20:21], v[20:21], v[16:17]
	v_pk_mul_f32 v[22:23], v[22:23], v[18:19]
	v_cvt_pk_bf16_f32 v20, v20, v21
	s_nop 0
	v_cvt_pk_bf16_f32 v21, v22, v23
	global_store_dwordx2 v[238:239], v[20:21], off offset:32
	s_add_u32 s36, s36, 0x200
	s_addc_u32 s37, s37, 0
	s_cmpk_lg_i32 s36, 0x1000
	s_barrier
	s_cbranch_scc1 .LBB0_833
	s_ashr_i32 s3, s2, 31
	s_lshl_b64 s[36:37], s[2:3], 19
	v_readlane_b32 s21, v254, 19
	v_mbcnt_lo_u32_b32 v6, -1, 0
	v_mbcnt_hi_u32_b32 v6, -1, v6
	s_add_u32 s21, s6, s21
	v_readlane_b32 s23, v254, 20
	s_addc_u32 s23, s7, s23
	v_lshlrev_b32_e32 v2, 3, v6
	s_add_u32 s38, s21, s36
	v_ashrrev_i32_e32 v3, 31, v2
	s_addc_u32 s39, s23, s37
	s_mov_b32 s3, 0
	v_cmp_eq_u32_e64 s[42:43], 0, v6
	v_lshl_add_u64 v[4:5], v[2:3], 1, s[38:39]
	global_load_dwordx4 v[32:35], v[4:5], off
	global_load_dwordx4 v[36:39], v[4:5], off offset:1024
	v_lshl_add_u64 v[4:5], v[4:5], 0, s[78:79]
	global_load_dwordx4 v[40:43], v[4:5], off
	global_load_dwordx4 v[44:47], v[4:5], off offset:1024
	v_lshl_add_u64 v[4:5], v[4:5], 0, s[78:79]
	global_load_dwordx4 v[48:51], v[4:5], off
	global_load_dwordx4 v[52:55], v[4:5], off offset:1024
	v_lshl_add_u64 v[4:5], v[4:5], 0, s[78:79]
	global_load_dwordx4 v[56:59], v[4:5], off
	global_load_dwordx4 v[60:63], v[4:5], off offset:1024
	v_lshl_add_u64 v[4:5], v[4:5], 0, s[78:79]
	global_load_dwordx4 v[64:67], v[4:5], off
	global_load_dwordx4 v[68:71], v[4:5], off offset:1024
	v_lshl_add_u64 v[4:5], v[4:5], 0, s[78:79]
	global_load_dwordx4 v[72:75], v[4:5], off
	global_load_dwordx4 v[76:79], v[4:5], off offset:1024
	v_lshl_add_u64 v[4:5], v[4:5], 0, s[78:79]
	global_load_dwordx4 v[80:83], v[4:5], off
	global_load_dwordx4 v[84:87], v[4:5], off offset:1024
	v_lshl_add_u64 v[4:5], v[4:5], 0, s[78:79]
	global_load_dwordx4 v[88:91], v[4:5], off
	global_load_dwordx4 v[92:95], v[4:5], off offset:1024
	v_lshl_add_u64 v[4:5], v[4:5], 0, s[78:79]
	global_load_dwordx4 v[100:103], v[4:5], off
	global_load_dwordx4 v[104:107], v[4:5], off offset:1024
	v_lshl_add_u64 v[4:5], v[4:5], 0, s[78:79]
	global_load_dwordx4 v[108:111], v[4:5], off
	global_load_dwordx4 v[112:115], v[4:5], off offset:1024
	v_lshl_add_u64 v[4:5], v[4:5], 0, s[78:79]
	global_load_dwordx4 v[116:119], v[4:5], off
	global_load_dwordx4 v[120:123], v[4:5], off offset:1024
	v_lshl_add_u64 v[4:5], v[4:5], 0, s[78:79]
	global_load_dwordx4 v[124:127], v[4:5], off
	global_load_dwordx4 v[128:131], v[4:5], off offset:1024
	v_lshl_add_u64 v[4:5], v[4:5], 0, s[78:79]
	global_load_dwordx4 v[132:135], v[4:5], off
	global_load_dwordx4 v[136:139], v[4:5], off offset:1024
	v_lshl_add_u64 v[4:5], v[4:5], 0, s[78:79]
	global_load_dwordx4 v[140:143], v[4:5], off
	global_load_dwordx4 v[144:147], v[4:5], off offset:1024
	v_lshl_add_u64 v[4:5], v[4:5], 0, s[78:79]
	global_load_dwordx4 v[148:151], v[4:5], off
	global_load_dwordx4 v[152:155], v[4:5], off offset:1024
	v_lshl_add_u64 v[4:5], v[4:5], 0, s[78:79]
	global_load_dwordx4 v[156:159], v[4:5], off
	global_load_dwordx4 v[160:163], v[4:5], off offset:1024
	v_lshl_add_u64 v[4:5], v[4:5], 0, s[78:79]
	s_waitcnt vmcnt(30)
	v_lshlrev_b32_e32 v16, 16, v32
	v_and_b32_e32 v17, 0xffff0000, v32
	v_lshlrev_b32_e32 v8, 16, v33
	v_and_b32_e32 v9, 0xffff0000, v33
	v_lshlrev_b32_e32 v18, 16, v34
	v_and_b32_e32 v19, 0xffff0000, v34
	v_lshlrev_b32_e32 v10, 16, v35
	v_and_b32_e32 v11, 0xffff0000, v35
	v_lshlrev_b32_e32 v20, 16, v36
	v_and_b32_e32 v21, 0xffff0000, v36
	v_lshlrev_b32_e32 v12, 16, v37
	v_and_b32_e32 v13, 0xffff0000, v37
	v_lshlrev_b32_e32 v22, 16, v38
	v_and_b32_e32 v23, 0xffff0000, v38
	v_lshlrev_b32_e32 v14, 16, v39
	v_and_b32_e32 v15, 0xffff0000, v39
	v_pk_add_f32 v[24:25], v[16:17], v[18:19]
	v_pk_add_f32 v[26:27], v[8:9], v[10:11]
	v_pk_add_f32 v[28:29], v[20:21], v[22:23]
	v_pk_add_f32 v[30:31], v[12:13], v[14:15]
	v_pk_mul_f32 v[10:11], v[10:11], v[10:11]
	v_pk_mul_f32 v[18:19], v[18:19], v[18:19]
	v_pk_mul_f32 v[14:15], v[14:15], v[14:15]
	v_pk_mul_f32 v[22:23], v[22:23], v[22:23]
	v_pk_add_f32 v[26:27], v[26:27], v[30:31]
	v_pk_add_f32 v[24:25], v[24:25], v[28:29]
	v_pk_fma_f32 v[16:17], v[16:17], v[16:17], v[18:19]
	v_pk_fma_f32 v[8:9], v[8:9], v[8:9], v[10:11]
	v_pk_fma_f32 v[10:11], v[20:21], v[20:21], v[22:23]
	v_pk_fma_f32 v[12:13], v[12:13], v[12:13], v[14:15]
	v_pk_add_f32 v[10:11], v[16:17], v[10:11]
	v_pk_add_f32 v[8:9], v[8:9], v[12:13]
	v_add_f32_e32 v1, v24, v25
	v_add_f32_e32 v3, v26, v27
	v_add_f32_e32 v1, v1, v3
	v_add_f32_e32 v3, v10, v11
	v_add_f32_e32 v7, v8, v9
	v_add_f32_e32 v3, v3, v7
	v_add_f32_dpp v1, v1, v1 quad_perm:[1,0,3,2] row_mask:0xf bank_mask:0xf bound_ctrl:1
	s_nop 0
	v_add_f32_dpp v3, v3, v3 quad_perm:[1,0,3,2] row_mask:0xf bank_mask:0xf bound_ctrl:1
	v_add_f32_dpp v1, v1, v1 quad_perm:[2,3,0,1] row_mask:0xf bank_mask:0xf bound_ctrl:1
	s_nop 0
	v_add_f32_dpp v3, v3, v3 quad_perm:[2,3,0,1] row_mask:0xf bank_mask:0xf bound_ctrl:1
	v_add_f32_dpp v1, v1, v1 row_half_mirror row_mask:0xf bank_mask:0xf bound_ctrl:1
	s_nop 0
	v_add_f32_dpp v3, v3, v3 row_half_mirror row_mask:0xf bank_mask:0xf bound_ctrl:1
	v_add_f32_dpp v1, v1, v1 row_mirror row_mask:0xf bank_mask:0xf bound_ctrl:1
	v_mov_b32_e32 v7, v1
	v_add_f32_dpp v8, v3, v3 row_mirror row_mask:0xf bank_mask:0xf bound_ctrl:1
	v_mov_b32_e32 v9, v8
	v_permlane16_swap_b32_e32 v1, v7
	s_nop 0
	v_permlane16_swap_b32_e32 v8, v9
	v_add_f32_e32 v1, v1, v7
	v_add_f32_e32 v7, v8, v9
	v_mov_b32_e32 v3, v1
	v_mov_b32_e32 v8, v7
	s_nop 0
	v_permlane32_swap_b32_e32 v1, v3
	v_permlane32_swap_b32_e32 v7, v8
	s_and_saveexec_b64 s[38:39], s[42:43]
	s_cbranch_execz .Lgm_u2_st0
; __device__ __forceinline__ void unpk8(const u32x4 w, f32x4& a, f32x4& b) { a = (f32x4){bflo(w.x), bfhi(w.x), bflo(w.y), bfhi(w.y)}; b = (f32x4){bflo(w.z), bfhi(w.z), bflo(w.w), bfhi(w.w)}; }
; __device__ __forceinline__ void gmlp_unit(Frame& F, const Args& a, int layer, int unit) {
;     ...
;     for (int r = 0; r < 16; ++r) { const int tok = wave * 16 + r; const bf16* rowp = GUV + (t0 + tok) * 2048 + 1024;
;         f32x4 x0, x1, x2, x3; unpk8(*(const v4u*)(rowp + lane * 8), x0, x1); unpk8(*(const v4u*)(rowp + 512 + lane * 8), x2, x3);
;         const f32x4 sv = (x0 + x1) + (x2 + x3), qv = (x0 * x0 + x1 * x1) + (x2 * x2 + x3 * x3);
;         const float s = wave_sum((sv.x + sv.y) + (sv.z + sv.w)), q = wave_sum((qv.x + qv.y) + (qv.z + qv.w));
;         const float mean = s * (1.f / 1024.f), var = fmaxf(q * (1.f / 1024.f) - mean * mean, 0.f);
;         if (lane == 0) { st[tok * 2] = mean; st[tok * 2 + 1] = 1.f / sqrtf(var + 1e-5f); } }
	v_add_f32_e32 v1, v1, v3
	v_add_f32_e32 v7, v7, v8
	v_mul_f32_e32 v8, 0x3a800000, v1
	v_mul_f32_e32 v1, v8, v8
	v_fma_f32 v1, v7, s13, -v1
	v_max_f32_e32 v1, 0, v1
	v_add_f32_e32 v1, 0x3727c5ac, v1
	v_mul_f32_e32 v3, 0x4f800000, v1
	v_cmp_gt_f32_e32 vcc, s69, v1
	s_add_i32 s21, s11, s3
	s_nop 0
	v_cndmask_b32_e32 v1, v1, v3, vcc
	v_sqrt_f32_e32 v3, v1
	s_nop 0
	v_add_u32_e32 v7, -1, v3
	v_fma_f32 v9, -v7, v3, v1
	v_cmp_ge_f32_e64 s[44:45], 0, v9
	v_add_u32_e32 v9, 1, v3
	s_nop 0
	v_cndmask_b32_e64 v7, v3, v7, s[44:45]
	v_fma_f32 v3, -v9, v3, v1
	v_cmp_lt_f32_e64 s[44:45], 0, v3
	s_nop 1
	v_cndmask_b32_e64 v3, v7, v9, s[44:45]
	v_mul_f32_e32 v7, 0x37800000, v3
	v_cndmask_b32_e32 v3, v3, v7, vcc
	v_cmp_class_f32_e32 vcc, v1, v242
	s_nop 1
	v_cndmask_b32_e32 v1, v3, v1, vcc
	v_div_scale_f32 v3, s[44:45], v1, v1, 1.0
	v_rcp_f32_e32 v7, v3
	s_nop 0
	v_fma_f32 v9, -v3, v7, 1.0
	v_fmac_f32_e32 v7, v9, v7
	v_div_scale_f32 v9, vcc, 1.0, v1, 1.0
	v_mul_f32_e32 v10, v9, v7
	v_fma_f32 v11, -v3, v10, v9
	v_fmac_f32_e32 v10, v11, v7
	v_fma_f32 v3, -v3, v10, v9
	v_div_fmas_f32 v3, v3, v7, v10
	v_div_fixup_f32 v9, v3, v1, 1.0
	v_mov_b32_e32 v1, s21
	ds_write_b64 v1, v[8:9]
.Lgm_u2_st0:
	s_or_b64 exec, exec, s[38:39]
	s_add_i32 s3, s3, 8
	s_waitcnt vmcnt(28)
	v_lshlrev_b32_e32 v16, 16, v40
	v_and_b32_e32 v17, 0xffff0000, v40
	v_lshlrev_b32_e32 v8, 16, v41
	v_and_b32_e32 v9, 0xffff0000, v41
	v_lshlrev_b32_e32 v18, 16, v42
	v_and_b32_e32 v19, 0xffff0000, v42
	v_lshlrev_b32_e32 v10, 16, v43
	v_and_b32_e32 v11, 0xffff0000, v43
	v_lshlrev_b32_e32 v20, 16, v44
	v_and_b32_e32 v21, 0xffff0000, v44
	v_lshlrev_b32_e32 v12, 16, v45
	v_and_b32_e32 v13, 0xffff0000, v45
	v_lshlrev_b32_e32 v22, 16, v46
	v_and_b32_e32 v23, 0xffff0000, v46
	v_lshlrev_b32_e32 v14, 16, v47
	v_and_b32_e32 v15, 0xffff0000, v47
	v_pk_add_f32 v[24:25], v[16:17], v[18:19]
	v_pk_add_f32 v[26:27], v[8:9], v[10:11]
	v_pk_add_f32 v[28:29], v[20:21], v[22:23]
	v_pk_add_f32 v[30:31], v[12:13], v[14:15]
	v_pk_mul_f32 v[10:11], v[10:11], v[10:11]
	v_pk_mul_f32 v[18:19], v[18:19], v[18:19]
	v_pk_mul_f32 v[14:15], v[14:15], v[14:15]
	v_pk_mul_f32 v[22:23], v[22:23], v[22:23]
	v_pk_add_f32 v[26:27], v[26:27], v[30:31]
	v_pk_add_f32 v[24:25], v[24:25], v[28:29]
	v_pk_fma_f32 v[16:17], v[16:17], v[16:17], v[18:19]
	v_pk_fma_f32 v[8:9], v[8:9], v[8:9], v[10:11]
	v_pk_fma_f32 v[10:11], v[20:21], v[20:21], v[22:23]
	v_pk_fma_f32 v[12:13], v[12:13], v[12:13], v[14:15]
	v_pk_add_f32 v[10:11], v[16:17], v[10:11]
	v_pk_add_f32 v[8:9], v[8:9], v[12:13]
	v_add_f32_e32 v1, v24, v25
	v_add_f32_e32 v3, v26, v27
	v_add_f32_e32 v1, v1, v3
	v_add_f32_e32 v3, v10, v11
	v_add_f32_e32 v7, v8, v9
	v_add_f32_e32 v3, v3, v7
	v_add_f32_dpp v1, v1, v1 quad_perm:[1,0,3,2] row_mask:0xf bank_mask:0xf bound_ctrl:1
	s_nop 0
	v_add_f32_dpp v3, v3, v3 quad_perm:[1,0,3,2] row_mask:0xf bank_mask:0xf bound_ctrl:1
	v_add_f32_dpp v1, v1, v1 quad_perm:[2,3,0,1] row_mask:0xf bank_mask:0xf bound_ctrl:1
	s_nop 0
	v_add_f32_dpp v3, v3, v3 quad_perm:[2,3,0,1] row_mask:0xf bank_mask:0xf bound_ctrl:1
	v_add_f32_dpp v1, v1, v1 row_half_mirror row_mask:0xf bank_mask:0xf bound_ctrl:1
	s_nop 0
	v_add_f32_dpp v3, v3, v3 row_half_mirror row_mask:0xf bank_mask:0xf bound_ctrl:1
	v_add_f32_dpp v1, v1, v1 row_mirror row_mask:0xf bank_mask:0xf bound_ctrl:1
	v_mov_b32_e32 v7, v1
	v_add_f32_dpp v8, v3, v3 row_mirror row_mask:0xf bank_mask:0xf bound_ctrl:1
	v_mov_b32_e32 v9, v8
	v_permlane16_swap_b32_e32 v1, v7
	s_nop 0
	v_permlane16_swap_b32_e32 v8, v9
	v_add_f32_e32 v1, v1, v7
	v_add_f32_e32 v7, v8, v9
	v_mov_b32_e32 v3, v1
	v_mov_b32_e32 v8, v7
	s_nop 0
	v_permlane32_swap_b32_e32 v1, v3
	v_permlane32_swap_b32_e32 v7, v8
	s_and_saveexec_b64 s[38:39], s[42:43]
	s_cbranch_execz .Lgm_u2_st1
	v_add_f32_e32 v1, v1, v3
	v_add_f32_e32 v7, v7, v8
	v_mul_f32_e32 v8, 0x3a800000, v1
	v_mul_f32_e32 v1, v8, v8
	v_fma_f32 v1, v7, s13, -v1
	v_max_f32_e32 v1, 0, v1
	v_add_f32_e32 v1, 0x3727c5ac, v1
	v_mul_f32_e32 v3, 0x4f800000, v1
	v_cmp_gt_f32_e32 vcc, s69, v1
	s_add_i32 s21, s11, s3
	s_nop 0
	v_cndmask_b32_e32 v1, v1, v3, vcc
	v_sqrt_f32_e32 v3, v1
	s_nop 0
	v_add_u32_e32 v7, -1, v3
	v_fma_f32 v9, -v7, v3, v1
	v_cmp_ge_f32_e64 s[44:45], 0, v9
	v_add_u32_e32 v9, 1, v3
	s_nop 0
	v_cndmask_b32_e64 v7, v3, v7, s[44:45]
	v_fma_f32 v3, -v9, v3, v1
	v_cmp_lt_f32_e64 s[44:45], 0, v3
	s_nop 1
	v_cndmask_b32_e64 v3, v7, v9, s[44:45]
	v_mul_f32_e32 v7, 0x37800000, v3
	v_cndmask_b32_e32 v3, v3, v7, vcc
	v_cmp_class_f32_e32 vcc, v1, v242
	s_nop 1
	v_cndmask_b32_e32 v1, v3, v1, vcc
	v_div_scale_f32 v3, s[44:45], v1, v1, 1.0
	v_rcp_f32_e32 v7, v3
	s_nop 0
	v_fma_f32 v9, -v3, v7, 1.0
	v_fmac_f32_e32 v7, v9, v7
	v_div_scale_f32 v9, vcc, 1.0, v1, 1.0
	v_mul_f32_e32 v10, v9, v7
	v_fma_f32 v11, -v3, v10, v9
	v_fmac_f32_e32 v10, v11, v7
	v_fma_f32 v3, -v3, v10, v9
	v_div_fmas_f32 v3, v3, v7, v10
	v_div_fixup_f32 v9, v3, v1, 1.0
	v_mov_b32_e32 v1, s21
	ds_write_b64 v1, v[8:9]
; __device__ __forceinline__ void unpk8(const u32x4 w, f32x4& a, f32x4& b) { a = (f32x4){bflo(w.x), bfhi(w.x), bflo(w.y), bfhi(w.y)}; b = (f32x4){bflo(w.z), bfhi(w.z), bflo(w.w), bfhi(w.w)}; }
; __device__ __forceinline__ void gmlp_unit(Frame& F, const Args& a, int layer, int unit) {
;     ...
;     for (int r = 0; r < 16; ++r) { const int tok = wave * 16 + r; const bf16* rowp = GUV + (t0 + tok) * 2048 + 1024;
;         f32x4 x0, x1, x2, x3; unpk8(*(const v4u*)(rowp + lane * 8), x0, x1); unpk8(*(const v4u*)(rowp + 512 + lane * 8), x2, x3);
;         const f32x4 sv = (x0 + x1) + (x2 + x3), qv = (x0 * x0 + x1 * x1) + (x2 * x2 + x3 * x3);
;         const float s = wave_sum((sv.x + sv.y) + (sv.z + sv.w)), q = wave_sum((qv.x + qv.y) + (qv.z + qv.w));
;         const float mean = s * (1.f / 1024.f), var = fmaxf(q * (1.f / 1024.f) - mean * mean, 0.f);
;         if (lane == 0) { st[tok * 2] = mean; st[tok * 2 + 1] = 1.f / sqrtf(var + 1e-5f); } }
.Lgm_u2_st1:
	s_or_b64 exec, exec, s[38:39]
	s_add_i32 s3, s3, 8
	s_waitcnt vmcnt(26)
	v_lshlrev_b32_e32 v16, 16, v48
	v_and_b32_e32 v17, 0xffff0000, v48
	v_lshlrev_b32_e32 v8, 16, v49
	v_and_b32_e32 v9, 0xffff0000, v49
	v_lshlrev_b32_e32 v18, 16, v50
	v_and_b32_e32 v19, 0xffff0000, v50
	v_lshlrev_b32_e32 v10, 16, v51
	v_and_b32_e32 v11, 0xffff0000, v51
	v_lshlrev_b32_e32 v20, 16, v52
	v_and_b32_e32 v21, 0xffff0000, v52
	v_lshlrev_b32_e32 v12, 16, v53
	v_and_b32_e32 v13, 0xffff0000, v53
	v_lshlrev_b32_e32 v22, 16, v54
	v_and_b32_e32 v23, 0xffff0000, v54
	v_lshlrev_b32_e32 v14, 16, v55
	v_and_b32_e32 v15, 0xffff0000, v55
	v_pk_add_f32 v[24:25], v[16:17], v[18:19]
	v_pk_add_f32 v[26:27], v[8:9], v[10:11]
	v_pk_add_f32 v[28:29], v[20:21], v[22:23]
	v_pk_add_f32 v[30:31], v[12:13], v[14:15]
	v_pk_mul_f32 v[10:11], v[10:11], v[10:11]
	v_pk_mul_f32 v[18:19], v[18:19], v[18:19]
	v_pk_mul_f32 v[14:15], v[14:15], v[14:15]
	v_pk_mul_f32 v[22:23], v[22:23], v[22:23]
	v_pk_add_f32 v[26:27], v[26:27], v[30:31]
	v_pk_add_f32 v[24:25], v[24:25], v[28:29]
	v_pk_fma_f32 v[16:17], v[16:17], v[16:17], v[18:19]
	v_pk_fma_f32 v[8:9], v[8:9], v[8:9], v[10:11]
	v_pk_fma_f32 v[10:11], v[20:21], v[20:21], v[22:23]
	v_pk_fma_f32 v[12:13], v[12:13], v[12:13], v[14:15]
	v_pk_add_f32 v[10:11], v[16:17], v[10:11]
	v_pk_add_f32 v[8:9], v[8:9], v[12:13]
	v_add_f32_e32 v1, v24, v25
	v_add_f32_e32 v3, v26, v27
	v_add_f32_e32 v1, v1, v3
	v_add_f32_e32 v3, v10, v11
	v_add_f32_e32 v7, v8, v9
	v_add_f32_e32 v3, v3, v7
	v_add_f32_dpp v1, v1, v1 quad_perm:[1,0,3,2] row_mask:0xf bank_mask:0xf bound_ctrl:1
	s_nop 0
	v_add_f32_dpp v3, v3, v3 quad_perm:[1,0,3,2] row_mask:0xf bank_mask:0xf bound_ctrl:1
	v_add_f32_dpp v1, v1, v1 quad_perm:[2,3,0,1] row_mask:0xf bank_mask:0xf bound_ctrl:1
	s_nop 0
	v_add_f32_dpp v3, v3, v3 quad_perm:[2,3,0,1] row_mask:0xf bank_mask:0xf bound_ctrl:1
	v_add_f32_dpp v1, v1, v1 row_half_mirror row_mask:0xf bank_mask:0xf bound_ctrl:1
	s_nop 0
	v_add_f32_dpp v3, v3, v3 row_half_mirror row_mask:0xf bank_mask:0xf bound_ctrl:1
	v_add_f32_dpp v1, v1, v1 row_mirror row_mask:0xf bank_mask:0xf bound_ctrl:1
	v_mov_b32_e32 v7, v1
	v_add_f32_dpp v8, v3, v3 row_mirror row_mask:0xf bank_mask:0xf bound_ctrl:1
	v_mov_b32_e32 v9, v8
	v_permlane16_swap_b32_e32 v1, v7
	s_nop 0
	v_permlane16_swap_b32_e32 v8, v9
	v_add_f32_e32 v1, v1, v7
	v_add_f32_e32 v7, v8, v9
	v_mov_b32_e32 v3, v1
	v_mov_b32_e32 v8, v7
	s_nop 0
	v_permlane32_swap_b32_e32 v1, v3
	v_permlane32_swap_b32_e32 v7, v8
	s_and_saveexec_b64 s[38:39], s[42:43]
	s_cbranch_execz .Lgm_u2_st2
	v_add_f32_e32 v1, v1, v3
	v_add_f32_e32 v7, v7, v8
	v_mul_f32_e32 v8, 0x3a800000, v1
	v_mul_f32_e32 v1, v8, v8
	v_fma_f32 v1, v7, s13, -v1
	v_max_f32_e32 v1, 0, v1
	v_add_f32_e32 v1, 0x3727c5ac, v1
	v_mul_f32_e32 v3, 0x4f800000, v1
	v_cmp_gt_f32_e32 vcc, s69, v1
	s_add_i32 s21, s11, s3
	s_nop 0
	v_cndmask_b32_e32 v1, v1, v3, vcc
	v_sqrt_f32_e32 v3, v1
	s_nop 0
	v_add_u32_e32 v7, -1, v3
	v_fma_f32 v9, -v7, v3, v1
	v_cmp_ge_f32_e64 s[44:45], 0, v9
	v_add_u32_e32 v9, 1, v3
	s_nop 0
	v_cndmask_b32_e64 v7, v3, v7, s[44:45]
	v_fma_f32 v3, -v9, v3, v1
	v_cmp_lt_f32_e64 s[44:45], 0, v3
	s_nop 1
	v_cndmask_b32_e64 v3, v7, v9, s[44:45]
	v_mul_f32_e32 v7, 0x37800000, v3
	v_cndmask_b32_e32 v3, v3, v7, vcc
	v_cmp_class_f32_e32 vcc, v1, v242
	s_nop 1
	v_cndmask_b32_e32 v1, v3, v1, vcc
	v_div_scale_f32 v3, s[44:45], v1, v1, 1.0
	v_rcp_f32_e32 v7, v3
	s_nop 0
	v_fma_f32 v9, -v3, v7, 1.0
	v_fmac_f32_e32 v7, v9, v7
	v_div_scale_f32 v9, vcc, 1.0, v1, 1.0
	v_mul_f32_e32 v10, v9, v7
	v_fma_f32 v11, -v3, v10, v9
	v_fmac_f32_e32 v10, v11, v7
	v_fma_f32 v3, -v3, v10, v9
	v_div_fmas_f32 v3, v3, v7, v10
	v_div_fixup_f32 v9, v3, v1, 1.0
	v_mov_b32_e32 v1, s21
	ds_write_b64 v1, v[8:9]
.Lgm_u2_st2:
	s_or_b64 exec, exec, s[38:39]
	s_add_i32 s3, s3, 8
	s_waitcnt vmcnt(24)
	v_lshlrev_b32_e32 v16, 16, v56
	v_and_b32_e32 v17, 0xffff0000, v56
	v_lshlrev_b32_e32 v8, 16, v57
	v_and_b32_e32 v9, 0xffff0000, v57
	v_lshlrev_b32_e32 v18, 16, v58
	v_and_b32_e32 v19, 0xffff0000, v58
	v_lshlrev_b32_e32 v10, 16, v59
	v_and_b32_e32 v11, 0xffff0000, v59
	v_lshlrev_b32_e32 v20, 16, v60
	v_and_b32_e32 v21, 0xffff0000, v60
	v_lshlrev_b32_e32 v12, 16, v61
	v_and_b32_e32 v13, 0xffff0000, v61
	v_lshlrev_b32_e32 v22, 16, v62
	v_and_b32_e32 v23, 0xffff0000, v62
	v_lshlrev_b32_e32 v14, 16, v63
	v_and_b32_e32 v15, 0xffff0000, v63
	v_pk_add_f32 v[24:25], v[16:17], v[18:19]
	v_pk_add_f32 v[26:27], v[8:9], v[10:11]
	v_pk_add_f32 v[28:29], v[20:21], v[22:23]
	v_pk_add_f32 v[30:31], v[12:13], v[14:15]
	v_pk_mul_f32 v[10:11], v[10:11], v[10:11]
	v_pk_mul_f32 v[18:19], v[18:19], v[18:19]
	v_pk_mul_f32 v[14:15], v[14:15], v[14:15]
	v_pk_mul_f32 v[22:23], v[22:23], v[22:23]
	v_pk_add_f32 v[26:27], v[26:27], v[30:31]
	v_pk_add_f32 v[24:25], v[24:25], v[28:29]
	v_pk_fma_f32 v[16:17], v[16:17], v[16:17], v[18:19]
	v_pk_fma_f32 v[8:9], v[8:9], v[8:9], v[10:11]
	v_pk_fma_f32 v[10:11], v[20:21], v[20:21], v[22:23]
	v_pk_fma_f32 v[12:13], v[12:13], v[12:13], v[14:15]
	v_pk_add_f32 v[10:11], v[16:17], v[10:11]
	v_pk_add_f32 v[8:9], v[8:9], v[12:13]
	v_add_f32_e32 v1, v24, v25
	v_add_f32_e32 v3, v26, v27
	v_add_f32_e32 v1, v1, v3
	v_add_f32_e32 v3, v10, v11
	v_add_f32_e32 v7, v8, v9
	v_add_f32_e32 v3, v3, v7
	v_add_f32_dpp v1, v1, v1 quad_perm:[1,0,3,2] row_mask:0xf bank_mask:0xf bound_ctrl:1
	s_nop 0
	v_add_f32_dpp v3, v3, v3 quad_perm:[1,0,3,2] row_mask:0xf bank_mask:0xf bound_ctrl:1
	v_add_f32_dpp v1, v1, v1 quad_perm:[2,3,0,1] row_mask:0xf bank_mask:0xf bound_ctrl:1
	s_nop 0
	v_add_f32_dpp v3, v3, v3 quad_perm:[2,3,0,1] row_mask:0xf bank_mask:0xf bound_ctrl:1
	v_add_f32_dpp v1, v1, v1 row_half_mirror row_mask:0xf bank_mask:0xf bound_ctrl:1
	s_nop 0
	v_add_f32_dpp v3, v3, v3 row_half_mirror row_mask:0xf bank_mask:0xf bound_ctrl:1
	v_add_f32_dpp v1, v1, v1 row_mirror row_mask:0xf bank_mask:0xf bound_ctrl:1
	v_mov_b32_e32 v7, v1
	v_add_f32_dpp v8, v3, v3 row_mirror row_mask:0xf bank_mask:0xf bound_ctrl:1
	v_mov_b32_e32 v9, v8
	v_permlane16_swap_b32_e32 v1, v7
	s_nop 0
	v_permlane16_swap_b32_e32 v8, v9
	v_add_f32_e32 v1, v1, v7
	v_add_f32_e32 v7, v8, v9
	v_mov_b32_e32 v3, v1
	v_mov_b32_e32 v8, v7
	s_nop 0
	v_permlane32_swap_b32_e32 v1, v3
	v_permlane32_swap_b32_e32 v7, v8
	s_and_saveexec_b64 s[38:39], s[42:43]
	s_cbranch_execz .Lgm_u2_st3
; __device__ __forceinline__ void unpk8(const u32x4 w, f32x4& a, f32x4& b) { a = (f32x4){bflo(w.x), bfhi(w.x), bflo(w.y), bfhi(w.y)}; b = (f32x4){bflo(w.z), bfhi(w.z), bflo(w.w), bfhi(w.w)}; }
; __device__ __forceinline__ void gmlp_unit(Frame& F, const Args& a, int layer, int unit) {
;     ...
;     for (int r = 0; r < 16; ++r) { const int tok = wave * 16 + r; const bf16* rowp = GUV + (t0 + tok) * 2048 + 1024;
;         f32x4 x0, x1, x2, x3; unpk8(*(const v4u*)(rowp + lane * 8), x0, x1); unpk8(*(const v4u*)(rowp + 512 + lane * 8), x2, x3);
;         const f32x4 sv = (x0 + x1) + (x2 + x3), qv = (x0 * x0 + x1 * x1) + (x2 * x2 + x3 * x3);
;         const float s = wave_sum((sv.x + sv.y) + (sv.z + sv.w)), q = wave_sum((qv.x + qv.y) + (qv.z + qv.w));
;         const float mean = s * (1.f / 1024.f), var = fmaxf(q * (1.f / 1024.f) - mean * mean, 0.f);
;         if (lane == 0) { st[tok * 2] = mean; st[tok * 2 + 1] = 1.f / sqrtf(var + 1e-5f); } }
	v_add_f32_e32 v1, v1, v3
	v_add_f32_e32 v7, v7, v8
	v_mul_f32_e32 v8, 0x3a800000, v1
	v_mul_f32_e32 v1, v8, v8
	v_fma_f32 v1, v7, s13, -v1
	v_max_f32_e32 v1, 0, v1
	v_add_f32_e32 v1, 0x3727c5ac, v1
	v_mul_f32_e32 v3, 0x4f800000, v1
	v_cmp_gt_f32_e32 vcc, s69, v1
	s_add_i32 s21, s11, s3
	s_nop 0
	v_cndmask_b32_e32 v1, v1, v3, vcc
	v_sqrt_f32_e32 v3, v1
	s_nop 0
	v_add_u32_e32 v7, -1, v3
	v_fma_f32 v9, -v7, v3, v1
	v_cmp_ge_f32_e64 s[44:45], 0, v9
	v_add_u32_e32 v9, 1, v3
	s_nop 0
	v_cndmask_b32_e64 v7, v3, v7, s[44:45]
	v_fma_f32 v3, -v9, v3, v1
	v_cmp_lt_f32_e64 s[44:45], 0, v3
	s_nop 1
	v_cndmask_b32_e64 v3, v7, v9, s[44:45]
	v_mul_f32_e32 v7, 0x37800000, v3
	v_cndmask_b32_e32 v3, v3, v7, vcc
	v_cmp_class_f32_e32 vcc, v1, v242
	s_nop 1
	v_cndmask_b32_e32 v1, v3, v1, vcc
	v_div_scale_f32 v3, s[44:45], v1, v1, 1.0
	v_rcp_f32_e32 v7, v3
	s_nop 0
	v_fma_f32 v9, -v3, v7, 1.0
	v_fmac_f32_e32 v7, v9, v7
	v_div_scale_f32 v9, vcc, 1.0, v1, 1.0
	v_mul_f32_e32 v10, v9, v7
	v_fma_f32 v11, -v3, v10, v9
	v_fmac_f32_e32 v10, v11, v7
	v_fma_f32 v3, -v3, v10, v9
	v_div_fmas_f32 v3, v3, v7, v10
	v_div_fixup_f32 v9, v3, v1, 1.0
	v_mov_b32_e32 v1, s21
	ds_write_b64 v1, v[8:9]
.Lgm_u2_st3:
	s_or_b64 exec, exec, s[38:39]
	s_add_i32 s3, s3, 8
	s_waitcnt vmcnt(22)
	v_lshlrev_b32_e32 v16, 16, v64
	v_and_b32_e32 v17, 0xffff0000, v64
	v_lshlrev_b32_e32 v8, 16, v65
	v_and_b32_e32 v9, 0xffff0000, v65
	v_lshlrev_b32_e32 v18, 16, v66
	v_and_b32_e32 v19, 0xffff0000, v66
	v_lshlrev_b32_e32 v10, 16, v67
	v_and_b32_e32 v11, 0xffff0000, v67
	v_lshlrev_b32_e32 v20, 16, v68
	v_and_b32_e32 v21, 0xffff0000, v68
	v_lshlrev_b32_e32 v12, 16, v69
	v_and_b32_e32 v13, 0xffff0000, v69
	v_lshlrev_b32_e32 v22, 16, v70
	v_and_b32_e32 v23, 0xffff0000, v70
	v_lshlrev_b32_e32 v14, 16, v71
	v_and_b32_e32 v15, 0xffff0000, v71
	v_pk_add_f32 v[24:25], v[16:17], v[18:19]
	v_pk_add_f32 v[26:27], v[8:9], v[10:11]
	v_pk_add_f32 v[28:29], v[20:21], v[22:23]
	v_pk_add_f32 v[30:31], v[12:13], v[14:15]
	v_pk_mul_f32 v[10:11], v[10:11], v[10:11]
	v_pk_mul_f32 v[18:19], v[18:19], v[18:19]
	v_pk_mul_f32 v[14:15], v[14:15], v[14:15]
	v_pk_mul_f32 v[22:23], v[22:23], v[22:23]
	v_pk_add_f32 v[26:27], v[26:27], v[30:31]
	v_pk_add_f32 v[24:25], v[24:25], v[28:29]
	v_pk_fma_f32 v[16:17], v[16:17], v[16:17], v[18:19]
	v_pk_fma_f32 v[8:9], v[8:9], v[8:9], v[10:11]
	v_pk_fma_f32 v[10:11], v[20:21], v[20:21], v[22:23]
	v_pk_fma_f32 v[12:13], v[12:13], v[12:13], v[14:15]
	v_pk_add_f32 v[10:11], v[16:17], v[10:11]
	v_pk_add_f32 v[8:9], v[8:9], v[12:13]
	v_add_f32_e32 v1, v24, v25
	v_add_f32_e32 v3, v26, v27
	v_add_f32_e32 v1, v1, v3
	v_add_f32_e32 v3, v10, v11
	v_add_f32_e32 v7, v8, v9
	v_add_f32_e32 v3, v3, v7
	v_add_f32_dpp v1, v1, v1 quad_perm:[1,0,3,2] row_mask:0xf bank_mask:0xf bound_ctrl:1
	s_nop 0
	v_add_f32_dpp v3, v3, v3 quad_perm:[1,0,3,2] row_mask:0xf bank_mask:0xf bound_ctrl:1
	v_add_f32_dpp v1, v1, v1 quad_perm:[2,3,0,1] row_mask:0xf bank_mask:0xf bound_ctrl:1
	s_nop 0
	v_add_f32_dpp v3, v3, v3 quad_perm:[2,3,0,1] row_mask:0xf bank_mask:0xf bound_ctrl:1
	v_add_f32_dpp v1, v1, v1 row_half_mirror row_mask:0xf bank_mask:0xf bound_ctrl:1
	s_nop 0
	v_add_f32_dpp v3, v3, v3 row_half_mirror row_mask:0xf bank_mask:0xf bound_ctrl:1
	v_add_f32_dpp v1, v1, v1 row_mirror row_mask:0xf bank_mask:0xf bound_ctrl:1
	v_mov_b32_e32 v7, v1
	v_add_f32_dpp v8, v3, v3 row_mirror row_mask:0xf bank_mask:0xf bound_ctrl:1
	v_mov_b32_e32 v9, v8
	v_permlane16_swap_b32_e32 v1, v7
	s_nop 0
	v_permlane16_swap_b32_e32 v8, v9
	v_add_f32_e32 v1, v1, v7
	v_add_f32_e32 v7, v8, v9
	v_mov_b32_e32 v3, v1
	v_mov_b32_e32 v8, v7
	s_nop 0
	v_permlane32_swap_b32_e32 v1, v3
	v_permlane32_swap_b32_e32 v7, v8
	s_and_saveexec_b64 s[38:39], s[42:43]
	s_cbranch_execz .Lgm_u2_st4
	v_add_f32_e32 v1, v1, v3
	v_add_f32_e32 v7, v7, v8
	v_mul_f32_e32 v8, 0x3a800000, v1
	v_mul_f32_e32 v1, v8, v8
	v_fma_f32 v1, v7, s13, -v1
	v_max_f32_e32 v1, 0, v1
	v_add_f32_e32 v1, 0x3727c5ac, v1
	v_mul_f32_e32 v3, 0x4f800000, v1
	v_cmp_gt_f32_e32 vcc, s69, v1
	s_add_i32 s21, s11, s3
	s_nop 0
	v_cndmask_b32_e32 v1, v1, v3, vcc
	v_sqrt_f32_e32 v3, v1
	s_nop 0
	v_add_u32_e32 v7, -1, v3
	v_fma_f32 v9, -v7, v3, v1
	v_cmp_ge_f32_e64 s[44:45], 0, v9
	v_add_u32_e32 v9, 1, v3
	s_nop 0
	v_cndmask_b32_e64 v7, v3, v7, s[44:45]
	v_fma_f32 v3, -v9, v3, v1
	v_cmp_lt_f32_e64 s[44:45], 0, v3
	s_nop 1
	v_cndmask_b32_e64 v3, v7, v9, s[44:45]
	v_mul_f32_e32 v7, 0x37800000, v3
	v_cndmask_b32_e32 v3, v3, v7, vcc
	v_cmp_class_f32_e32 vcc, v1, v242
	s_nop 1
	v_cndmask_b32_e32 v1, v3, v1, vcc
	v_div_scale_f32 v3, s[44:45], v1, v1, 1.0
	v_rcp_f32_e32 v7, v3
	s_nop 0
	v_fma_f32 v9, -v3, v7, 1.0
	v_fmac_f32_e32 v7, v9, v7
	v_div_scale_f32 v9, vcc, 1.0, v1, 1.0
	v_mul_f32_e32 v10, v9, v7
	v_fma_f32 v11, -v3, v10, v9
	v_fmac_f32_e32 v10, v11, v7
	v_fma_f32 v3, -v3, v10, v9
	v_div_fmas_f32 v3, v3, v7, v10
	v_div_fixup_f32 v9, v3, v1, 1.0
	v_mov_b32_e32 v1, s21
	ds_write_b64 v1, v[8:9]
; __device__ __forceinline__ void unpk8(const u32x4 w, f32x4& a, f32x4& b) { a = (f32x4){bflo(w.x), bfhi(w.x), bflo(w.y), bfhi(w.y)}; b = (f32x4){bflo(w.z), bfhi(w.z), bflo(w.w), bfhi(w.w)}; }
; __device__ __forceinline__ void gmlp_unit(Frame& F, const Args& a, int layer, int unit) {
;     ...
;     for (int r = 0; r < 16; ++r) { const int tok = wave * 16 + r; const bf16* rowp = GUV + (t0 + tok) * 2048 + 1024;
;         f32x4 x0, x1, x2, x3; unpk8(*(const v4u*)(rowp + lane * 8), x0, x1); unpk8(*(const v4u*)(rowp + 512 + lane * 8), x2, x3);
;         const f32x4 sv = (x0 + x1) + (x2 + x3), qv = (x0 * x0 + x1 * x1) + (x2 * x2 + x3 * x3);
;         const float s = wave_sum((sv.x + sv.y) + (sv.z + sv.w)), q = wave_sum((qv.x + qv.y) + (qv.z + qv.w));
;         const float mean = s * (1.f / 1024.f), var = fmaxf(q * (1.f / 1024.f) - mean * mean, 0.f);
;         if (lane == 0) { st[tok * 2] = mean; st[tok * 2 + 1] = 1.f / sqrtf(var + 1e-5f); } }
.Lgm_u2_st4:
	s_or_b64 exec, exec, s[38:39]
	s_add_i32 s3, s3, 8
	s_waitcnt vmcnt(20)
	v_lshlrev_b32_e32 v16, 16, v72
	v_and_b32_e32 v17, 0xffff0000, v72
	v_lshlrev_b32_e32 v8, 16, v73
	v_and_b32_e32 v9, 0xffff0000, v73
	v_lshlrev_b32_e32 v18, 16, v74
	v_and_b32_e32 v19, 0xffff0000, v74
	v_lshlrev_b32_e32 v10, 16, v75
	v_and_b32_e32 v11, 0xffff0000, v75
	v_lshlrev_b32_e32 v20, 16, v76
	v_and_b32_e32 v21, 0xffff0000, v76
	v_lshlrev_b32_e32 v12, 16, v77
	v_and_b32_e32 v13, 0xffff0000, v77
	v_lshlrev_b32_e32 v22, 16, v78
	v_and_b32_e32 v23, 0xffff0000, v78
	v_lshlrev_b32_e32 v14, 16, v79
	v_and_b32_e32 v15, 0xffff0000, v79
	v_pk_add_f32 v[24:25], v[16:17], v[18:19]
	v_pk_add_f32 v[26:27], v[8:9], v[10:11]
	v_pk_add_f32 v[28:29], v[20:21], v[22:23]
	v_pk_add_f32 v[30:31], v[12:13], v[14:15]
	v_pk_mul_f32 v[10:11], v[10:11], v[10:11]
	v_pk_mul_f32 v[18:19], v[18:19], v[18:19]
	v_pk_mul_f32 v[14:15], v[14:15], v[14:15]
	v_pk_mul_f32 v[22:23], v[22:23], v[22:23]
	v_pk_add_f32 v[26:27], v[26:27], v[30:31]
	v_pk_add_f32 v[24:25], v[24:25], v[28:29]
	v_pk_fma_f32 v[16:17], v[16:17], v[16:17], v[18:19]
	v_pk_fma_f32 v[8:9], v[8:9], v[8:9], v[10:11]
	v_pk_fma_f32 v[10:11], v[20:21], v[20:21], v[22:23]
	v_pk_fma_f32 v[12:13], v[12:13], v[12:13], v[14:15]
	v_pk_add_f32 v[10:11], v[16:17], v[10:11]
	v_pk_add_f32 v[8:9], v[8:9], v[12:13]
	v_add_f32_e32 v1, v24, v25
	v_add_f32_e32 v3, v26, v27
	v_add_f32_e32 v1, v1, v3
	v_add_f32_e32 v3, v10, v11
	v_add_f32_e32 v7, v8, v9
	v_add_f32_e32 v3, v3, v7
	v_add_f32_dpp v1, v1, v1 quad_perm:[1,0,3,2] row_mask:0xf bank_mask:0xf bound_ctrl:1
	s_nop 0
	v_add_f32_dpp v3, v3, v3 quad_perm:[1,0,3,2] row_mask:0xf bank_mask:0xf bound_ctrl:1
	v_add_f32_dpp v1, v1, v1 quad_perm:[2,3,0,1] row_mask:0xf bank_mask:0xf bound_ctrl:1
	s_nop 0
	v_add_f32_dpp v3, v3, v3 quad_perm:[2,3,0,1] row_mask:0xf bank_mask:0xf bound_ctrl:1
	v_add_f32_dpp v1, v1, v1 row_half_mirror row_mask:0xf bank_mask:0xf bound_ctrl:1
	s_nop 0
	v_add_f32_dpp v3, v3, v3 row_half_mirror row_mask:0xf bank_mask:0xf bound_ctrl:1
	v_add_f32_dpp v1, v1, v1 row_mirror row_mask:0xf bank_mask:0xf bound_ctrl:1
	v_mov_b32_e32 v7, v1
	v_add_f32_dpp v8, v3, v3 row_mirror row_mask:0xf bank_mask:0xf bound_ctrl:1
	v_mov_b32_e32 v9, v8
	v_permlane16_swap_b32_e32 v1, v7
	s_nop 0
	v_permlane16_swap_b32_e32 v8, v9
	v_add_f32_e32 v1, v1, v7
	v_add_f32_e32 v7, v8, v9
	v_mov_b32_e32 v3, v1
	v_mov_b32_e32 v8, v7
	s_nop 0
	v_permlane32_swap_b32_e32 v1, v3
	v_permlane32_swap_b32_e32 v7, v8
	s_and_saveexec_b64 s[38:39], s[42:43]
	s_cbranch_execz .Lgm_u2_st5
	v_add_f32_e32 v1, v1, v3
	v_add_f32_e32 v7, v7, v8
	v_mul_f32_e32 v8, 0x3a800000, v1
	v_mul_f32_e32 v1, v8, v8
	v_fma_f32 v1, v7, s13, -v1
	v_max_f32_e32 v1, 0, v1
	v_add_f32_e32 v1, 0x3727c5ac, v1
	v_mul_f32_e32 v3, 0x4f800000, v1
	v_cmp_gt_f32_e32 vcc, s69, v1
	s_add_i32 s21, s11, s3
	s_nop 0
	v_cndmask_b32_e32 v1, v1, v3, vcc
	v_sqrt_f32_e32 v3, v1
	s_nop 0
	v_add_u32_e32 v7, -1, v3
	v_fma_f32 v9, -v7, v3, v1
	v_cmp_ge_f32_e64 s[44:45], 0, v9
	v_add_u32_e32 v9, 1, v3
	s_nop 0
	v_cndmask_b32_e64 v7, v3, v7, s[44:45]
	v_fma_f32 v3, -v9, v3, v1
	v_cmp_lt_f32_e64 s[44:45], 0, v3
	s_nop 1
	v_cndmask_b32_e64 v3, v7, v9, s[44:45]
	v_mul_f32_e32 v7, 0x37800000, v3
	v_cndmask_b32_e32 v3, v3, v7, vcc
	v_cmp_class_f32_e32 vcc, v1, v242
	s_nop 1
	v_cndmask_b32_e32 v1, v3, v1, vcc
	v_div_scale_f32 v3, s[44:45], v1, v1, 1.0
	v_rcp_f32_e32 v7, v3
	s_nop 0
	v_fma_f32 v9, -v3, v7, 1.0
	v_fmac_f32_e32 v7, v9, v7
	v_div_scale_f32 v9, vcc, 1.0, v1, 1.0
	v_mul_f32_e32 v10, v9, v7
	v_fma_f32 v11, -v3, v10, v9
	v_fmac_f32_e32 v10, v11, v7
	v_fma_f32 v3, -v3, v10, v9
	v_div_fmas_f32 v3, v3, v7, v10
	v_div_fixup_f32 v9, v3, v1, 1.0
	v_mov_b32_e32 v1, s21
	ds_write_b64 v1, v[8:9]
.Lgm_u2_st5:
	s_or_b64 exec, exec, s[38:39]
	s_add_i32 s3, s3, 8
	s_waitcnt vmcnt(18)
	v_lshlrev_b32_e32 v16, 16, v80
	v_and_b32_e32 v17, 0xffff0000, v80
	v_lshlrev_b32_e32 v8, 16, v81
	v_and_b32_e32 v9, 0xffff0000, v81
	v_lshlrev_b32_e32 v18, 16, v82
	v_and_b32_e32 v19, 0xffff0000, v82
	v_lshlrev_b32_e32 v10, 16, v83
	v_and_b32_e32 v11, 0xffff0000, v83
	v_lshlrev_b32_e32 v20, 16, v84
	v_and_b32_e32 v21, 0xffff0000, v84
	v_lshlrev_b32_e32 v12, 16, v85
	v_and_b32_e32 v13, 0xffff0000, v85
	v_lshlrev_b32_e32 v22, 16, v86
	v_and_b32_e32 v23, 0xffff0000, v86
	v_lshlrev_b32_e32 v14, 16, v87
	v_and_b32_e32 v15, 0xffff0000, v87
	v_pk_add_f32 v[24:25], v[16:17], v[18:19]
	v_pk_add_f32 v[26:27], v[8:9], v[10:11]
	v_pk_add_f32 v[28:29], v[20:21], v[22:23]
	v_pk_add_f32 v[30:31], v[12:13], v[14:15]
	v_pk_mul_f32 v[10:11], v[10:11], v[10:11]
	v_pk_mul_f32 v[18:19], v[18:19], v[18:19]
	v_pk_mul_f32 v[14:15], v[14:15], v[14:15]
	v_pk_mul_f32 v[22:23], v[22:23], v[22:23]
	v_pk_add_f32 v[26:27], v[26:27], v[30:31]
	v_pk_add_f32 v[24:25], v[24:25], v[28:29]
	v_pk_fma_f32 v[16:17], v[16:17], v[16:17], v[18:19]
	v_pk_fma_f32 v[8:9], v[8:9], v[8:9], v[10:11]
	v_pk_fma_f32 v[10:11], v[20:21], v[20:21], v[22:23]
	v_pk_fma_f32 v[12:13], v[12:13], v[12:13], v[14:15]
	v_pk_add_f32 v[10:11], v[16:17], v[10:11]
	v_pk_add_f32 v[8:9], v[8:9], v[12:13]
	v_add_f32_e32 v1, v24, v25
	v_add_f32_e32 v3, v26, v27
	v_add_f32_e32 v1, v1, v3
	v_add_f32_e32 v3, v10, v11
	v_add_f32_e32 v7, v8, v9
	v_add_f32_e32 v3, v3, v7
	v_add_f32_dpp v1, v1, v1 quad_perm:[1,0,3,2] row_mask:0xf bank_mask:0xf bound_ctrl:1
	s_nop 0
	v_add_f32_dpp v3, v3, v3 quad_perm:[1,0,3,2] row_mask:0xf bank_mask:0xf bound_ctrl:1
	v_add_f32_dpp v1, v1, v1 quad_perm:[2,3,0,1] row_mask:0xf bank_mask:0xf bound_ctrl:1
	s_nop 0
	v_add_f32_dpp v3, v3, v3 quad_perm:[2,3,0,1] row_mask:0xf bank_mask:0xf bound_ctrl:1
	v_add_f32_dpp v1, v1, v1 row_half_mirror row_mask:0xf bank_mask:0xf bound_ctrl:1
	s_nop 0
	v_add_f32_dpp v3, v3, v3 row_half_mirror row_mask:0xf bank_mask:0xf bound_ctrl:1
	v_add_f32_dpp v1, v1, v1 row_mirror row_mask:0xf bank_mask:0xf bound_ctrl:1
	v_mov_b32_e32 v7, v1
	v_add_f32_dpp v8, v3, v3 row_mirror row_mask:0xf bank_mask:0xf bound_ctrl:1
	v_mov_b32_e32 v9, v8
	v_permlane16_swap_b32_e32 v1, v7
	s_nop 0
	v_permlane16_swap_b32_e32 v8, v9
	v_add_f32_e32 v1, v1, v7
	v_add_f32_e32 v7, v8, v9
	v_mov_b32_e32 v3, v1
	v_mov_b32_e32 v8, v7
	s_nop 0
	v_permlane32_swap_b32_e32 v1, v3
	v_permlane32_swap_b32_e32 v7, v8
	s_and_saveexec_b64 s[38:39], s[42:43]
	s_cbranch_execz .Lgm_u2_st6
; __device__ __forceinline__ void unpk8(const u32x4 w, f32x4& a, f32x4& b) { a = (f32x4){bflo(w.x), bfhi(w.x), bflo(w.y), bfhi(w.y)}; b = (f32x4){bflo(w.z), bfhi(w.z), bflo(w.w), bfhi(w.w)}; }
; __device__ __forceinline__ void gmlp_unit(Frame& F, const Args& a, int layer, int unit) {
;     ...
;     for (int r = 0; r < 16; ++r) { const int tok = wave * 16 + r; const bf16* rowp = GUV + (t0 + tok) * 2048 + 1024;
;         f32x4 x0, x1, x2, x3; unpk8(*(const v4u*)(rowp + lane * 8), x0, x1); unpk8(*(const v4u*)(rowp + 512 + lane * 8), x2, x3);
;         const f32x4 sv = (x0 + x1) + (x2 + x3), qv = (x0 * x0 + x1 * x1) + (x2 * x2 + x3 * x3);
;         const float s = wave_sum((sv.x + sv.y) + (sv.z + sv.w)), q = wave_sum((qv.x + qv.y) + (qv.z + qv.w));
;         const float mean = s * (1.f / 1024.f), var = fmaxf(q * (1.f / 1024.f) - mean * mean, 0.f);
;         if (lane == 0) { st[tok * 2] = mean; st[tok * 2 + 1] = 1.f / sqrtf(var + 1e-5f); } }
	v_add_f32_e32 v1, v1, v3
	v_add_f32_e32 v7, v7, v8
	v_mul_f32_e32 v8, 0x3a800000, v1
	v_mul_f32_e32 v1, v8, v8
	v_fma_f32 v1, v7, s13, -v1
	v_max_f32_e32 v1, 0, v1
	v_add_f32_e32 v1, 0x3727c5ac, v1
	v_mul_f32_e32 v3, 0x4f800000, v1
	v_cmp_gt_f32_e32 vcc, s69, v1
	s_add_i32 s21, s11, s3
	s_nop 0
	v_cndmask_b32_e32 v1, v1, v3, vcc
	v_sqrt_f32_e32 v3, v1
	s_nop 0
	v_add_u32_e32 v7, -1, v3
	v_fma_f32 v9, -v7, v3, v1
	v_cmp_ge_f32_e64 s[44:45], 0, v9
	v_add_u32_e32 v9, 1, v3
	s_nop 0
	v_cndmask_b32_e64 v7, v3, v7, s[44:45]
	v_fma_f32 v3, -v9, v3, v1
	v_cmp_lt_f32_e64 s[44:45], 0, v3
	s_nop 1
	v_cndmask_b32_e64 v3, v7, v9, s[44:45]
	v_mul_f32_e32 v7, 0x37800000, v3
	v_cndmask_b32_e32 v3, v3, v7, vcc
	v_cmp_class_f32_e32 vcc, v1, v242
	s_nop 1
	v_cndmask_b32_e32 v1, v3, v1, vcc
	v_div_scale_f32 v3, s[44:45], v1, v1, 1.0
	v_rcp_f32_e32 v7, v3
	s_nop 0
	v_fma_f32 v9, -v3, v7, 1.0
	v_fmac_f32_e32 v7, v9, v7
	v_div_scale_f32 v9, vcc, 1.0, v1, 1.0
	v_mul_f32_e32 v10, v9, v7
	v_fma_f32 v11, -v3, v10, v9
	v_fmac_f32_e32 v10, v11, v7
	v_fma_f32 v3, -v3, v10, v9
	v_div_fmas_f32 v3, v3, v7, v10
	v_div_fixup_f32 v9, v3, v1, 1.0
	v_mov_b32_e32 v1, s21
	ds_write_b64 v1, v[8:9]
.Lgm_u2_st6:
	s_or_b64 exec, exec, s[38:39]
	s_add_i32 s3, s3, 8
	s_waitcnt vmcnt(16)
	v_lshlrev_b32_e32 v16, 16, v88
	v_and_b32_e32 v17, 0xffff0000, v88
	v_lshlrev_b32_e32 v8, 16, v89
	v_and_b32_e32 v9, 0xffff0000, v89
	v_lshlrev_b32_e32 v18, 16, v90
	v_and_b32_e32 v19, 0xffff0000, v90
	v_lshlrev_b32_e32 v10, 16, v91
	v_and_b32_e32 v11, 0xffff0000, v91
	v_lshlrev_b32_e32 v20, 16, v92
	v_and_b32_e32 v21, 0xffff0000, v92
	v_lshlrev_b32_e32 v12, 16, v93
	v_and_b32_e32 v13, 0xffff0000, v93
	v_lshlrev_b32_e32 v22, 16, v94
	v_and_b32_e32 v23, 0xffff0000, v94
	v_lshlrev_b32_e32 v14, 16, v95
	v_and_b32_e32 v15, 0xffff0000, v95
	v_pk_add_f32 v[24:25], v[16:17], v[18:19]
	v_pk_add_f32 v[26:27], v[8:9], v[10:11]
	v_pk_add_f32 v[28:29], v[20:21], v[22:23]
	v_pk_add_f32 v[30:31], v[12:13], v[14:15]
	v_pk_mul_f32 v[10:11], v[10:11], v[10:11]
	v_pk_mul_f32 v[18:19], v[18:19], v[18:19]
	v_pk_mul_f32 v[14:15], v[14:15], v[14:15]
	v_pk_mul_f32 v[22:23], v[22:23], v[22:23]
	v_pk_add_f32 v[26:27], v[26:27], v[30:31]
	v_pk_add_f32 v[24:25], v[24:25], v[28:29]
	v_pk_fma_f32 v[16:17], v[16:17], v[16:17], v[18:19]
	v_pk_fma_f32 v[8:9], v[8:9], v[8:9], v[10:11]
	v_pk_fma_f32 v[10:11], v[20:21], v[20:21], v[22:23]
	v_pk_fma_f32 v[12:13], v[12:13], v[12:13], v[14:15]
	v_pk_add_f32 v[10:11], v[16:17], v[10:11]
	v_pk_add_f32 v[8:9], v[8:9], v[12:13]
	v_add_f32_e32 v1, v24, v25
	v_add_f32_e32 v3, v26, v27
	v_add_f32_e32 v1, v1, v3
	v_add_f32_e32 v3, v10, v11
	v_add_f32_e32 v7, v8, v9
	v_add_f32_e32 v3, v3, v7
	v_add_f32_dpp v1, v1, v1 quad_perm:[1,0,3,2] row_mask:0xf bank_mask:0xf bound_ctrl:1
	s_nop 0
	v_add_f32_dpp v3, v3, v3 quad_perm:[1,0,3,2] row_mask:0xf bank_mask:0xf bound_ctrl:1
	v_add_f32_dpp v1, v1, v1 quad_perm:[2,3,0,1] row_mask:0xf bank_mask:0xf bound_ctrl:1
	s_nop 0
	v_add_f32_dpp v3, v3, v3 quad_perm:[2,3,0,1] row_mask:0xf bank_mask:0xf bound_ctrl:1
	v_add_f32_dpp v1, v1, v1 row_half_mirror row_mask:0xf bank_mask:0xf bound_ctrl:1
	s_nop 0
	v_add_f32_dpp v3, v3, v3 row_half_mirror row_mask:0xf bank_mask:0xf bound_ctrl:1
	v_add_f32_dpp v1, v1, v1 row_mirror row_mask:0xf bank_mask:0xf bound_ctrl:1
	v_mov_b32_e32 v7, v1
	v_add_f32_dpp v8, v3, v3 row_mirror row_mask:0xf bank_mask:0xf bound_ctrl:1
	v_mov_b32_e32 v9, v8
	v_permlane16_swap_b32_e32 v1, v7
	s_nop 0
	v_permlane16_swap_b32_e32 v8, v9
	v_add_f32_e32 v1, v1, v7
	v_add_f32_e32 v7, v8, v9
	v_mov_b32_e32 v3, v1
	v_mov_b32_e32 v8, v7
	s_nop 0
	v_permlane32_swap_b32_e32 v1, v3
	v_permlane32_swap_b32_e32 v7, v8
	s_and_saveexec_b64 s[38:39], s[42:43]
	s_cbranch_execz .Lgm_u2_st7
	v_add_f32_e32 v1, v1, v3
	v_add_f32_e32 v7, v7, v8
	v_mul_f32_e32 v8, 0x3a800000, v1
	v_mul_f32_e32 v1, v8, v8
	v_fma_f32 v1, v7, s13, -v1
	v_max_f32_e32 v1, 0, v1
	v_add_f32_e32 v1, 0x3727c5ac, v1
	v_mul_f32_e32 v3, 0x4f800000, v1
	v_cmp_gt_f32_e32 vcc, s69, v1
	s_add_i32 s21, s11, s3
	s_nop 0
	v_cndmask_b32_e32 v1, v1, v3, vcc
	v_sqrt_f32_e32 v3, v1
	s_nop 0
	v_add_u32_e32 v7, -1, v3
	v_fma_f32 v9, -v7, v3, v1
	v_cmp_ge_f32_e64 s[44:45], 0, v9
	v_add_u32_e32 v9, 1, v3
	s_nop 0
	v_cndmask_b32_e64 v7, v3, v7, s[44:45]
	v_fma_f32 v3, -v9, v3, v1
	v_cmp_lt_f32_e64 s[44:45], 0, v3
	s_nop 1
	v_cndmask_b32_e64 v3, v7, v9, s[44:45]
	v_mul_f32_e32 v7, 0x37800000, v3
	v_cndmask_b32_e32 v3, v3, v7, vcc
	v_cmp_class_f32_e32 vcc, v1, v242
	s_nop 1
	v_cndmask_b32_e32 v1, v3, v1, vcc
	v_div_scale_f32 v3, s[44:45], v1, v1, 1.0
	v_rcp_f32_e32 v7, v3
	s_nop 0
	v_fma_f32 v9, -v3, v7, 1.0
	v_fmac_f32_e32 v7, v9, v7
	v_div_scale_f32 v9, vcc, 1.0, v1, 1.0
	v_mul_f32_e32 v10, v9, v7
	v_fma_f32 v11, -v3, v10, v9
	v_fmac_f32_e32 v10, v11, v7
	v_fma_f32 v3, -v3, v10, v9
	v_div_fmas_f32 v3, v3, v7, v10
	v_div_fixup_f32 v9, v3, v1, 1.0
	v_mov_b32_e32 v1, s21
	ds_write_b64 v1, v[8:9]
; __device__ __forceinline__ void unpk8(const u32x4 w, f32x4& a, f32x4& b) { a = (f32x4){bflo(w.x), bfhi(w.x), bflo(w.y), bfhi(w.y)}; b = (f32x4){bflo(w.z), bfhi(w.z), bflo(w.w), bfhi(w.w)}; }
; __device__ __forceinline__ void gmlp_unit(Frame& F, const Args& a, int layer, int unit) {
;     ...
;     for (int r = 0; r < 16; ++r) { const int tok = wave * 16 + r; const bf16* rowp = GUV + (t0 + tok) * 2048 + 1024;
;         f32x4 x0, x1, x2, x3; unpk8(*(const v4u*)(rowp + lane * 8), x0, x1); unpk8(*(const v4u*)(rowp + 512 + lane * 8), x2, x3);
;         const f32x4 sv = (x0 + x1) + (x2 + x3), qv = (x0 * x0 + x1 * x1) + (x2 * x2 + x3 * x3);
;         const float s = wave_sum((sv.x + sv.y) + (sv.z + sv.w)), q = wave_sum((qv.x + qv.y) + (qv.z + qv.w));
;         const float mean = s * (1.f / 1024.f), var = fmaxf(q * (1.f / 1024.f) - mean * mean, 0.f);
;         if (lane == 0) { st[tok * 2] = mean; st[tok * 2 + 1] = 1.f / sqrtf(var + 1e-5f); } }
.Lgm_u2_st7:
	s_or_b64 exec, exec, s[38:39]
	s_add_i32 s3, s3, 8
	s_waitcnt vmcnt(14)
	v_lshlrev_b32_e32 v16, 16, v100
	v_and_b32_e32 v17, 0xffff0000, v100
	v_lshlrev_b32_e32 v8, 16, v101
	v_and_b32_e32 v9, 0xffff0000, v101
	v_lshlrev_b32_e32 v18, 16, v102
	v_and_b32_e32 v19, 0xffff0000, v102
	v_lshlrev_b32_e32 v10, 16, v103
	v_and_b32_e32 v11, 0xffff0000, v103
	v_lshlrev_b32_e32 v20, 16, v104
	v_and_b32_e32 v21, 0xffff0000, v104
	v_lshlrev_b32_e32 v12, 16, v105
	v_and_b32_e32 v13, 0xffff0000, v105
	v_lshlrev_b32_e32 v22, 16, v106
	v_and_b32_e32 v23, 0xffff0000, v106
	v_lshlrev_b32_e32 v14, 16, v107
	v_and_b32_e32 v15, 0xffff0000, v107
	v_pk_add_f32 v[24:25], v[16:17], v[18:19]
	v_pk_add_f32 v[26:27], v[8:9], v[10:11]
	v_pk_add_f32 v[28:29], v[20:21], v[22:23]
	v_pk_add_f32 v[30:31], v[12:13], v[14:15]
	v_pk_mul_f32 v[10:11], v[10:11], v[10:11]
	v_pk_mul_f32 v[18:19], v[18:19], v[18:19]
	v_pk_mul_f32 v[14:15], v[14:15], v[14:15]
	v_pk_mul_f32 v[22:23], v[22:23], v[22:23]
	v_pk_add_f32 v[26:27], v[26:27], v[30:31]
	v_pk_add_f32 v[24:25], v[24:25], v[28:29]
	v_pk_fma_f32 v[16:17], v[16:17], v[16:17], v[18:19]
	v_pk_fma_f32 v[8:9], v[8:9], v[8:9], v[10:11]
	v_pk_fma_f32 v[10:11], v[20:21], v[20:21], v[22:23]
	v_pk_fma_f32 v[12:13], v[12:13], v[12:13], v[14:15]
	v_pk_add_f32 v[10:11], v[16:17], v[10:11]
	v_pk_add_f32 v[8:9], v[8:9], v[12:13]
	v_add_f32_e32 v1, v24, v25
	v_add_f32_e32 v3, v26, v27
	v_add_f32_e32 v1, v1, v3
	v_add_f32_e32 v3, v10, v11
	v_add_f32_e32 v7, v8, v9
	v_add_f32_e32 v3, v3, v7
	v_add_f32_dpp v1, v1, v1 quad_perm:[1,0,3,2] row_mask:0xf bank_mask:0xf bound_ctrl:1
	s_nop 0
	v_add_f32_dpp v3, v3, v3 quad_perm:[1,0,3,2] row_mask:0xf bank_mask:0xf bound_ctrl:1
	v_add_f32_dpp v1, v1, v1 quad_perm:[2,3,0,1] row_mask:0xf bank_mask:0xf bound_ctrl:1
	s_nop 0
	v_add_f32_dpp v3, v3, v3 quad_perm:[2,3,0,1] row_mask:0xf bank_mask:0xf bound_ctrl:1
	v_add_f32_dpp v1, v1, v1 row_half_mirror row_mask:0xf bank_mask:0xf bound_ctrl:1
	s_nop 0
	v_add_f32_dpp v3, v3, v3 row_half_mirror row_mask:0xf bank_mask:0xf bound_ctrl:1
	v_add_f32_dpp v1, v1, v1 row_mirror row_mask:0xf bank_mask:0xf bound_ctrl:1
	v_mov_b32_e32 v7, v1
	v_add_f32_dpp v8, v3, v3 row_mirror row_mask:0xf bank_mask:0xf bound_ctrl:1
	v_mov_b32_e32 v9, v8
	v_permlane16_swap_b32_e32 v1, v7
	s_nop 0
	v_permlane16_swap_b32_e32 v8, v9
	v_add_f32_e32 v1, v1, v7
	v_add_f32_e32 v7, v8, v9
	v_mov_b32_e32 v3, v1
	v_mov_b32_e32 v8, v7
	s_nop 0
	v_permlane32_swap_b32_e32 v1, v3
	v_permlane32_swap_b32_e32 v7, v8
	s_and_saveexec_b64 s[38:39], s[42:43]
	s_cbranch_execz .Lgm_u2_st8
	v_add_f32_e32 v1, v1, v3
	v_add_f32_e32 v7, v7, v8
	v_mul_f32_e32 v8, 0x3a800000, v1
	v_mul_f32_e32 v1, v8, v8
	v_fma_f32 v1, v7, s13, -v1
	v_max_f32_e32 v1, 0, v1
	v_add_f32_e32 v1, 0x3727c5ac, v1
	v_mul_f32_e32 v3, 0x4f800000, v1
	v_cmp_gt_f32_e32 vcc, s69, v1
	s_add_i32 s21, s11, s3
	s_nop 0
	v_cndmask_b32_e32 v1, v1, v3, vcc
	v_sqrt_f32_e32 v3, v1
	s_nop 0
	v_add_u32_e32 v7, -1, v3
	v_fma_f32 v9, -v7, v3, v1
	v_cmp_ge_f32_e64 s[44:45], 0, v9
	v_add_u32_e32 v9, 1, v3
	s_nop 0
	v_cndmask_b32_e64 v7, v3, v7, s[44:45]
	v_fma_f32 v3, -v9, v3, v1
	v_cmp_lt_f32_e64 s[44:45], 0, v3
	s_nop 1
	v_cndmask_b32_e64 v3, v7, v9, s[44:45]
	v_mul_f32_e32 v7, 0x37800000, v3
	v_cndmask_b32_e32 v3, v3, v7, vcc
	v_cmp_class_f32_e32 vcc, v1, v242
	s_nop 1
	v_cndmask_b32_e32 v1, v3, v1, vcc
	v_div_scale_f32 v3, s[44:45], v1, v1, 1.0
	v_rcp_f32_e32 v7, v3
	s_nop 0
	v_fma_f32 v9, -v3, v7, 1.0
	v_fmac_f32_e32 v7, v9, v7
	v_div_scale_f32 v9, vcc, 1.0, v1, 1.0
	v_mul_f32_e32 v10, v9, v7
	v_fma_f32 v11, -v3, v10, v9
	v_fmac_f32_e32 v10, v11, v7
	v_fma_f32 v3, -v3, v10, v9
	v_div_fmas_f32 v3, v3, v7, v10
	v_div_fixup_f32 v9, v3, v1, 1.0
	v_mov_b32_e32 v1, s21
	ds_write_b64 v1, v[8:9]
.Lgm_u2_st8:
	s_or_b64 exec, exec, s[38:39]
	s_add_i32 s3, s3, 8
	s_waitcnt vmcnt(12)
	v_lshlrev_b32_e32 v16, 16, v108
	v_and_b32_e32 v17, 0xffff0000, v108
	v_lshlrev_b32_e32 v8, 16, v109
	v_and_b32_e32 v9, 0xffff0000, v109
	v_lshlrev_b32_e32 v18, 16, v110
	v_and_b32_e32 v19, 0xffff0000, v110
	v_lshlrev_b32_e32 v10, 16, v111
	v_and_b32_e32 v11, 0xffff0000, v111
	v_lshlrev_b32_e32 v20, 16, v112
	v_and_b32_e32 v21, 0xffff0000, v112
	v_lshlrev_b32_e32 v12, 16, v113
	v_and_b32_e32 v13, 0xffff0000, v113
	v_lshlrev_b32_e32 v22, 16, v114
	v_and_b32_e32 v23, 0xffff0000, v114
	v_lshlrev_b32_e32 v14, 16, v115
	v_and_b32_e32 v15, 0xffff0000, v115
	v_pk_add_f32 v[24:25], v[16:17], v[18:19]
	v_pk_add_f32 v[26:27], v[8:9], v[10:11]
	v_pk_add_f32 v[28:29], v[20:21], v[22:23]
	v_pk_add_f32 v[30:31], v[12:13], v[14:15]
	v_pk_mul_f32 v[10:11], v[10:11], v[10:11]
	v_pk_mul_f32 v[18:19], v[18:19], v[18:19]
	v_pk_mul_f32 v[14:15], v[14:15], v[14:15]
	v_pk_mul_f32 v[22:23], v[22:23], v[22:23]
	v_pk_add_f32 v[26:27], v[26:27], v[30:31]
	v_pk_add_f32 v[24:25], v[24:25], v[28:29]
	v_pk_fma_f32 v[16:17], v[16:17], v[16:17], v[18:19]
	v_pk_fma_f32 v[8:9], v[8:9], v[8:9], v[10:11]
	v_pk_fma_f32 v[10:11], v[20:21], v[20:21], v[22:23]
	v_pk_fma_f32 v[12:13], v[12:13], v[12:13], v[14:15]
	v_pk_add_f32 v[10:11], v[16:17], v[10:11]
	v_pk_add_f32 v[8:9], v[8:9], v[12:13]
	v_add_f32_e32 v1, v24, v25
	v_add_f32_e32 v3, v26, v27
	v_add_f32_e32 v1, v1, v3
	v_add_f32_e32 v3, v10, v11
	v_add_f32_e32 v7, v8, v9
	v_add_f32_e32 v3, v3, v7
	v_add_f32_dpp v1, v1, v1 quad_perm:[1,0,3,2] row_mask:0xf bank_mask:0xf bound_ctrl:1
	s_nop 0
	v_add_f32_dpp v3, v3, v3 quad_perm:[1,0,3,2] row_mask:0xf bank_mask:0xf bound_ctrl:1
	v_add_f32_dpp v1, v1, v1 quad_perm:[2,3,0,1] row_mask:0xf bank_mask:0xf bound_ctrl:1
	s_nop 0
	v_add_f32_dpp v3, v3, v3 quad_perm:[2,3,0,1] row_mask:0xf bank_mask:0xf bound_ctrl:1
	v_add_f32_dpp v1, v1, v1 row_half_mirror row_mask:0xf bank_mask:0xf bound_ctrl:1
	s_nop 0
	v_add_f32_dpp v3, v3, v3 row_half_mirror row_mask:0xf bank_mask:0xf bound_ctrl:1
	v_add_f32_dpp v1, v1, v1 row_mirror row_mask:0xf bank_mask:0xf bound_ctrl:1
	v_mov_b32_e32 v7, v1
	v_add_f32_dpp v8, v3, v3 row_mirror row_mask:0xf bank_mask:0xf bound_ctrl:1
	v_mov_b32_e32 v9, v8
	v_permlane16_swap_b32_e32 v1, v7
	s_nop 0
	v_permlane16_swap_b32_e32 v8, v9
	v_add_f32_e32 v1, v1, v7
	v_add_f32_e32 v7, v8, v9
	v_mov_b32_e32 v3, v1
	v_mov_b32_e32 v8, v7
	s_nop 0
	v_permlane32_swap_b32_e32 v1, v3
	v_permlane32_swap_b32_e32 v7, v8
	s_and_saveexec_b64 s[38:39], s[42:43]
	s_cbranch_execz .Lgm_u2_st9
; __device__ __forceinline__ void unpk8(const u32x4 w, f32x4& a, f32x4& b) { a = (f32x4){bflo(w.x), bfhi(w.x), bflo(w.y), bfhi(w.y)}; b = (f32x4){bflo(w.z), bfhi(w.z), bflo(w.w), bfhi(w.w)}; }
; __device__ __forceinline__ void gmlp_unit(Frame& F, const Args& a, int layer, int unit) {
;     ...
;     for (int r = 0; r < 16; ++r) { const int tok = wave * 16 + r; const bf16* rowp = GUV + (t0 + tok) * 2048 + 1024;
;         f32x4 x0, x1, x2, x3; unpk8(*(const v4u*)(rowp + lane * 8), x0, x1); unpk8(*(const v4u*)(rowp + 512 + lane * 8), x2, x3);
;         const f32x4 sv = (x0 + x1) + (x2 + x3), qv = (x0 * x0 + x1 * x1) + (x2 * x2 + x3 * x3);
;         const float s = wave_sum((sv.x + sv.y) + (sv.z + sv.w)), q = wave_sum((qv.x + qv.y) + (qv.z + qv.w));
;         const float mean = s * (1.f / 1024.f), var = fmaxf(q * (1.f / 1024.f) - mean * mean, 0.f);
;         if (lane == 0) { st[tok * 2] = mean; st[tok * 2 + 1] = 1.f / sqrtf(var + 1e-5f); } }
	v_add_f32_e32 v1, v1, v3
	v_add_f32_e32 v7, v7, v8
	v_mul_f32_e32 v8, 0x3a800000, v1
	v_mul_f32_e32 v1, v8, v8
	v_fma_f32 v1, v7, s13, -v1
	v_max_f32_e32 v1, 0, v1
	v_add_f32_e32 v1, 0x3727c5ac, v1
	v_mul_f32_e32 v3, 0x4f800000, v1
	v_cmp_gt_f32_e32 vcc, s69, v1
	s_add_i32 s21, s11, s3
	s_nop 0
	v_cndmask_b32_e32 v1, v1, v3, vcc
	v_sqrt_f32_e32 v3, v1
	s_nop 0
	v_add_u32_e32 v7, -1, v3
	v_fma_f32 v9, -v7, v3, v1
	v_cmp_ge_f32_e64 s[44:45], 0, v9
	v_add_u32_e32 v9, 1, v3
	s_nop 0
	v_cndmask_b32_e64 v7, v3, v7, s[44:45]
	v_fma_f32 v3, -v9, v3, v1
	v_cmp_lt_f32_e64 s[44:45], 0, v3
	s_nop 1
	v_cndmask_b32_e64 v3, v7, v9, s[44:45]
	v_mul_f32_e32 v7, 0x37800000, v3
	v_cndmask_b32_e32 v3, v3, v7, vcc
	v_cmp_class_f32_e32 vcc, v1, v242
	s_nop 1
	v_cndmask_b32_e32 v1, v3, v1, vcc
	v_div_scale_f32 v3, s[44:45], v1, v1, 1.0
	v_rcp_f32_e32 v7, v3
	s_nop 0
	v_fma_f32 v9, -v3, v7, 1.0
	v_fmac_f32_e32 v7, v9, v7
	v_div_scale_f32 v9, vcc, 1.0, v1, 1.0
	v_mul_f32_e32 v10, v9, v7
	v_fma_f32 v11, -v3, v10, v9
	v_fmac_f32_e32 v10, v11, v7
	v_fma_f32 v3, -v3, v10, v9
	v_div_fmas_f32 v3, v3, v7, v10
	v_div_fixup_f32 v9, v3, v1, 1.0
	v_mov_b32_e32 v1, s21
	ds_write_b64 v1, v[8:9]
.Lgm_u2_st9:
	s_or_b64 exec, exec, s[38:39]
	s_add_i32 s3, s3, 8
	s_waitcnt vmcnt(10)
	v_lshlrev_b32_e32 v16, 16, v116
	v_and_b32_e32 v17, 0xffff0000, v116
	v_lshlrev_b32_e32 v8, 16, v117
	v_and_b32_e32 v9, 0xffff0000, v117
	v_lshlrev_b32_e32 v18, 16, v118
	v_and_b32_e32 v19, 0xffff0000, v118
	v_lshlrev_b32_e32 v10, 16, v119
	v_and_b32_e32 v11, 0xffff0000, v119
	v_lshlrev_b32_e32 v20, 16, v120
	v_and_b32_e32 v21, 0xffff0000, v120
	v_lshlrev_b32_e32 v12, 16, v121
	v_and_b32_e32 v13, 0xffff0000, v121
	v_lshlrev_b32_e32 v22, 16, v122
	v_and_b32_e32 v23, 0xffff0000, v122
	v_lshlrev_b32_e32 v14, 16, v123
	v_and_b32_e32 v15, 0xffff0000, v123
	v_pk_add_f32 v[24:25], v[16:17], v[18:19]
	v_pk_add_f32 v[26:27], v[8:9], v[10:11]
	v_pk_add_f32 v[28:29], v[20:21], v[22:23]
	v_pk_add_f32 v[30:31], v[12:13], v[14:15]
	v_pk_mul_f32 v[10:11], v[10:11], v[10:11]
	v_pk_mul_f32 v[18:19], v[18:19], v[18:19]
	v_pk_mul_f32 v[14:15], v[14:15], v[14:15]
	v_pk_mul_f32 v[22:23], v[22:23], v[22:23]
	v_pk_add_f32 v[26:27], v[26:27], v[30:31]
	v_pk_add_f32 v[24:25], v[24:25], v[28:29]
	v_pk_fma_f32 v[16:17], v[16:17], v[16:17], v[18:19]
	v_pk_fma_f32 v[8:9], v[8:9], v[8:9], v[10:11]
	v_pk_fma_f32 v[10:11], v[20:21], v[20:21], v[22:23]
	v_pk_fma_f32 v[12:13], v[12:13], v[12:13], v[14:15]
	v_pk_add_f32 v[10:11], v[16:17], v[10:11]
	v_pk_add_f32 v[8:9], v[8:9], v[12:13]
	v_add_f32_e32 v1, v24, v25
	v_add_f32_e32 v3, v26, v27
	v_add_f32_e32 v1, v1, v3
	v_add_f32_e32 v3, v10, v11
	v_add_f32_e32 v7, v8, v9
	v_add_f32_e32 v3, v3, v7
	v_add_f32_dpp v1, v1, v1 quad_perm:[1,0,3,2] row_mask:0xf bank_mask:0xf bound_ctrl:1
	s_nop 0
	v_add_f32_dpp v3, v3, v3 quad_perm:[1,0,3,2] row_mask:0xf bank_mask:0xf bound_ctrl:1
	v_add_f32_dpp v1, v1, v1 quad_perm:[2,3,0,1] row_mask:0xf bank_mask:0xf bound_ctrl:1
	s_nop 0
	v_add_f32_dpp v3, v3, v3 quad_perm:[2,3,0,1] row_mask:0xf bank_mask:0xf bound_ctrl:1
	v_add_f32_dpp v1, v1, v1 row_half_mirror row_mask:0xf bank_mask:0xf bound_ctrl:1
	s_nop 0
	v_add_f32_dpp v3, v3, v3 row_half_mirror row_mask:0xf bank_mask:0xf bound_ctrl:1
	v_add_f32_dpp v1, v1, v1 row_mirror row_mask:0xf bank_mask:0xf bound_ctrl:1
	v_mov_b32_e32 v7, v1
	v_add_f32_dpp v8, v3, v3 row_mirror row_mask:0xf bank_mask:0xf bound_ctrl:1
	v_mov_b32_e32 v9, v8
	v_permlane16_swap_b32_e32 v1, v7
	s_nop 0
	v_permlane16_swap_b32_e32 v8, v9
	v_add_f32_e32 v1, v1, v7
	v_add_f32_e32 v7, v8, v9
	v_mov_b32_e32 v3, v1
	v_mov_b32_e32 v8, v7
	s_nop 0
	v_permlane32_swap_b32_e32 v1, v3
	v_permlane32_swap_b32_e32 v7, v8
	s_and_saveexec_b64 s[38:39], s[42:43]
	s_cbranch_execz .Lgm_u2_st10
	v_add_f32_e32 v1, v1, v3
	v_add_f32_e32 v7, v7, v8
	v_mul_f32_e32 v8, 0x3a800000, v1
	v_mul_f32_e32 v1, v8, v8
	v_fma_f32 v1, v7, s13, -v1
	v_max_f32_e32 v1, 0, v1
	v_add_f32_e32 v1, 0x3727c5ac, v1
	v_mul_f32_e32 v3, 0x4f800000, v1
	v_cmp_gt_f32_e32 vcc, s69, v1
	s_add_i32 s21, s11, s3
	s_nop 0
	v_cndmask_b32_e32 v1, v1, v3, vcc
	v_sqrt_f32_e32 v3, v1
	s_nop 0
	v_add_u32_e32 v7, -1, v3
	v_fma_f32 v9, -v7, v3, v1
	v_cmp_ge_f32_e64 s[44:45], 0, v9
	v_add_u32_e32 v9, 1, v3
	s_nop 0
	v_cndmask_b32_e64 v7, v3, v7, s[44:45]
	v_fma_f32 v3, -v9, v3, v1
	v_cmp_lt_f32_e64 s[44:45], 0, v3
	s_nop 1
	v_cndmask_b32_e64 v3, v7, v9, s[44:45]
	v_mul_f32_e32 v7, 0x37800000, v3
	v_cndmask_b32_e32 v3, v3, v7, vcc
	v_cmp_class_f32_e32 vcc, v1, v242
	s_nop 1
	v_cndmask_b32_e32 v1, v3, v1, vcc
	v_div_scale_f32 v3, s[44:45], v1, v1, 1.0
	v_rcp_f32_e32 v7, v3
	s_nop 0
	v_fma_f32 v9, -v3, v7, 1.0
	v_fmac_f32_e32 v7, v9, v7
	v_div_scale_f32 v9, vcc, 1.0, v1, 1.0
	v_mul_f32_e32 v10, v9, v7
	v_fma_f32 v11, -v3, v10, v9
	v_fmac_f32_e32 v10, v11, v7
	v_fma_f32 v3, -v3, v10, v9
	v_div_fmas_f32 v3, v3, v7, v10
	v_div_fixup_f32 v9, v3, v1, 1.0
	v_mov_b32_e32 v1, s21
	ds_write_b64 v1, v[8:9]
; __device__ __forceinline__ void unpk8(const u32x4 w, f32x4& a, f32x4& b) { a = (f32x4){bflo(w.x), bfhi(w.x), bflo(w.y), bfhi(w.y)}; b = (f32x4){bflo(w.z), bfhi(w.z), bflo(w.w), bfhi(w.w)}; }
; __device__ __forceinline__ void gmlp_unit(Frame& F, const Args& a, int layer, int unit) {
;     ...
;     for (int r = 0; r < 16; ++r) { const int tok = wave * 16 + r; const bf16* rowp = GUV + (t0 + tok) * 2048 + 1024;
;         f32x4 x0, x1, x2, x3; unpk8(*(const v4u*)(rowp + lane * 8), x0, x1); unpk8(*(const v4u*)(rowp + 512 + lane * 8), x2, x3);
;         const f32x4 sv = (x0 + x1) + (x2 + x3), qv = (x0 * x0 + x1 * x1) + (x2 * x2 + x3 * x3);
;         const float s = wave_sum((sv.x + sv.y) + (sv.z + sv.w)), q = wave_sum((qv.x + qv.y) + (qv.z + qv.w));
;         const float mean = s * (1.f / 1024.f), var = fmaxf(q * (1.f / 1024.f) - mean * mean, 0.f);
;         if (lane == 0) { st[tok * 2] = mean; st[tok * 2 + 1] = 1.f / sqrtf(var + 1e-5f); } }
.Lgm_u2_st10:
	s_or_b64 exec, exec, s[38:39]
	s_add_i32 s3, s3, 8
	s_waitcnt vmcnt(8)
	v_lshlrev_b32_e32 v16, 16, v124
	v_and_b32_e32 v17, 0xffff0000, v124
	v_lshlrev_b32_e32 v8, 16, v125
	v_and_b32_e32 v9, 0xffff0000, v125
	v_lshlrev_b32_e32 v18, 16, v126
	v_and_b32_e32 v19, 0xffff0000, v126
	v_lshlrev_b32_e32 v10, 16, v127
	v_and_b32_e32 v11, 0xffff0000, v127
	v_lshlrev_b32_e32 v20, 16, v128
	v_and_b32_e32 v21, 0xffff0000, v128
	v_lshlrev_b32_e32 v12, 16, v129
	v_and_b32_e32 v13, 0xffff0000, v129
	v_lshlrev_b32_e32 v22, 16, v130
	v_and_b32_e32 v23, 0xffff0000, v130
	v_lshlrev_b32_e32 v14, 16, v131
	v_and_b32_e32 v15, 0xffff0000, v131
	v_pk_add_f32 v[24:25], v[16:17], v[18:19]
	v_pk_add_f32 v[26:27], v[8:9], v[10:11]
	v_pk_add_f32 v[28:29], v[20:21], v[22:23]
	v_pk_add_f32 v[30:31], v[12:13], v[14:15]
	v_pk_mul_f32 v[10:11], v[10:11], v[10:11]
	v_pk_mul_f32 v[18:19], v[18:19], v[18:19]
	v_pk_mul_f32 v[14:15], v[14:15], v[14:15]
	v_pk_mul_f32 v[22:23], v[22:23], v[22:23]
	v_pk_add_f32 v[26:27], v[26:27], v[30:31]
	v_pk_add_f32 v[24:25], v[24:25], v[28:29]
	v_pk_fma_f32 v[16:17], v[16:17], v[16:17], v[18:19]
	v_pk_fma_f32 v[8:9], v[8:9], v[8:9], v[10:11]
	v_pk_fma_f32 v[10:11], v[20:21], v[20:21], v[22:23]
	v_pk_fma_f32 v[12:13], v[12:13], v[12:13], v[14:15]
	v_pk_add_f32 v[10:11], v[16:17], v[10:11]
	v_pk_add_f32 v[8:9], v[8:9], v[12:13]
	v_add_f32_e32 v1, v24, v25
	v_add_f32_e32 v3, v26, v27
	v_add_f32_e32 v1, v1, v3
	v_add_f32_e32 v3, v10, v11
	v_add_f32_e32 v7, v8, v9
	v_add_f32_e32 v3, v3, v7
	v_add_f32_dpp v1, v1, v1 quad_perm:[1,0,3,2] row_mask:0xf bank_mask:0xf bound_ctrl:1
	s_nop 0
	v_add_f32_dpp v3, v3, v3 quad_perm:[1,0,3,2] row_mask:0xf bank_mask:0xf bound_ctrl:1
	v_add_f32_dpp v1, v1, v1 quad_perm:[2,3,0,1] row_mask:0xf bank_mask:0xf bound_ctrl:1
	s_nop 0
	v_add_f32_dpp v3, v3, v3 quad_perm:[2,3,0,1] row_mask:0xf bank_mask:0xf bound_ctrl:1
	v_add_f32_dpp v1, v1, v1 row_half_mirror row_mask:0xf bank_mask:0xf bound_ctrl:1
	s_nop 0
	v_add_f32_dpp v3, v3, v3 row_half_mirror row_mask:0xf bank_mask:0xf bound_ctrl:1
	v_add_f32_dpp v1, v1, v1 row_mirror row_mask:0xf bank_mask:0xf bound_ctrl:1
	v_mov_b32_e32 v7, v1
	v_add_f32_dpp v8, v3, v3 row_mirror row_mask:0xf bank_mask:0xf bound_ctrl:1
	v_mov_b32_e32 v9, v8
	v_permlane16_swap_b32_e32 v1, v7
	s_nop 0
	v_permlane16_swap_b32_e32 v8, v9
	v_add_f32_e32 v1, v1, v7
	v_add_f32_e32 v7, v8, v9
	v_mov_b32_e32 v3, v1
	v_mov_b32_e32 v8, v7
	s_nop 0
	v_permlane32_swap_b32_e32 v1, v3
	v_permlane32_swap_b32_e32 v7, v8
	s_and_saveexec_b64 s[38:39], s[42:43]
	s_cbranch_execz .Lgm_u2_st11
	v_add_f32_e32 v1, v1, v3
	v_add_f32_e32 v7, v7, v8
	v_mul_f32_e32 v8, 0x3a800000, v1
	v_mul_f32_e32 v1, v8, v8
	v_fma_f32 v1, v7, s13, -v1
	v_max_f32_e32 v1, 0, v1
	v_add_f32_e32 v1, 0x3727c5ac, v1
	v_mul_f32_e32 v3, 0x4f800000, v1
	v_cmp_gt_f32_e32 vcc, s69, v1
	s_add_i32 s21, s11, s3
	s_nop 0
	v_cndmask_b32_e32 v1, v1, v3, vcc
	v_sqrt_f32_e32 v3, v1
	s_nop 0
	v_add_u32_e32 v7, -1, v3
	v_fma_f32 v9, -v7, v3, v1
	v_cmp_ge_f32_e64 s[44:45], 0, v9
	v_add_u32_e32 v9, 1, v3
	s_nop 0
	v_cndmask_b32_e64 v7, v3, v7, s[44:45]
	v_fma_f32 v3, -v9, v3, v1
	v_cmp_lt_f32_e64 s[44:45], 0, v3
	s_nop 1
	v_cndmask_b32_e64 v3, v7, v9, s[44:45]
	v_mul_f32_e32 v7, 0x37800000, v3
	v_cndmask_b32_e32 v3, v3, v7, vcc
	v_cmp_class_f32_e32 vcc, v1, v242
	s_nop 1
	v_cndmask_b32_e32 v1, v3, v1, vcc
	v_div_scale_f32 v3, s[44:45], v1, v1, 1.0
	v_rcp_f32_e32 v7, v3
	s_nop 0
	v_fma_f32 v9, -v3, v7, 1.0
	v_fmac_f32_e32 v7, v9, v7
	v_div_scale_f32 v9, vcc, 1.0, v1, 1.0
	v_mul_f32_e32 v10, v9, v7
	v_fma_f32 v11, -v3, v10, v9
	v_fmac_f32_e32 v10, v11, v7
	v_fma_f32 v3, -v3, v10, v9
	v_div_fmas_f32 v3, v3, v7, v10
	v_div_fixup_f32 v9, v3, v1, 1.0
	v_mov_b32_e32 v1, s21
	ds_write_b64 v1, v[8:9]
.Lgm_u2_st11:
	s_or_b64 exec, exec, s[38:39]
	s_add_i32 s3, s3, 8
	s_waitcnt vmcnt(6)
	v_lshlrev_b32_e32 v16, 16, v132
	v_and_b32_e32 v17, 0xffff0000, v132
	v_lshlrev_b32_e32 v8, 16, v133
	v_and_b32_e32 v9, 0xffff0000, v133
	v_lshlrev_b32_e32 v18, 16, v134
	v_and_b32_e32 v19, 0xffff0000, v134
	v_lshlrev_b32_e32 v10, 16, v135
	v_and_b32_e32 v11, 0xffff0000, v135
	v_lshlrev_b32_e32 v20, 16, v136
	v_and_b32_e32 v21, 0xffff0000, v136
	v_lshlrev_b32_e32 v12, 16, v137
	v_and_b32_e32 v13, 0xffff0000, v137
	v_lshlrev_b32_e32 v22, 16, v138
	v_and_b32_e32 v23, 0xffff0000, v138
	v_lshlrev_b32_e32 v14, 16, v139
	v_and_b32_e32 v15, 0xffff0000, v139
	v_pk_add_f32 v[24:25], v[16:17], v[18:19]
	v_pk_add_f32 v[26:27], v[8:9], v[10:11]
	v_pk_add_f32 v[28:29], v[20:21], v[22:23]
	v_pk_add_f32 v[30:31], v[12:13], v[14:15]
	v_pk_mul_f32 v[10:11], v[10:11], v[10:11]
	v_pk_mul_f32 v[18:19], v[18:19], v[18:19]
	v_pk_mul_f32 v[14:15], v[14:15], v[14:15]
	v_pk_mul_f32 v[22:23], v[22:23], v[22:23]
	v_pk_add_f32 v[26:27], v[26:27], v[30:31]
	v_pk_add_f32 v[24:25], v[24:25], v[28:29]
	v_pk_fma_f32 v[16:17], v[16:17], v[16:17], v[18:19]
	v_pk_fma_f32 v[8:9], v[8:9], v[8:9], v[10:11]
	v_pk_fma_f32 v[10:11], v[20:21], v[20:21], v[22:23]
	v_pk_fma_f32 v[12:13], v[12:13], v[12:13], v[14:15]
	v_pk_add_f32 v[10:11], v[16:17], v[10:11]
	v_pk_add_f32 v[8:9], v[8:9], v[12:13]
	v_add_f32_e32 v1, v24, v25
	v_add_f32_e32 v3, v26, v27
	v_add_f32_e32 v1, v1, v3
	v_add_f32_e32 v3, v10, v11
	v_add_f32_e32 v7, v8, v9
	v_add_f32_e32 v3, v3, v7
	v_add_f32_dpp v1, v1, v1 quad_perm:[1,0,3,2] row_mask:0xf bank_mask:0xf bound_ctrl:1
	s_nop 0
	v_add_f32_dpp v3, v3, v3 quad_perm:[1,0,3,2] row_mask:0xf bank_mask:0xf bound_ctrl:1
	v_add_f32_dpp v1, v1, v1 quad_perm:[2,3,0,1] row_mask:0xf bank_mask:0xf bound_ctrl:1
	s_nop 0
	v_add_f32_dpp v3, v3, v3 quad_perm:[2,3,0,1] row_mask:0xf bank_mask:0xf bound_ctrl:1
	v_add_f32_dpp v1, v1, v1 row_half_mirror row_mask:0xf bank_mask:0xf bound_ctrl:1
	s_nop 0
	v_add_f32_dpp v3, v3, v3 row_half_mirror row_mask:0xf bank_mask:0xf bound_ctrl:1
	v_add_f32_dpp v1, v1, v1 row_mirror row_mask:0xf bank_mask:0xf bound_ctrl:1
	v_mov_b32_e32 v7, v1
	v_add_f32_dpp v8, v3, v3 row_mirror row_mask:0xf bank_mask:0xf bound_ctrl:1
	v_mov_b32_e32 v9, v8
	v_permlane16_swap_b32_e32 v1, v7
	s_nop 0
	v_permlane16_swap_b32_e32 v8, v9
	v_add_f32_e32 v1, v1, v7
	v_add_f32_e32 v7, v8, v9
	v_mov_b32_e32 v3, v1
	v_mov_b32_e32 v8, v7
	s_nop 0
	v_permlane32_swap_b32_e32 v1, v3
	v_permlane32_swap_b32_e32 v7, v8
	s_and_saveexec_b64 s[38:39], s[42:43]
	s_cbranch_execz .Lgm_u2_st12
; __device__ __forceinline__ void unpk8(const u32x4 w, f32x4& a, f32x4& b) { a = (f32x4){bflo(w.x), bfhi(w.x), bflo(w.y), bfhi(w.y)}; b = (f32x4){bflo(w.z), bfhi(w.z), bflo(w.w), bfhi(w.w)}; }
; __device__ __forceinline__ void gmlp_unit(Frame& F, const Args& a, int layer, int unit) {
;     ...
;     for (int r = 0; r < 16; ++r) { const int tok = wave * 16 + r; const bf16* rowp = GUV + (t0 + tok) * 2048 + 1024;
;         f32x4 x0, x1, x2, x3; unpk8(*(const v4u*)(rowp + lane * 8), x0, x1); unpk8(*(const v4u*)(rowp + 512 + lane * 8), x2, x3);
;         const f32x4 sv = (x0 + x1) + (x2 + x3), qv = (x0 * x0 + x1 * x1) + (x2 * x2 + x3 * x3);
;         const float s = wave_sum((sv.x + sv.y) + (sv.z + sv.w)), q = wave_sum((qv.x + qv.y) + (qv.z + qv.w));
;         const float mean = s * (1.f / 1024.f), var = fmaxf(q * (1.f / 1024.f) - mean * mean, 0.f);
;         if (lane == 0) { st[tok * 2] = mean; st[tok * 2 + 1] = 1.f / sqrtf(var + 1e-5f); } }
	v_add_f32_e32 v1, v1, v3
	v_add_f32_e32 v7, v7, v8
	v_mul_f32_e32 v8, 0x3a800000, v1
	v_mul_f32_e32 v1, v8, v8
	v_fma_f32 v1, v7, s13, -v1
	v_max_f32_e32 v1, 0, v1
	v_add_f32_e32 v1, 0x3727c5ac, v1
	v_mul_f32_e32 v3, 0x4f800000, v1
	v_cmp_gt_f32_e32 vcc, s69, v1
	s_add_i32 s21, s11, s3
	s_nop 0
	v_cndmask_b32_e32 v1, v1, v3, vcc
	v_sqrt_f32_e32 v3, v1
	s_nop 0
	v_add_u32_e32 v7, -1, v3
	v_fma_f32 v9, -v7, v3, v1
	v_cmp_ge_f32_e64 s[44:45], 0, v9
	v_add_u32_e32 v9, 1, v3
	s_nop 0
	v_cndmask_b32_e64 v7, v3, v7, s[44:45]
	v_fma_f32 v3, -v9, v3, v1
	v_cmp_lt_f32_e64 s[44:45], 0, v3
	s_nop 1
	v_cndmask_b32_e64 v3, v7, v9, s[44:45]
	v_mul_f32_e32 v7, 0x37800000, v3
	v_cndmask_b32_e32 v3, v3, v7, vcc
	v_cmp_class_f32_e32 vcc, v1, v242
	s_nop 1
	v_cndmask_b32_e32 v1, v3, v1, vcc
	v_div_scale_f32 v3, s[44:45], v1, v1, 1.0
	v_rcp_f32_e32 v7, v3
	s_nop 0
	v_fma_f32 v9, -v3, v7, 1.0
	v_fmac_f32_e32 v7, v9, v7
	v_div_scale_f32 v9, vcc, 1.0, v1, 1.0
	v_mul_f32_e32 v10, v9, v7
	v_fma_f32 v11, -v3, v10, v9
	v_fmac_f32_e32 v10, v11, v7
	v_fma_f32 v3, -v3, v10, v9
	v_div_fmas_f32 v3, v3, v7, v10
	v_div_fixup_f32 v9, v3, v1, 1.0
	v_mov_b32_e32 v1, s21
	ds_write_b64 v1, v[8:9]
.Lgm_u2_st12:
	s_or_b64 exec, exec, s[38:39]
	s_add_i32 s3, s3, 8
	s_waitcnt vmcnt(4)
	v_lshlrev_b32_e32 v16, 16, v140
	v_and_b32_e32 v17, 0xffff0000, v140
	v_lshlrev_b32_e32 v8, 16, v141
	v_and_b32_e32 v9, 0xffff0000, v141
	v_lshlrev_b32_e32 v18, 16, v142
	v_and_b32_e32 v19, 0xffff0000, v142
	v_lshlrev_b32_e32 v10, 16, v143
	v_and_b32_e32 v11, 0xffff0000, v143
	v_lshlrev_b32_e32 v20, 16, v144
	v_and_b32_e32 v21, 0xffff0000, v144
	v_lshlrev_b32_e32 v12, 16, v145
	v_and_b32_e32 v13, 0xffff0000, v145
	v_lshlrev_b32_e32 v22, 16, v146
	v_and_b32_e32 v23, 0xffff0000, v146
	v_lshlrev_b32_e32 v14, 16, v147
	v_and_b32_e32 v15, 0xffff0000, v147
	v_pk_add_f32 v[24:25], v[16:17], v[18:19]
	v_pk_add_f32 v[26:27], v[8:9], v[10:11]
	v_pk_add_f32 v[28:29], v[20:21], v[22:23]
	v_pk_add_f32 v[30:31], v[12:13], v[14:15]
	v_pk_mul_f32 v[10:11], v[10:11], v[10:11]
	v_pk_mul_f32 v[18:19], v[18:19], v[18:19]
	v_pk_mul_f32 v[14:15], v[14:15], v[14:15]
	v_pk_mul_f32 v[22:23], v[22:23], v[22:23]
	v_pk_add_f32 v[26:27], v[26:27], v[30:31]
	v_pk_add_f32 v[24:25], v[24:25], v[28:29]
	v_pk_fma_f32 v[16:17], v[16:17], v[16:17], v[18:19]
	v_pk_fma_f32 v[8:9], v[8:9], v[8:9], v[10:11]
	v_pk_fma_f32 v[10:11], v[20:21], v[20:21], v[22:23]
	v_pk_fma_f32 v[12:13], v[12:13], v[12:13], v[14:15]
	v_pk_add_f32 v[10:11], v[16:17], v[10:11]
	v_pk_add_f32 v[8:9], v[8:9], v[12:13]
	v_add_f32_e32 v1, v24, v25
	v_add_f32_e32 v3, v26, v27
	v_add_f32_e32 v1, v1, v3
	v_add_f32_e32 v3, v10, v11
	v_add_f32_e32 v7, v8, v9
	v_add_f32_e32 v3, v3, v7
	v_add_f32_dpp v1, v1, v1 quad_perm:[1,0,3,2] row_mask:0xf bank_mask:0xf bound_ctrl:1
	s_nop 0
	v_add_f32_dpp v3, v3, v3 quad_perm:[1,0,3,2] row_mask:0xf bank_mask:0xf bound_ctrl:1
	v_add_f32_dpp v1, v1, v1 quad_perm:[2,3,0,1] row_mask:0xf bank_mask:0xf bound_ctrl:1
	s_nop 0
	v_add_f32_dpp v3, v3, v3 quad_perm:[2,3,0,1] row_mask:0xf bank_mask:0xf bound_ctrl:1
	v_add_f32_dpp v1, v1, v1 row_half_mirror row_mask:0xf bank_mask:0xf bound_ctrl:1
	s_nop 0
	v_add_f32_dpp v3, v3, v3 row_half_mirror row_mask:0xf bank_mask:0xf bound_ctrl:1
	v_add_f32_dpp v1, v1, v1 row_mirror row_mask:0xf bank_mask:0xf bound_ctrl:1
	v_mov_b32_e32 v7, v1
	v_add_f32_dpp v8, v3, v3 row_mirror row_mask:0xf bank_mask:0xf bound_ctrl:1
	v_mov_b32_e32 v9, v8
	v_permlane16_swap_b32_e32 v1, v7
	s_nop 0
	v_permlane16_swap_b32_e32 v8, v9
	v_add_f32_e32 v1, v1, v7
	v_add_f32_e32 v7, v8, v9
	v_mov_b32_e32 v3, v1
	v_mov_b32_e32 v8, v7
	s_nop 0
	v_permlane32_swap_b32_e32 v1, v3
	v_permlane32_swap_b32_e32 v7, v8
	s_and_saveexec_b64 s[38:39], s[42:43]
	s_cbranch_execz .Lgm_u2_st13
	v_add_f32_e32 v1, v1, v3
	v_add_f32_e32 v7, v7, v8
	v_mul_f32_e32 v8, 0x3a800000, v1
	v_mul_f32_e32 v1, v8, v8
	v_fma_f32 v1, v7, s13, -v1
	v_max_f32_e32 v1, 0, v1
	v_add_f32_e32 v1, 0x3727c5ac, v1
	v_mul_f32_e32 v3, 0x4f800000, v1
	v_cmp_gt_f32_e32 vcc, s69, v1
	s_add_i32 s21, s11, s3
	s_nop 0
	v_cndmask_b32_e32 v1, v1, v3, vcc
	v_sqrt_f32_e32 v3, v1
	s_nop 0
	v_add_u32_e32 v7, -1, v3
	v_fma_f32 v9, -v7, v3, v1
	v_cmp_ge_f32_e64 s[44:45], 0, v9
	v_add_u32_e32 v9, 1, v3
	s_nop 0
	v_cndmask_b32_e64 v7, v3, v7, s[44:45]
	v_fma_f32 v3, -v9, v3, v1
	v_cmp_lt_f32_e64 s[44:45], 0, v3
	s_nop 1
	v_cndmask_b32_e64 v3, v7, v9, s[44:45]
	v_mul_f32_e32 v7, 0x37800000, v3
	v_cndmask_b32_e32 v3, v3, v7, vcc
	v_cmp_class_f32_e32 vcc, v1, v242
	s_nop 1
	v_cndmask_b32_e32 v1, v3, v1, vcc
	v_div_scale_f32 v3, s[44:45], v1, v1, 1.0
	v_rcp_f32_e32 v7, v3
	s_nop 0
	v_fma_f32 v9, -v3, v7, 1.0
	v_fmac_f32_e32 v7, v9, v7
	v_div_scale_f32 v9, vcc, 1.0, v1, 1.0
	v_mul_f32_e32 v10, v9, v7
	v_fma_f32 v11, -v3, v10, v9
	v_fmac_f32_e32 v10, v11, v7
	v_fma_f32 v3, -v3, v10, v9
	v_div_fmas_f32 v3, v3, v7, v10
	v_div_fixup_f32 v9, v3, v1, 1.0
	v_mov_b32_e32 v1, s21
	ds_write_b64 v1, v[8:9]
; __device__ __forceinline__ void unpk8(const u32x4 w, f32x4& a, f32x4& b) { a = (f32x4){bflo(w.x), bfhi(w.x), bflo(w.y), bfhi(w.y)}; b = (f32x4){bflo(w.z), bfhi(w.z), bflo(w.w), bfhi(w.w)}; }
; __device__ __forceinline__ void gmlp_unit(Frame& F, const Args& a, int layer, int unit) {
;     ...
;     for (int r = 0; r < 16; ++r) { const int tok = wave * 16 + r; const bf16* rowp = GUV + (t0 + tok) * 2048 + 1024;
;         f32x4 x0, x1, x2, x3; unpk8(*(const v4u*)(rowp + lane * 8), x0, x1); unpk8(*(const v4u*)(rowp + 512 + lane * 8), x2, x3);
;         const f32x4 sv = (x0 + x1) + (x2 + x3), qv = (x0 * x0 + x1 * x1) + (x2 * x2 + x3 * x3);
;         const float s = wave_sum((sv.x + sv.y) + (sv.z + sv.w)), q = wave_sum((qv.x + qv.y) + (qv.z + qv.w));
;         const float mean = s * (1.f / 1024.f), var = fmaxf(q * (1.f / 1024.f) - mean * mean, 0.f);
;         if (lane == 0) { st[tok * 2] = mean; st[tok * 2 + 1] = 1.f / sqrtf(var + 1e-5f); } }
.Lgm_u2_st13:
	s_or_b64 exec, exec, s[38:39]
	s_add_i32 s3, s3, 8
	s_waitcnt vmcnt(2)
	v_lshlrev_b32_e32 v16, 16, v148
	v_and_b32_e32 v17, 0xffff0000, v148
	v_lshlrev_b32_e32 v8, 16, v149
	v_and_b32_e32 v9, 0xffff0000, v149
	v_lshlrev_b32_e32 v18, 16, v150
	v_and_b32_e32 v19, 0xffff0000, v150
	v_lshlrev_b32_e32 v10, 16, v151
	v_and_b32_e32 v11, 0xffff0000, v151
	v_lshlrev_b32_e32 v20, 16, v152
	v_and_b32_e32 v21, 0xffff0000, v152
	v_lshlrev_b32_e32 v12, 16, v153
	v_and_b32_e32 v13, 0xffff0000, v153
	v_lshlrev_b32_e32 v22, 16, v154
	v_and_b32_e32 v23, 0xffff0000, v154
	v_lshlrev_b32_e32 v14, 16, v155
	v_and_b32_e32 v15, 0xffff0000, v155
	v_pk_add_f32 v[24:25], v[16:17], v[18:19]
	v_pk_add_f32 v[26:27], v[8:9], v[10:11]
	v_pk_add_f32 v[28:29], v[20:21], v[22:23]
	v_pk_add_f32 v[30:31], v[12:13], v[14:15]
	v_pk_mul_f32 v[10:11], v[10:11], v[10:11]
	v_pk_mul_f32 v[18:19], v[18:19], v[18:19]
	v_pk_mul_f32 v[14:15], v[14:15], v[14:15]
	v_pk_mul_f32 v[22:23], v[22:23], v[22:23]
	v_pk_add_f32 v[26:27], v[26:27], v[30:31]
	v_pk_add_f32 v[24:25], v[24:25], v[28:29]
	v_pk_fma_f32 v[16:17], v[16:17], v[16:17], v[18:19]
	v_pk_fma_f32 v[8:9], v[8:9], v[8:9], v[10:11]
	v_pk_fma_f32 v[10:11], v[20:21], v[20:21], v[22:23]
	v_pk_fma_f32 v[12:13], v[12:13], v[12:13], v[14:15]
	v_pk_add_f32 v[10:11], v[16:17], v[10:11]
	v_pk_add_f32 v[8:9], v[8:9], v[12:13]
	v_add_f32_e32 v1, v24, v25
	v_add_f32_e32 v3, v26, v27
	v_add_f32_e32 v1, v1, v3
	v_add_f32_e32 v3, v10, v11
	v_add_f32_e32 v7, v8, v9
	v_add_f32_e32 v3, v3, v7
	v_add_f32_dpp v1, v1, v1 quad_perm:[1,0,3,2] row_mask:0xf bank_mask:0xf bound_ctrl:1
	s_nop 0
	v_add_f32_dpp v3, v3, v3 quad_perm:[1,0,3,2] row_mask:0xf bank_mask:0xf bound_ctrl:1
	v_add_f32_dpp v1, v1, v1 quad_perm:[2,3,0,1] row_mask:0xf bank_mask:0xf bound_ctrl:1
	s_nop 0
	v_add_f32_dpp v3, v3, v3 quad_perm:[2,3,0,1] row_mask:0xf bank_mask:0xf bound_ctrl:1
	v_add_f32_dpp v1, v1, v1 row_half_mirror row_mask:0xf bank_mask:0xf bound_ctrl:1
	s_nop 0
	v_add_f32_dpp v3, v3, v3 row_half_mirror row_mask:0xf bank_mask:0xf bound_ctrl:1
	v_add_f32_dpp v1, v1, v1 row_mirror row_mask:0xf bank_mask:0xf bound_ctrl:1
	v_mov_b32_e32 v7, v1
	v_add_f32_dpp v8, v3, v3 row_mirror row_mask:0xf bank_mask:0xf bound_ctrl:1
	v_mov_b32_e32 v9, v8
	v_permlane16_swap_b32_e32 v1, v7
	s_nop 0
	v_permlane16_swap_b32_e32 v8, v9
	v_add_f32_e32 v1, v1, v7
	v_add_f32_e32 v7, v8, v9
	v_mov_b32_e32 v3, v1
	v_mov_b32_e32 v8, v7
	s_nop 0
	v_permlane32_swap_b32_e32 v1, v3
	v_permlane32_swap_b32_e32 v7, v8
	s_and_saveexec_b64 s[38:39], s[42:43]
	s_cbranch_execz .Lgm_u2_st14
	v_add_f32_e32 v1, v1, v3
	v_add_f32_e32 v7, v7, v8
	v_mul_f32_e32 v8, 0x3a800000, v1
	v_mul_f32_e32 v1, v8, v8
	v_fma_f32 v1, v7, s13, -v1
	v_max_f32_e32 v1, 0, v1
	v_add_f32_e32 v1, 0x3727c5ac, v1
	v_mul_f32_e32 v3, 0x4f800000, v1
	v_cmp_gt_f32_e32 vcc, s69, v1
	s_add_i32 s21, s11, s3
	s_nop 0
	v_cndmask_b32_e32 v1, v1, v3, vcc
	v_sqrt_f32_e32 v3, v1
	s_nop 0
	v_add_u32_e32 v7, -1, v3
	v_fma_f32 v9, -v7, v3, v1
	v_cmp_ge_f32_e64 s[44:45], 0, v9
	v_add_u32_e32 v9, 1, v3
	s_nop 0
	v_cndmask_b32_e64 v7, v3, v7, s[44:45]
	v_fma_f32 v3, -v9, v3, v1
	v_cmp_lt_f32_e64 s[44:45], 0, v3
	s_nop 1
	v_cndmask_b32_e64 v3, v7, v9, s[44:45]
	v_mul_f32_e32 v7, 0x37800000, v3
	v_cndmask_b32_e32 v3, v3, v7, vcc
	v_cmp_class_f32_e32 vcc, v1, v242
	s_nop 1
	v_cndmask_b32_e32 v1, v3, v1, vcc
	v_div_scale_f32 v3, s[44:45], v1, v1, 1.0
	v_rcp_f32_e32 v7, v3
	s_nop 0
	v_fma_f32 v9, -v3, v7, 1.0
	v_fmac_f32_e32 v7, v9, v7
	v_div_scale_f32 v9, vcc, 1.0, v1, 1.0
	v_mul_f32_e32 v10, v9, v7
	v_fma_f32 v11, -v3, v10, v9
	v_fmac_f32_e32 v10, v11, v7
	v_fma_f32 v3, -v3, v10, v9
	v_div_fmas_f32 v3, v3, v7, v10
	v_div_fixup_f32 v9, v3, v1, 1.0
	v_mov_b32_e32 v1, s21
	ds_write_b64 v1, v[8:9]
.Lgm_u2_st14:
	s_or_b64 exec, exec, s[38:39]
	s_add_i32 s3, s3, 8
	s_waitcnt vmcnt(0)
	v_lshlrev_b32_e32 v16, 16, v156
	v_and_b32_e32 v17, 0xffff0000, v156
	v_lshlrev_b32_e32 v8, 16, v157
	v_and_b32_e32 v9, 0xffff0000, v157
	v_lshlrev_b32_e32 v18, 16, v158
	v_and_b32_e32 v19, 0xffff0000, v158
	v_lshlrev_b32_e32 v10, 16, v159
	v_and_b32_e32 v11, 0xffff0000, v159
	v_lshlrev_b32_e32 v20, 16, v160
	v_and_b32_e32 v21, 0xffff0000, v160
	v_lshlrev_b32_e32 v12, 16, v161
	v_and_b32_e32 v13, 0xffff0000, v161
	v_lshlrev_b32_e32 v22, 16, v162
	v_and_b32_e32 v23, 0xffff0000, v162
	v_lshlrev_b32_e32 v14, 16, v163
	v_and_b32_e32 v15, 0xffff0000, v163
	v_pk_add_f32 v[24:25], v[16:17], v[18:19]
	v_pk_add_f32 v[26:27], v[8:9], v[10:11]
	v_pk_add_f32 v[28:29], v[20:21], v[22:23]
	v_pk_add_f32 v[30:31], v[12:13], v[14:15]
	v_pk_mul_f32 v[10:11], v[10:11], v[10:11]
	v_pk_mul_f32 v[18:19], v[18:19], v[18:19]
	v_pk_mul_f32 v[14:15], v[14:15], v[14:15]
	v_pk_mul_f32 v[22:23], v[22:23], v[22:23]
	v_pk_add_f32 v[26:27], v[26:27], v[30:31]
	v_pk_add_f32 v[24:25], v[24:25], v[28:29]
	v_pk_fma_f32 v[16:17], v[16:17], v[16:17], v[18:19]
	v_pk_fma_f32 v[8:9], v[8:9], v[8:9], v[10:11]
	v_pk_fma_f32 v[10:11], v[20:21], v[20:21], v[22:23]
	v_pk_fma_f32 v[12:13], v[12:13], v[12:13], v[14:15]
	v_pk_add_f32 v[10:11], v[16:17], v[10:11]
	v_pk_add_f32 v[8:9], v[8:9], v[12:13]
	v_add_f32_e32 v1, v24, v25
	v_add_f32_e32 v3, v26, v27
	v_add_f32_e32 v1, v1, v3
	v_add_f32_e32 v3, v10, v11
	v_add_f32_e32 v7, v8, v9
	v_add_f32_e32 v3, v3, v7
	v_add_f32_dpp v1, v1, v1 quad_perm:[1,0,3,2] row_mask:0xf bank_mask:0xf bound_ctrl:1
	s_nop 0
	v_add_f32_dpp v3, v3, v3 quad_perm:[1,0,3,2] row_mask:0xf bank_mask:0xf bound_ctrl:1
	v_add_f32_dpp v1, v1, v1 quad_perm:[2,3,0,1] row_mask:0xf bank_mask:0xf bound_ctrl:1
	s_nop 0
	v_add_f32_dpp v3, v3, v3 quad_perm:[2,3,0,1] row_mask:0xf bank_mask:0xf bound_ctrl:1
	v_add_f32_dpp v1, v1, v1 row_half_mirror row_mask:0xf bank_mask:0xf bound_ctrl:1
	s_nop 0
	v_add_f32_dpp v3, v3, v3 row_half_mirror row_mask:0xf bank_mask:0xf bound_ctrl:1
	v_add_f32_dpp v1, v1, v1 row_mirror row_mask:0xf bank_mask:0xf bound_ctrl:1
	v_mov_b32_e32 v7, v1
	v_add_f32_dpp v8, v3, v3 row_mirror row_mask:0xf bank_mask:0xf bound_ctrl:1
	v_mov_b32_e32 v9, v8
	v_permlane16_swap_b32_e32 v1, v7
	s_nop 0
	v_permlane16_swap_b32_e32 v8, v9
	v_add_f32_e32 v1, v1, v7
	v_add_f32_e32 v7, v8, v9
	v_mov_b32_e32 v3, v1
	v_mov_b32_e32 v8, v7
	s_nop 0
	v_permlane32_swap_b32_e32 v1, v3
	v_permlane32_swap_b32_e32 v7, v8
	s_and_saveexec_b64 s[38:39], s[42:43]
	s_cbranch_execz .Lgm_u2_st15
; #define LAS __attribute__((address_space(3)))
; __device__ __forceinline__ void gmlp_unit(Frame& F, const Args& a, int layer, int unit) {
;     ...
;     for (int r = 0; r < 16; ++r) { const int tok = wave * 16 + r; const bf16* rowp = GUV + (t0 + tok) * 2048 + 1024;
;         f32x4 x0, x1, x2, x3; unpk8(*(const v4u*)(rowp + lane * 8), x0, x1); unpk8(*(const v4u*)(rowp + 512 + lane * 8), x2, x3);
;         const f32x4 sv = (x0 + x1) + (x2 + x3), qv = (x0 * x0 + x1 * x1) + (x2 * x2 + x3 * x3);
;         const float s = wave_sum((sv.x + sv.y) + (sv.z + sv.w)), q = wave_sum((qv.x + qv.y) + (qv.z + qv.w));
;         const float mean = s * (1.f / 1024.f), var = fmaxf(q * (1.f / 1024.f) - mean * mean, 0.f);
;         if (lane == 0) { st[tok * 2] = mean; st[tok * 2 + 1] = 1.f / sqrtf(var + 1e-5f); } }
;     ...
;     for (int g = 0; g < 8; ++g) {
; #pragma unroll
;         for (int i = 0; i < 4; ++i) { const int pc = tid + 512 * i, rr = pc >> 4, c16 = pc & 15;
;             *(LAS v4u*)(sA + rr * TP + c16 * 8) = *(const v4u*)(GMW + (size_t)g * 16384 + rr * 128 + c16 * 8); }
;         { const int p = tid & 127, oc0 = tid >> 7; const float mean = st[p * 2], rstd = st[p * 2 + 1];
; #pragma unroll
;           for (int i = 0; i < 4; ++i) { const int oc = oc0 + 4 * i, c0 = g * 128 + oc * 8;
;               f32x4 x0, x1; unpk8(*(const v4u*)(GUV + (t0 + p) * 2048 + 1024 + c0), x0, x1);
;               const f32x4 g0 = *(const f32x4*)(lng + c0), g1 = *(const f32x4*)(lng + c0 + 4), b0 = *(const f32x4*)(lnb + c0), b1 = *(const f32x4*)(lnb + c0 + 4);
;               x0 = (x0 - mean) * rstd * g0 + b0; x1 = (x1 - mean) * rstd * g1 + b1;
;               const v4u w = pk8(x0, x1);
;               LAS bf16* d = sB + (oc * 8) * TP + p;
;               d[0 * TP] = (bf16)(w.x & 0xffffu); d[1 * TP] = (bf16)(w.x >> 16); d[2 * TP] = (bf16)(w.y & 0xffffu); d[3 * TP] = (bf16)(w.y >> 16);
;               d[4 * TP] = (bf16)(w.z & 0xffffu); d[5 * TP] = (bf16)(w.z >> 16); d[6 * TP] = (bf16)(w.w & 0xffffu); d[7 * TP] = (bf16)(w.w >> 16); } }
;         __syncthreads();
;         f32x4 acc[4][2];
; #pragma unroll
;         for (int mt = 0; mt < 4; ++mt)
; #pragma unroll
;             for (int nt = 0; nt < 2; ++nt) acc[mt][nt] = (f32x4){0.f, 0.f, 0.f, 0.f};
;         mma_128(sA, sB, wave, lane, acc);
;         { const int wm = wave >> 2, wn = wave & 3, fr = lane & 15, fq = lane >> 4;
; #pragma unroll
	v_add_f32_e32 v1, v1, v3
	v_add_f32_e32 v7, v7, v8
	v_mul_f32_e32 v8, 0x3a800000, v1
	v_mul_f32_e32 v1, v8, v8
	v_fma_f32 v1, v7, s13, -v1
	v_max_f32_e32 v1, 0, v1
	v_add_f32_e32 v1, 0x3727c5ac, v1
	v_mul_f32_e32 v3, 0x4f800000, v1
	v_cmp_gt_f32_e32 vcc, s69, v1
	s_add_i32 s21, s11, s3
	s_nop 0
	v_cndmask_b32_e32 v1, v1, v3, vcc
	v_sqrt_f32_e32 v3, v1
	s_nop 0
	v_add_u32_e32 v7, -1, v3
	v_fma_f32 v9, -v7, v3, v1
	v_cmp_ge_f32_e64 s[44:45], 0, v9
	v_add_u32_e32 v9, 1, v3
	s_nop 0
	v_cndmask_b32_e64 v7, v3, v7, s[44:45]
	v_fma_f32 v3, -v9, v3, v1
	v_cmp_lt_f32_e64 s[44:45], 0, v3
	s_nop 1
	v_cndmask_b32_e64 v3, v7, v9, s[44:45]
	v_mul_f32_e32 v7, 0x37800000, v3
	v_cndmask_b32_e32 v3, v3, v7, vcc
	v_cmp_class_f32_e32 vcc, v1, v242
	s_nop 1
	v_cndmask_b32_e32 v1, v3, v1, vcc
	v_div_scale_f32 v3, s[44:45], v1, v1, 1.0
	v_rcp_f32_e32 v7, v3
	s_nop 0
	v_fma_f32 v9, -v3, v7, 1.0
	v_fmac_f32_e32 v7, v9, v7
	v_div_scale_f32 v9, vcc, 1.0, v1, 1.0
	v_mul_f32_e32 v10, v9, v7
	v_fma_f32 v11, -v3, v10, v9
	v_fmac_f32_e32 v10, v11, v7
	v_fma_f32 v3, -v3, v10, v9
	v_div_fmas_f32 v3, v3, v7, v10
	v_div_fixup_f32 v9, v3, v1, 1.0
	v_mov_b32_e32 v1, s21
	ds_write_b64 v1, v[8:9]
.Lgm_u2_st15:
	s_or_b64 exec, exec, s[38:39]
	s_add_i32 s3, s3, 8
.LBB0_838:
	s_or_b32 s22, s22, 1
	v_and_b32_e32 v19, 15, v6
	v_and_b32_e32 v4, -16, v6
	s_ashr_i32 s23, s22, 31
	v_add_u32_e32 v3, s27, v6
	v_add_u32_e32 v20, 0, v4
	v_or_b32_e32 v7, s75, v19
	v_or_b32_e32 v4, s77, v19
	v_ashrrev_i32_e32 v6, 2, v6
	s_lshl_b64 s[22:23], s[22:23], 7
	v_mul_u32_u24_e32 v22, 0x110, v7
	v_and_b32_e32 v23, -4, v6
	v_or_b32_e32 v6, 48, v4
	v_mov_b32_e32 v7, v0
	s_add_u32 s38, s6, 0x28400000
	v_lshl_add_u64 v[6:7], s[22:23], 0, v[6:7]
	s_addc_u32 s39, s7, 0
	v_ashrrev_i32_e32 v5, 4, v3
	s_movk_i32 s3, 0x110
	v_lshlrev_b64 v[6:7], 12, v[6:7]
	v_and_b32_e32 v1, 0x78, v2
	v_and_b32_e32 v2, -8, v5
	v_lshl_add_u64 v[26:27], s[38:39], 0, v[6:7]
	v_lshlrev_b32_e32 v6, 7, v5
	v_mul_lo_u32 v24, v5, s3
	v_add_u32_e32 v5, 0x200, v3
	v_ashrrev_i32_e32 v5, 4, v5
	v_lshlrev_b32_e32 v8, 7, v5
	v_mul_lo_u32 v25, v5, s3
	v_add_u32_e32 v5, 0x400, v3
	v_ashrrev_i32_e32 v5, 4, v5
	v_lshlrev_b32_e32 v10, 7, v5
	v_mul_lo_u32 v41, v5, s3
	v_mov_b32_e32 v5, v0
	v_lshl_add_u64 v[14:15], s[22:23], 0, v[4:5]
	v_lshlrev_b64 v[14:15], 12, v[14:15]
	v_mul_lo_u32 v21, v4, s3
	v_lshl_add_u64 v[28:29], s[38:39], 0, v[14:15]
	v_or_b32_e32 v14, 16, v4
	v_or_b32_e32 v4, 32, v4
	v_lshl_add_u64 v[4:5], s[22:23], 0, v[4:5]
	v_lshlrev_b64 v[4:5], 12, v[4:5]
	v_lshl_add_u64 v[32:33], s[38:39], 0, v[4:5]
	v_lshlrev_b32_e32 v4, 4, v19
	v_mov_b32_e32 v5, v0
	v_ashrrev_i32_e32 v7, 31, v6
	v_mov_b32_e32 v15, v0
	v_lshl_add_u64 v[4:5], s[0:1], 0, v[4:5]
	v_readlane_b32 s40, v251, 34
	v_and_b32_e32 v17, 0x7f, v3
	v_add_u32_e32 v3, 0x600, v3
	v_lshl_add_u64 v[14:15], s[22:23], 0, v[14:15]
	v_lshl_add_u64 v[34:35], v[6:7], 1, v[4:5]
	v_add_u32_e32 v6, s77, v19
	v_mov_b32_e32 v7, v0
	v_readlane_b32 s52, v251, 46
	v_readlane_b32 s53, v251, 47
	s_add_u32 s22, s36, 0x28400880
	v_ashrrev_i32_e32 v3, 4, v3
	v_lshl_add_u64 v[38:39], v[6:7], 2, s[52:53]
	s_addc_u32 s23, s37, 0
	v_lshlrev_b32_e32 v6, 12, v17
	v_lshl_add_u32 v16, v1, 1, 0
	v_lshl_add_u32 v1, v17, 3, 0
	v_lshlrev_b32_e32 v12, 7, v3
	v_mul_lo_u32 v52, v3, s3
	v_lshl_add_u64 v[6:7], s[22:23], 0, v[6:7]
	v_ashrrev_i32_e32 v3, 31, v2
	v_mad_i32_i24 v18, v17, -6, v1
	v_ashrrev_i32_e32 v9, 31, v8
	v_ashrrev_i32_e32 v11, 31, v10
	v_ashrrev_i32_e32 v13, 31, v12
	v_mul_lo_u32 v53, v2, s3
	v_lshlrev_b64 v[14:15], 12, v[14:15]
	v_readlane_b32 s46, v251, 40
	v_readlane_b32 s47, v251, 41
	v_readlane_b32 s48, v251, 42
	v_readlane_b32 s49, v251, 43
	v_lshl_add_u64 v[44:45], v[2:3], 1, v[6:7]
	v_lshlrev_b64 v[2:3], 2, v[2:3]
	v_lshl_add_u64 v[30:31], s[38:39], 0, v[14:15]
	v_lshl_add_u64 v[36:37], v[8:9], 1, v[4:5]
	v_add_u32_e32 v40, s75, v23
	v_lshl_add_u64 v[42:43], v[10:11], 1, v[4:5]
	v_lshl_add_u64 v[46:47], v[12:13], 1, v[4:5]
	v_lshl_add_u64 v[48:49], s[48:49], 0, v[2:3]
	v_lshl_add_u64 v[50:51], s[46:47], 0, v[2:3]
	s_mov_b64 s[22:23], 0
	v_add_u32_e32 v56, v16, v24
	v_add_u32_e32 v57, v16, v25
	v_add_u32_e32 v58, v16, v41
	v_add_u32_e32 v59, v16, v52
	v_add_u32_e32 v60, v18, v53
	v_add_u32_e32 v61, v20, v21
	v_add_u32_e32 v62, v20, v22
	s_waitcnt lgkmcnt(0)
	s_barrier
	v_readlane_b32 s41, v251, 35
	v_readlane_b32 s42, v251, 36
	v_readlane_b32 s43, v251, 37
	v_readlane_b32 s44, v251, 38
	v_readlane_b32 s45, v251, 39
	v_readlane_b32 s50, v251, 44
	v_readlane_b32 s51, v251, 45
	v_readlane_b32 s54, v251, 48
	v_readlane_b32 s55, v251, 49
; __device__ __forceinline__ void unpk8(const u32x4 w, f32x4& a, f32x4& b) { a = (f32x4){bflo(w.x), bfhi(w.x), bflo(w.y), bfhi(w.y)}; b = (f32x4){bflo(w.z), bfhi(w.z), bflo(w.w), bfhi(w.w)}; }
; __device__ __forceinline__ u32x4 pk8(const f32x4 a, const f32x4 b) { u32x4 w; w.x = cvt_pk_bf16(a[0], a[1]); w.y = cvt_pk_bf16(a[2], a[3]); w.z = cvt_pk_bf16(b[0], b[1]); w.w = cvt_pk_bf16(b[2], b[3]); return w; }
; #define LAS __attribute__((address_space(3)))
; __device__ __forceinline__ void gmlp_unit(Frame& F, const Args& a, int layer, int unit) {
;     ...
;     for (int g = 0; g < 8; ++g) {
; #pragma unroll
;         for (int i = 0; i < 4; ++i) { const int pc = tid + 512 * i, rr = pc >> 4, c16 = pc & 15;
;             *(LAS v4u*)(sA + rr * TP + c16 * 8) = *(const v4u*)(GMW + (size_t)g * 16384 + rr * 128 + c16 * 8); }
;         { const int p = tid & 127, oc0 = tid >> 7; const float mean = st[p * 2], rstd = st[p * 2 + 1];
; #pragma unroll
;           for (int i = 0; i < 4; ++i) { const int oc = oc0 + 4 * i, c0 = g * 128 + oc * 8;
;               f32x4 x0, x1; unpk8(*(const v4u*)(GUV + (t0 + p) * 2048 + 1024 + c0), x0, x1);
;               const f32x4 g0 = *(const f32x4*)(lng + c0), g1 = *(const f32x4*)(lng + c0 + 4), b0 = *(const f32x4*)(lnb + c0), b1 = *(const f32x4*)(lnb + c0 + 4);
;               x0 = (x0 - mean) * rstd * g0 + b0; x1 = (x1 - mean) * rstd * g1 + b1;
;               const v4u w = pk8(x0, x1);
;               LAS bf16* d = sB + (oc * 8) * TP + p;
;               d[0 * TP] = (bf16)(w.x & 0xffffu); d[1 * TP] = (bf16)(w.x >> 16); d[2 * TP] = (bf16)(w.y & 0xffffu); d[3 * TP] = (bf16)(w.y >> 16);
;               d[4 * TP] = (bf16)(w.z & 0xffffu); d[5 * TP] = (bf16)(w.z >> 16); d[6 * TP] = (bf16)(w.w & 0xffffu); d[7 * TP] = (bf16)(w.w >> 16); } }
;         __syncthreads();
.LBB0_839:
	v_lshl_add_u64 v[2:3], s[6:7], 0, v[34:35]
	global_load_dwordx4 v[100:103], v[2:3], off
	v_lshl_add_u64 v[34:35], v[34:35], 0, s[34:35]
	v_lshl_add_u64 v[2:3], s[6:7], 0, v[36:37]
	global_load_dwordx4 v[104:107], v[2:3], off
	v_lshl_add_u64 v[36:37], v[36:37], 0, s[34:35]
	v_lshl_add_u64 v[2:3], s[6:7], 0, v[42:43]
	global_load_dwordx4 v[108:111], v[2:3], off
	v_lshl_add_u64 v[42:43], v[42:43], 0, s[34:35]
	v_lshl_add_u64 v[2:3], s[6:7], 0, v[46:47]
	global_load_dwordx4 v[112:115], v[2:3], off
	v_lshl_add_u64 v[46:47], v[46:47], 0, s[34:35]
	v_lshl_add_u64 v[4:5], s[6:7], 0, v[44:45]
	v_lshl_add_u64 v[8:9], v[50:51], 0, s[22:23]
	v_lshl_add_u64 v[6:7], v[48:49], 0, s[22:23]
	ds_read_b64 v[2:3], v1
	v_lshl_add_u64 v[44:45], v[44:45], 0, s[66:67]
	global_load_dwordx4 v[116:119], v[4:5], off offset:-128
	global_load_dwordx4 v[132:135], v[8:9], off
	global_load_dwordx4 v[136:139], v[8:9], off offset:16
	global_load_dwordx4 v[164:167], v[6:7], off
	global_load_dwordx4 v[168:171], v[6:7], off offset:16
	global_load_dwordx4 v[120:123], v[4:5], off offset:-64
	global_load_dwordx4 v[140:143], v[8:9], off offset:128
	global_load_dwordx4 v[144:147], v[8:9], off offset:144
	global_load_dwordx4 v[172:175], v[6:7], off offset:128
	global_load_dwordx4 v[176:179], v[6:7], off offset:144
	global_load_dwordx4 v[124:127], v[4:5], off
	global_load_dwordx4 v[148:151], v[8:9], off offset:256
	global_load_dwordx4 v[152:155], v[8:9], off offset:272
	global_load_dwordx4 v[180:183], v[6:7], off offset:256
	global_load_dwordx4 v[184:187], v[6:7], off offset:272
	global_load_dwordx4 v[128:131], v[4:5], off offset:64
	global_load_dwordx4 v[156:159], v[8:9], off offset:384
	global_load_dwordx4 v[160:163], v[8:9], off offset:400
	global_load_dwordx4 v[188:191], v[6:7], off offset:384
	global_load_dwordx4 v[192:195], v[6:7], off offset:400
	v_ashrrev_i32_e32 v41, 31, v40
	v_lshl_add_u64 v[54:55], v[38:39], 0, s[22:23]
	v_lshlrev_b64 v[52:53], 1, v[40:41]
	v_add_u32_e32 v40, 0x80, v40
	v_lshl_add_u64 v[232:233], v[28:29], 0, v[52:53]
	v_lshl_add_u64 v[234:235], v[30:31], 0, v[52:53]
	v_lshl_add_u64 v[236:237], v[32:33], 0, v[52:53]
	v_lshl_add_u64 v[238:239], v[26:27], 0, v[52:53]
	global_load_dword v196, v[54:55], off
	global_load_dwordx2 v[204:205], v[232:233], off
	global_load_dwordx2 v[206:207], v[232:233], off offset:32
	global_load_dword v198, v[54:55], off offset:64
	global_load_dwordx2 v[224:225], v[234:235], off
	global_load_dwordx2 v[226:227], v[234:235], off offset:32
	global_load_dword v200, v[54:55], off offset:128
	global_load_dwordx2 v[228:229], v[236:237], off
	global_load_dwordx2 v[230:231], v[236:237], off offset:32
	global_load_dword v202, v[54:55], off offset:192
	global_load_dwordx2 v[246:247], v[238:239], off
	global_load_dwordx2 v[248:249], v[238:239], off offset:32
	s_waitcnt vmcnt(35)
	ds_write_b128 v56, v[100:103] offset:1024
	s_waitcnt vmcnt(34)
	ds_write_b128 v57, v[104:107] offset:1024
	s_waitcnt vmcnt(33)
	ds_write_b128 v58, v[108:111] offset:1024
	s_waitcnt vmcnt(32)
	ds_write_b128 v59, v[112:115] offset:1024
	s_waitcnt lgkmcnt(4)
	s_waitcnt vmcnt(27)
	v_lshlrev_b32_e32 v41, 16, v116
	v_and_b32_e32 v54, 0xffff0000, v116
	v_lshlrev_b32_e32 v52, 16, v117
	v_and_b32_e32 v53, 0xffff0000, v117
	v_lshlrev_b32_e32 v63, 16, v118
	v_and_b32_e32 v64, 0xffff0000, v118
	v_lshlrev_b32_e32 v65, 16, v119
	v_and_b32_e32 v66, 0xffff0000, v119
	v_sub_f32_e32 v53, v53, v2
	v_sub_f32_e32 v52, v52, v2
	v_sub_f32_e32 v55, v54, v2
	v_sub_f32_e32 v54, v41, v2
	v_pk_mul_f32 v[52:53], v[2:3], v[52:53] op_sel:[1,0]
	v_pk_mul_f32 v[54:55], v[2:3], v[54:55] op_sel:[1,0]
	v_pk_fma_f32 v[134:135], v[134:135], v[52:53], v[166:167]
	v_sub_f32_e32 v167, v64, v2
	v_sub_f32_e32 v166, v63, v2
	v_pk_fma_f32 v[132:133], v[132:133], v[54:55], v[164:165]
	v_sub_f32_e32 v165, v66, v2
	v_sub_f32_e32 v164, v65, v2
	v_pk_mul_f32 v[166:167], v[2:3], v[166:167] op_sel:[1,0]
	v_pk_mul_f32 v[164:165], v[2:3], v[164:165] op_sel:[1,0]
	v_pk_fma_f32 v[136:137], v[136:137], v[166:167], v[168:169]
	v_cvt_pk_bf16_f32 v132, v132, v133
	v_pk_fma_f32 v[138:139], v[138:139], v[164:165], v[170:171]
	v_cvt_pk_bf16_f32 v133, v134, v135
	v_cvt_pk_bf16_f32 v136, v136, v137
	s_nop 0
	v_cvt_pk_bf16_f32 v137, v138, v139
	ds_write_b16 v60, v132 offset:35840
	ds_write_b16_d16_hi v60, v132 offset:36112
	ds_write_b16 v60, v133 offset:36384
	ds_write_b16_d16_hi v60, v133 offset:36656
	ds_write_b16 v60, v136 offset:36928
	ds_write_b16_d16_hi v60, v136 offset:37200
	ds_write_b16 v60, v137 offset:37472
	ds_write_b16_d16_hi v60, v137 offset:37744
	s_waitcnt vmcnt(22)
	v_lshlrev_b32_e32 v41, 16, v120
	v_and_b32_e32 v54, 0xffff0000, v120
	v_lshlrev_b32_e32 v52, 16, v121
	v_and_b32_e32 v53, 0xffff0000, v121
	v_lshlrev_b32_e32 v63, 16, v122
	v_and_b32_e32 v64, 0xffff0000, v122
	v_lshlrev_b32_e32 v65, 16, v123
	v_and_b32_e32 v66, 0xffff0000, v123
	v_sub_f32_e32 v53, v53, v2
	v_sub_f32_e32 v52, v52, v2
	v_sub_f32_e32 v55, v54, v2
	v_sub_f32_e32 v54, v41, v2
	v_pk_mul_f32 v[52:53], v[2:3], v[52:53] op_sel:[1,0]
	v_pk_mul_f32 v[54:55], v[2:3], v[54:55] op_sel:[1,0]
	v_pk_fma_f32 v[142:143], v[142:143], v[52:53], v[174:175]
	v_sub_f32_e32 v175, v64, v2
	v_sub_f32_e32 v174, v63, v2
	v_pk_fma_f32 v[140:141], v[140:141], v[54:55], v[172:173]
	v_sub_f32_e32 v173, v66, v2
	v_sub_f32_e32 v172, v65, v2
	v_pk_mul_f32 v[174:175], v[2:3], v[174:175] op_sel:[1,0]
	v_pk_mul_f32 v[172:173], v[2:3], v[172:173] op_sel:[1,0]
	v_pk_fma_f32 v[144:145], v[144:145], v[174:175], v[176:177]
	v_cvt_pk_bf16_f32 v140, v140, v141
	v_pk_fma_f32 v[146:147], v[146:147], v[172:173], v[178:179]
	v_cvt_pk_bf16_f32 v141, v142, v143
	v_cvt_pk_bf16_f32 v144, v144, v145
	s_nop 0
	v_cvt_pk_bf16_f32 v145, v146, v147
	ds_write_b16 v60, v140 offset:44544
	ds_write_b16_d16_hi v60, v140 offset:44816
	ds_write_b16 v60, v141 offset:45088
	ds_write_b16_d16_hi v60, v141 offset:45360
	ds_write_b16 v60, v144 offset:45632
	ds_write_b16_d16_hi v60, v144 offset:45904
	ds_write_b16 v60, v145 offset:46176
	ds_write_b16_d16_hi v60, v145 offset:46448
	s_waitcnt vmcnt(17)
; __device__ __forceinline__ void unpk8(const u32x4 w, f32x4& a, f32x4& b) { a = (f32x4){bflo(w.x), bfhi(w.x), bflo(w.y), bfhi(w.y)}; b = (f32x4){bflo(w.z), bfhi(w.z), bflo(w.w), bfhi(w.w)}; }
; __device__ __forceinline__ u32x4 pk8(const f32x4 a, const f32x4 b) { u32x4 w; w.x = cvt_pk_bf16(a[0], a[1]); w.y = cvt_pk_bf16(a[2], a[3]); w.z = cvt_pk_bf16(b[0], b[1]); w.w = cvt_pk_bf16(b[2], b[3]); return w; }
; #define LAS __attribute__((address_space(3)))
; __device__ __forceinline__ void mma_128(const LAS bf16* sA, const LAS bf16* sBt, int wave, int lane, f32x4 (&acc)[4][2]) {
;     const int wm = wave >> 2, wn = wave & 3, fr = lane & 15, fq = lane >> 4;
; #pragma unroll
;     for (int kk = 0; kk < 4; ++kk) {
;         bf16x8 af[4], bf_[2];
; #pragma unroll
;         for (int mt = 0; mt < 4; ++mt) af[mt] = *(const LAS bf16x8*)(sA + (64 * wm + 16 * mt + fr) * TP + 32 * kk + 8 * fq);
; #pragma unroll
;         for (int nt = 0; nt < 2; ++nt) bf_[nt] = *(const LAS bf16x8*)(sBt + (32 * wn + 16 * nt + fr) * TP + 32 * kk + 8 * fq);
; #pragma unroll
;         for (int mt = 0; mt < 4; ++mt)
; #pragma unroll
;             for (int nt = 0; nt < 2; ++nt) acc[mt][nt] = __builtin_amdgcn_mfma_f32_16x16x32_bf16(bf_[nt], af[mt], acc[mt][nt], 0, 0, 0);
;     }
; }
; __device__ __forceinline__ void gmlp_unit(Frame& F, const Args& a, int layer, int unit) {
;     ...
;         { const int p = tid & 127, oc0 = tid >> 7; const float mean = st[p * 2], rstd = st[p * 2 + 1];
; #pragma unroll
;           for (int i = 0; i < 4; ++i) { const int oc = oc0 + 4 * i, c0 = g * 128 + oc * 8;
;               f32x4 x0, x1; unpk8(*(const v4u*)(GUV + (t0 + p) * 2048 + 1024 + c0), x0, x1);
;               const f32x4 g0 = *(const f32x4*)(lng + c0), g1 = *(const f32x4*)(lng + c0 + 4), b0 = *(const f32x4*)(lnb + c0), b1 = *(const f32x4*)(lnb + c0 + 4);
;               x0 = (x0 - mean) * rstd * g0 + b0; x1 = (x1 - mean) * rstd * g1 + b1;
;               const v4u w = pk8(x0, x1);
;               LAS bf16* d = sB + (oc * 8) * TP + p;
;               d[0 * TP] = (bf16)(w.x & 0xffffu); d[1 * TP] = (bf16)(w.x >> 16); d[2 * TP] = (bf16)(w.y & 0xffffu); d[3 * TP] = (bf16)(w.y >> 16);
;               d[4 * TP] = (bf16)(w.z & 0xffffu); d[5 * TP] = (bf16)(w.z >> 16); d[6 * TP] = (bf16)(w.w & 0xffffu); d[7 * TP] = (bf16)(w.w >> 16); } }
;         __syncthreads();
	v_lshlrev_b32_e32 v41, 16, v124
	v_and_b32_e32 v54, 0xffff0000, v124
	v_lshlrev_b32_e32 v52, 16, v125
	v_and_b32_e32 v53, 0xffff0000, v125
	v_lshlrev_b32_e32 v63, 16, v126
	v_and_b32_e32 v64, 0xffff0000, v126
	v_lshlrev_b32_e32 v65, 16, v127
	v_and_b32_e32 v66, 0xffff0000, v127
	v_sub_f32_e32 v53, v53, v2
	v_sub_f32_e32 v52, v52, v2
	v_sub_f32_e32 v55, v54, v2
	v_sub_f32_e32 v54, v41, v2
	v_pk_mul_f32 v[52:53], v[2:3], v[52:53] op_sel:[1,0]
	v_pk_mul_f32 v[54:55], v[2:3], v[54:55] op_sel:[1,0]
	v_pk_fma_f32 v[150:151], v[150:151], v[52:53], v[182:183]
	v_sub_f32_e32 v183, v64, v2
	v_sub_f32_e32 v182, v63, v2
	v_pk_fma_f32 v[148:149], v[148:149], v[54:55], v[180:181]
	v_sub_f32_e32 v181, v66, v2
	v_sub_f32_e32 v180, v65, v2
	v_pk_mul_f32 v[182:183], v[2:3], v[182:183] op_sel:[1,0]
	v_pk_mul_f32 v[180:181], v[2:3], v[180:181] op_sel:[1,0]
	v_pk_fma_f32 v[152:153], v[152:153], v[182:183], v[184:185]
	v_cvt_pk_bf16_f32 v148, v148, v149
	v_pk_fma_f32 v[154:155], v[154:155], v[180:181], v[186:187]
	v_cvt_pk_bf16_f32 v149, v150, v151
	v_cvt_pk_bf16_f32 v152, v152, v153
	s_nop 0
	v_cvt_pk_bf16_f32 v153, v154, v155
	ds_write_b16 v60, v148 offset:53248
	ds_write_b16_d16_hi v60, v148 offset:53520
	ds_write_b16 v60, v149 offset:53792
	ds_write_b16_d16_hi v60, v149 offset:54064
	ds_write_b16 v60, v152 offset:54336
	ds_write_b16_d16_hi v60, v152 offset:54608
	ds_write_b16 v60, v153 offset:54880
	ds_write_b16_d16_hi v60, v153 offset:55152
	s_waitcnt vmcnt(12)
	v_lshlrev_b32_e32 v41, 16, v128
	v_and_b32_e32 v54, 0xffff0000, v128
	v_lshlrev_b32_e32 v52, 16, v129
	v_and_b32_e32 v53, 0xffff0000, v129
	v_lshlrev_b32_e32 v63, 16, v130
	v_and_b32_e32 v64, 0xffff0000, v130
	v_lshlrev_b32_e32 v65, 16, v131
	v_and_b32_e32 v66, 0xffff0000, v131
	v_sub_f32_e32 v53, v53, v2
	v_sub_f32_e32 v52, v52, v2
	v_sub_f32_e32 v55, v54, v2
	v_sub_f32_e32 v54, v41, v2
	v_pk_mul_f32 v[52:53], v[2:3], v[52:53] op_sel:[1,0]
	v_pk_mul_f32 v[54:55], v[2:3], v[54:55] op_sel:[1,0]
	v_pk_fma_f32 v[158:159], v[158:159], v[52:53], v[190:191]
	v_sub_f32_e32 v191, v64, v2
	v_sub_f32_e32 v190, v63, v2
	v_pk_fma_f32 v[156:157], v[156:157], v[54:55], v[188:189]
	v_sub_f32_e32 v189, v66, v2
	v_sub_f32_e32 v188, v65, v2
	v_pk_mul_f32 v[190:191], v[2:3], v[190:191] op_sel:[1,0]
	v_pk_mul_f32 v[188:189], v[2:3], v[188:189] op_sel:[1,0]
	v_pk_fma_f32 v[160:161], v[160:161], v[190:191], v[192:193]
	v_cvt_pk_bf16_f32 v156, v156, v157
	v_pk_fma_f32 v[162:163], v[162:163], v[188:189], v[194:195]
	v_cvt_pk_bf16_f32 v157, v158, v159
	v_cvt_pk_bf16_f32 v160, v160, v161
	s_nop 0
	v_cvt_pk_bf16_f32 v161, v162, v163
	ds_write_b16 v60, v156 offset:61952
	ds_write_b16_d16_hi v60, v156 offset:62224
	ds_write_b16 v60, v157 offset:62496
	ds_write_b16_d16_hi v60, v157 offset:62768
	ds_write_b16 v60, v160 offset:63040
	ds_write_b16_d16_hi v60, v160 offset:63312
	ds_write_b16 v60, v161 offset:63584
	ds_write_b16_d16_hi v60, v161 offset:63856
	s_waitcnt lgkmcnt(0)
	s_barrier
	ds_read_b128 v[2:5], v61 offset:1024
	ds_read_b128 v[6:9], v61 offset:5376
	ds_read_b128 v[10:13], v61 offset:9728
	ds_read_b128 v[14:17], v61 offset:14080
	ds_read_b128 v[18:21], v62 offset:35840
	ds_read_b128 v[22:25], v62 offset:40192
	ds_read_b128 v[84:87], v61 offset:1088
	ds_read_b128 v[88:91], v61 offset:5440
	ds_read_b128 v[92:95], v61 offset:9792
	ds_read_b128 v[96:99], v61 offset:14144
	ds_read_b128 v[76:79], v62 offset:35904
	ds_read_b128 v[80:83], v62 offset:40256
	s_waitcnt lgkmcnt(6)
	v_mfma_f32_16x16x32_bf16 v[100:103], v[18:21], v[2:5], 0
	v_mfma_f32_16x16x32_bf16 v[104:107], v[22:25], v[2:5], 0
	v_mfma_f32_16x16x32_bf16 v[108:111], v[18:21], v[6:9], 0
	v_mfma_f32_16x16x32_bf16 v[112:115], v[22:25], v[6:9], 0
	v_mfma_f32_16x16x32_bf16 v[116:119], v[18:21], v[10:13], 0
	v_mfma_f32_16x16x32_bf16 v[120:123], v[22:25], v[10:13], 0
	v_mfma_f32_16x16x32_bf16 v[124:127], v[18:21], v[14:17], 0
	v_mfma_f32_16x16x32_bf16 v[128:131], v[22:25], v[14:17], 0
	ds_read_b128 v[2:5], v61 offset:1152
	ds_read_b128 v[6:9], v61 offset:5504
	ds_read_b128 v[10:13], v61 offset:9856
	ds_read_b128 v[14:17], v61 offset:14208
	ds_read_b128 v[18:21], v62 offset:35968
	ds_read_b128 v[22:25], v62 offset:40320
	s_waitcnt lgkmcnt(6)
	v_mfma_f32_16x16x32_bf16 v[100:103], v[76:79], v[84:87], v[100:103]
	v_mfma_f32_16x16x32_bf16 v[104:107], v[80:83], v[84:87], v[104:107]
	v_mfma_f32_16x16x32_bf16 v[108:111], v[76:79], v[88:91], v[108:111]
	v_mfma_f32_16x16x32_bf16 v[112:115], v[80:83], v[88:91], v[112:115]
	v_mfma_f32_16x16x32_bf16 v[116:119], v[76:79], v[92:95], v[116:119]
	v_mfma_f32_16x16x32_bf16 v[120:123], v[80:83], v[92:95], v[120:123]
	v_mfma_f32_16x16x32_bf16 v[124:127], v[76:79], v[96:99], v[124:127]
	v_mfma_f32_16x16x32_bf16 v[128:131], v[80:83], v[96:99], v[128:131]
	ds_read_b128 v[84:87], v61 offset:1216
	ds_read_b128 v[88:91], v61 offset:5568
	ds_read_b128 v[92:95], v61 offset:9920
	ds_read_b128 v[96:99], v61 offset:14272
	ds_read_b128 v[76:79], v62 offset:36032
	ds_read_b128 v[80:83], v62 offset:40384
	s_waitcnt lgkmcnt(6)
; __device__ __forceinline__ unsigned cvt_pk_bf16(float lo, float hi) { unsigned r; asm volatile("v_cvt_pk_bf16_f32 %0, %1, %2" : "=v"(r) : "v"(lo), "v"(hi)); return r; }
; #define LAS __attribute__((address_space(3)))
; __device__ __forceinline__ void mma_128(const LAS bf16* sA, const LAS bf16* sBt, int wave, int lane, f32x4 (&acc)[4][2]) {
;     ...
;         for (int mt = 0; mt < 4; ++mt) af[mt] = *(const LAS bf16x8*)(sA + (64 * wm + 16 * mt + fr) * TP + 32 * kk + 8 * fq);
; #pragma unroll
;         for (int nt = 0; nt < 2; ++nt) bf_[nt] = *(const LAS bf16x8*)(sBt + (32 * wn + 16 * nt + fr) * TP + 32 * kk + 8 * fq);
; #pragma unroll
;         for (int mt = 0; mt < 4; ++mt)
; #pragma unroll
;             for (int nt = 0; nt < 2; ++nt) acc[mt][nt] = __builtin_amdgcn_mfma_f32_16x16x32_bf16(bf_[nt], af[mt], acc[mt][nt], 0, 0, 0);
;     }
; }
; __device__ __forceinline__ void gmlp_unit(Frame& F, const Args& a, int layer, int unit) {
;     ...
;         { const int wm = wave >> 2, wn = wave & 3, fr = lane & 15, fq = lane >> 4;
; #pragma unroll
;           for (int mt = 0; mt < 4; ++mt) { const int tt = 64 * wm + 16 * mt + fr; const float bsv = bsp[g * 128 + tt];
; #pragma unroll
;               for (int nt = 0; nt < 2; ++nt) { const int c = g * 128 + 32 * wn + 16 * nt + 4 * fq;
;                   const v2u uw = *(const v2u*)(GUV + (t0 + tt) * 2048 + c);
;                   const f32x4 u4 = (f32x4){bflo(uw.x), bfhi(uw.x), bflo(uw.y), bfhi(uw.y)};
;                   const f32x4 yb = u4 * (acc[mt][nt] + bsv);
;                   v2u ow; ow.x = cvt_pk_bf16(yb.x, yb.y); ow.y = cvt_pk_bf16(yb.z, yb.w);
;                   *(v2u*)(GUV + (t0 + tt) * 2048 + c) = ow; } } }
;         __syncthreads();
	v_mfma_f32_16x16x32_bf16 v[100:103], v[18:21], v[2:5], v[100:103]
	v_mfma_f32_16x16x32_bf16 v[104:107], v[22:25], v[2:5], v[104:107]
	v_mfma_f32_16x16x32_bf16 v[108:111], v[18:21], v[6:9], v[108:111]
	v_mfma_f32_16x16x32_bf16 v[112:115], v[22:25], v[6:9], v[112:115]
	v_mfma_f32_16x16x32_bf16 v[116:119], v[18:21], v[10:13], v[116:119]
	v_mfma_f32_16x16x32_bf16 v[120:123], v[22:25], v[10:13], v[120:123]
	v_mfma_f32_16x16x32_bf16 v[124:127], v[18:21], v[14:17], v[124:127]
	v_mfma_f32_16x16x32_bf16 v[128:131], v[22:25], v[14:17], v[128:131]
	s_waitcnt lgkmcnt(0)
	v_mfma_f32_16x16x32_bf16 v[100:103], v[76:79], v[84:87], v[100:103]
	v_mfma_f32_16x16x32_bf16 v[104:107], v[80:83], v[84:87], v[104:107]
	v_mfma_f32_16x16x32_bf16 v[108:111], v[76:79], v[88:91], v[108:111]
	v_mfma_f32_16x16x32_bf16 v[112:115], v[80:83], v[88:91], v[112:115]
	v_mfma_f32_16x16x32_bf16 v[116:119], v[76:79], v[92:95], v[116:119]
	v_mfma_f32_16x16x32_bf16 v[120:123], v[80:83], v[92:95], v[120:123]
	v_mfma_f32_16x16x32_bf16 v[124:127], v[76:79], v[96:99], v[124:127]
	v_mfma_f32_16x16x32_bf16 v[128:131], v[80:83], v[96:99], v[128:131]
	s_nop 7
	s_nop 1
	s_waitcnt vmcnt(9)
	v_lshlrev_b32_e32 v70, 16, v204
	v_and_b32_e32 v71, 0xffff0000, v204
	v_lshlrev_b32_e32 v68, 16, v205
	v_and_b32_e32 v69, 0xffff0000, v205
	v_pk_add_f32 v[72:73], v[102:103], v[196:197] op_sel_hi:[1,0]
	v_pk_add_f32 v[74:75], v[100:101], v[196:197] op_sel_hi:[1,0]
	v_pk_mul_f32 v[68:69], v[72:73], v[68:69]
	v_pk_mul_f32 v[70:71], v[74:75], v[70:71]
	v_cvt_pk_bf16_f32 v70, v70, v71
	v_cvt_pk_bf16_f32 v71, v68, v69
	global_store_dwordx2 v[232:233], v[70:71], off
	v_lshlrev_b32_e32 v16, 16, v206
	v_and_b32_e32 v17, 0xffff0000, v206
	v_lshlrev_b32_e32 v18, 16, v207
	v_and_b32_e32 v19, 0xffff0000, v207
	v_pk_add_f32 v[20:21], v[104:105], v[196:197] op_sel_hi:[1,0]
	v_pk_add_f32 v[22:23], v[106:107], v[196:197] op_sel_hi:[1,0]
	v_pk_mul_f32 v[20:21], v[20:21], v[16:17]
	v_pk_mul_f32 v[22:23], v[22:23], v[18:19]
	v_cvt_pk_bf16_f32 v20, v20, v21
	s_nop 0
	v_cvt_pk_bf16_f32 v21, v22, v23
	global_store_dwordx2 v[232:233], v[20:21], off offset:32
	s_waitcnt vmcnt(8)
	v_lshlrev_b32_e32 v70, 16, v224
	v_and_b32_e32 v71, 0xffff0000, v224
	v_lshlrev_b32_e32 v68, 16, v225
	v_and_b32_e32 v69, 0xffff0000, v225
	v_pk_add_f32 v[72:73], v[110:111], v[198:199] op_sel_hi:[1,0]
	v_pk_add_f32 v[74:75], v[108:109], v[198:199] op_sel_hi:[1,0]
	v_pk_mul_f32 v[68:69], v[72:73], v[68:69]
	v_pk_mul_f32 v[70:71], v[74:75], v[70:71]
	v_cvt_pk_bf16_f32 v70, v70, v71
	v_cvt_pk_bf16_f32 v71, v68, v69
	global_store_dwordx2 v[234:235], v[70:71], off
	v_lshlrev_b32_e32 v16, 16, v226
	v_and_b32_e32 v17, 0xffff0000, v226
	v_lshlrev_b32_e32 v18, 16, v227
	v_and_b32_e32 v19, 0xffff0000, v227
	v_pk_add_f32 v[20:21], v[112:113], v[198:199] op_sel_hi:[1,0]
	v_pk_add_f32 v[22:23], v[114:115], v[198:199] op_sel_hi:[1,0]
	v_pk_mul_f32 v[20:21], v[20:21], v[16:17]
	v_pk_mul_f32 v[22:23], v[22:23], v[18:19]
	v_cvt_pk_bf16_f32 v20, v20, v21
	s_nop 0
	v_cvt_pk_bf16_f32 v21, v22, v23
	global_store_dwordx2 v[234:235], v[20:21], off offset:32
	s_waitcnt vmcnt(7)
	v_lshlrev_b32_e32 v70, 16, v228
	v_and_b32_e32 v71, 0xffff0000, v228
	v_lshlrev_b32_e32 v68, 16, v229
	v_and_b32_e32 v69, 0xffff0000, v229
	v_pk_add_f32 v[72:73], v[118:119], v[200:201] op_sel_hi:[1,0]
	v_pk_add_f32 v[74:75], v[116:117], v[200:201] op_sel_hi:[1,0]
	v_pk_mul_f32 v[68:69], v[72:73], v[68:69]
	v_pk_mul_f32 v[70:71], v[74:75], v[70:71]
	v_cvt_pk_bf16_f32 v70, v70, v71
	v_cvt_pk_bf16_f32 v71, v68, v69
	global_store_dwordx2 v[236:237], v[70:71], off
	v_lshlrev_b32_e32 v16, 16, v230
	v_and_b32_e32 v17, 0xffff0000, v230
	v_lshlrev_b32_e32 v18, 16, v231
	v_and_b32_e32 v19, 0xffff0000, v231
	v_pk_add_f32 v[20:21], v[120:121], v[200:201] op_sel_hi:[1,0]
	v_pk_add_f32 v[22:23], v[122:123], v[200:201] op_sel_hi:[1,0]
	v_pk_mul_f32 v[20:21], v[20:21], v[16:17]
	v_pk_mul_f32 v[22:23], v[22:23], v[18:19]
	v_cvt_pk_bf16_f32 v20, v20, v21
	s_nop 0
	v_cvt_pk_bf16_f32 v21, v22, v23
	global_store_dwordx2 v[236:237], v[20:21], off offset:32
	s_waitcnt vmcnt(6)
	v_lshlrev_b32_e32 v70, 16, v246
	v_and_b32_e32 v71, 0xffff0000, v246
	v_lshlrev_b32_e32 v68, 16, v247
	v_and_b32_e32 v69, 0xffff0000, v247
	v_pk_add_f32 v[72:73], v[126:127], v[202:203] op_sel_hi:[1,0]
	v_pk_add_f32 v[74:75], v[124:125], v[202:203] op_sel_hi:[1,0]
	v_pk_mul_f32 v[68:69], v[72:73], v[68:69]
	v_pk_mul_f32 v[70:71], v[74:75], v[70:71]
	v_cvt_pk_bf16_f32 v70, v70, v71
	v_cvt_pk_bf16_f32 v71, v68, v69
	global_store_dwordx2 v[238:239], v[70:71], off
	v_lshlrev_b32_e32 v16, 16, v248
	v_and_b32_e32 v17, 0xffff0000, v248
	v_lshlrev_b32_e32 v18, 16, v249
	v_and_b32_e32 v19, 0xffff0000, v249
	v_pk_add_f32 v[20:21], v[128:129], v[202:203] op_sel_hi:[1,0]
	v_pk_add_f32 v[22:23], v[130:131], v[202:203] op_sel_hi:[1,0]
	v_pk_mul_f32 v[20:21], v[20:21], v[16:17]
	v_pk_mul_f32 v[22:23], v[22:23], v[18:19]
	v_cvt_pk_bf16_f32 v20, v20, v21
	s_nop 0
	v_cvt_pk_bf16_f32 v21, v22, v23
	global_store_dwordx2 v[238:239], v[20:21], off offset:32
	s_add_u32 s22, s22, 0x200
	s_addc_u32 s23, s23, 0
	s_cmpk_lg_i32 s22, 0x1000
	s_barrier
	s_cbranch_scc1 .LBB0_839
	v_readlane_b32 s3, v254, 8
	s_add_i32 s5, s5, s3
	v_readlane_b32 s3, v254, 21
	s_add_i32 s20, s20, s3
	s_add_i32 s2, s2, s3
	s_cmpk_gt_i32 s5, 0x7f
	s_cbranch_scc0 .LBB0_828
